# waitcnt cleanup: 113 s_waitcnt lgkmcnt(0) in GEMM K-loops that directly repeat an already executed one removed (per-phase setprio flips kept); on top of v61
# baseline (speedup 1.0000x reference)
.LBB0_451:
	ds_read_b128 v[146:149], v141
	ds_read_b128 v[150:153], v141 offset:1024
	ds_read_b128 v[154:157], v141 offset:2048
	ds_read_b128 v[158:161], v141 offset:3072
	s_add_i32 s48, s45, 0x80
	s_cmp_eq_u32 s28, s47
	s_cselect_b32 s50, s14, s48
	s_cselect_b32 s48, s15, s46
	s_or_b32 s49, s50, 0x80
	s_mov_b32 m0, s29
	v_add_u32_e32 v194, s45, v137
	ds_read_b128 v[162:165], v142
	ds_read_b128 v[166:169], v142 offset:1024
	ds_read_b128 v[170:173], v142 offset:2048
	ds_read_b128 v[174:177], v142 offset:3072
	ds_read_b128 v[178:181], v142 offset:4096
	ds_read_b128 v[182:185], v142 offset:5120
	ds_read_b128 v[186:189], v142 offset:6144
	ds_read_b128 v[190:193], v142 offset:7168
	global_load_lds_dwordx4 v194, s[4:5]
	v_add_u32_e32 v194, s45, v138
	s_mov_b32 m0, s30
	s_nop 0
	global_load_lds_dwordx4 v194, s[4:5]
	s_waitcnt lgkmcnt(8)
	s_barrier
	s_waitcnt lgkmcnt(0)
	s_setprio 1

	v_mfma_f32_16x16x32_bf16 v[122:125], v[146:149], v[162:165], v[122:125]
	v_mfma_f32_16x16x32_bf16 v[126:129], v[154:157], v[162:165], v[126:129]
	v_mfma_f32_16x16x32_bf16 v[110:113], v[146:149], v[170:173], v[110:113]
	v_mfma_f32_16x16x32_bf16 v[106:109], v[154:157], v[170:173], v[106:109]
	v_mfma_f32_16x16x32_bf16 v[94:97], v[146:149], v[178:181], v[94:97]
	v_mfma_f32_16x16x32_bf16 v[90:93], v[154:157], v[178:181], v[90:93]
	v_mfma_f32_16x16x32_bf16 v[78:81], v[146:149], v[186:189], v[78:81]
	v_mfma_f32_16x16x32_bf16 v[74:77], v[154:157], v[186:189], v[74:77]
	v_mfma_f32_16x16x32_bf16 v[122:125], v[150:153], v[166:169], v[122:125]
	v_mfma_f32_16x16x32_bf16 v[126:129], v[158:161], v[166:169], v[126:129]
	v_mfma_f32_16x16x32_bf16 v[110:113], v[150:153], v[174:177], v[110:113]
	v_mfma_f32_16x16x32_bf16 v[106:109], v[158:161], v[174:177], v[106:109]
	v_mfma_f32_16x16x32_bf16 v[94:97], v[150:153], v[182:185], v[94:97]
	v_mfma_f32_16x16x32_bf16 v[90:93], v[158:161], v[182:185], v[90:93]
	v_mfma_f32_16x16x32_bf16 v[78:81], v[150:153], v[190:193], v[78:81]
	v_mfma_f32_16x16x32_bf16 v[74:77], v[158:161], v[190:193], v[74:77]
	s_setprio 0
	s_barrier
	s_mov_b32 m0, s33
	v_add_u32_e32 v210, s48, v1
	ds_read_b128 v[194:197], v143
	ds_read_b128 v[198:201], v143 offset:1024
	ds_read_b128 v[202:205], v143 offset:2048
	ds_read_b128 v[206:209], v143 offset:3072
	global_load_lds_dwordx4 v210, s[6:7]
	v_add_u32_e32 v210, s48, v134
	s_mov_b32 m0, s34
	s_nop 0
	global_load_lds_dwordx4 v210, s[6:7]
	s_barrier
	s_waitcnt lgkmcnt(0)
	s_setprio 1

	v_mfma_f32_16x16x32_bf16 v[118:121], v[194:197], v[162:165], v[118:121]
	v_mfma_f32_16x16x32_bf16 v[114:117], v[202:205], v[162:165], v[114:117]
	v_mfma_f32_16x16x32_bf16 v[102:105], v[194:197], v[170:173], v[102:105]
	v_mfma_f32_16x16x32_bf16 v[98:101], v[202:205], v[170:173], v[98:101]
	v_mfma_f32_16x16x32_bf16 v[86:89], v[194:197], v[178:181], v[86:89]
	v_mfma_f32_16x16x32_bf16 v[82:85], v[202:205], v[178:181], v[82:85]
	v_mfma_f32_16x16x32_bf16 v[70:73], v[194:197], v[186:189], v[70:73]
	v_mfma_f32_16x16x32_bf16 v[66:69], v[202:205], v[186:189], v[66:69]
	v_mfma_f32_16x16x32_bf16 v[118:121], v[198:201], v[166:169], v[118:121]
	v_mfma_f32_16x16x32_bf16 v[114:117], v[206:209], v[166:169], v[114:117]
	v_mfma_f32_16x16x32_bf16 v[102:105], v[198:201], v[174:177], v[102:105]
	v_mfma_f32_16x16x32_bf16 v[98:101], v[206:209], v[174:177], v[98:101]
	v_mfma_f32_16x16x32_bf16 v[86:89], v[198:201], v[182:185], v[86:89]
	v_mfma_f32_16x16x32_bf16 v[82:85], v[206:209], v[182:185], v[82:85]
	v_mfma_f32_16x16x32_bf16 v[70:73], v[198:201], v[190:193], v[70:73]
	v_mfma_f32_16x16x32_bf16 v[66:69], v[206:209], v[190:193], v[66:69]
	s_setprio 0
	s_mov_b32 m0, s19
	v_add_u32_e32 v210, s50, v135
	s_barrier
	ds_read_b128 v[162:165], v142 offset:16384
	ds_read_b128 v[166:169], v142 offset:17408
	ds_read_b128 v[170:173], v142 offset:18432
	ds_read_b128 v[174:177], v142 offset:19456
	ds_read_b128 v[178:181], v142 offset:20480
	ds_read_b128 v[182:185], v142 offset:21504
	ds_read_b128 v[186:189], v142 offset:22528
	ds_read_b128 v[190:193], v142 offset:23552
	global_load_lds_dwordx4 v210, s[4:5]
	v_add_u32_e32 v210, s50, v136
	s_mov_b32 m0, s20
	s_nop 0
	global_load_lds_dwordx4 v210, s[4:5]
	s_barrier
	s_waitcnt lgkmcnt(0)
	s_setprio 1

	v_mfma_f32_16x16x32_bf16 v[62:65], v[146:149], v[162:165], v[62:65]
	v_mfma_f32_16x16x32_bf16 v[58:61], v[154:157], v[162:165], v[58:61]
	v_mfma_f32_16x16x32_bf16 v[46:49], v[146:149], v[170:173], v[46:49]
	v_mfma_f32_16x16x32_bf16 v[42:45], v[154:157], v[170:173], v[42:45]
	v_mfma_f32_16x16x32_bf16 v[30:33], v[146:149], v[178:181], v[30:33]
	v_mfma_f32_16x16x32_bf16 v[26:29], v[154:157], v[178:181], v[26:29]
	v_mfma_f32_16x16x32_bf16 v[14:17], v[146:149], v[186:189], v[14:17]
	v_mfma_f32_16x16x32_bf16 v[10:13], v[154:157], v[186:189], v[10:13]
	v_mfma_f32_16x16x32_bf16 v[62:65], v[150:153], v[166:169], v[62:65]
	v_mfma_f32_16x16x32_bf16 v[58:61], v[158:161], v[166:169], v[58:61]
	v_mfma_f32_16x16x32_bf16 v[46:49], v[150:153], v[174:177], v[46:49]
	v_mfma_f32_16x16x32_bf16 v[42:45], v[158:161], v[174:177], v[42:45]
	v_mfma_f32_16x16x32_bf16 v[30:33], v[150:153], v[182:185], v[30:33]
	v_mfma_f32_16x16x32_bf16 v[26:29], v[158:161], v[182:185], v[26:29]
	v_mfma_f32_16x16x32_bf16 v[14:17], v[150:153], v[190:193], v[14:17]
	v_mfma_f32_16x16x32_bf16 v[10:13], v[158:161], v[190:193], v[10:13]
	s_setprio 0
	s_barrier
	s_add_i32 s51, s48, 0x80000
	s_mov_b32 m0, s35
	v_add_u32_e32 v146, s51, v1
	global_load_lds_dwordx4 v146, s[6:7]
	v_add_u32_e32 v146, s51, v134
	s_mov_b32 m0, s36
	s_nop 0
	global_load_lds_dwordx4 v146, s[6:7]
	s_waitcnt vmcnt(6)
	s_barrier
	s_setprio 1
	v_mfma_f32_16x16x32_bf16 v[54:57], v[194:197], v[162:165], v[54:57]
	v_mfma_f32_16x16x32_bf16 v[50:53], v[202:205], v[162:165], v[50:53]
	v_mfma_f32_16x16x32_bf16 v[38:41], v[194:197], v[170:173], v[38:41]
	v_mfma_f32_16x16x32_bf16 v[34:37], v[202:205], v[170:173], v[34:37]
	v_mfma_f32_16x16x32_bf16 v[22:25], v[194:197], v[178:181], v[22:25]
	v_mfma_f32_16x16x32_bf16 v[18:21], v[202:205], v[178:181], v[18:21]
	v_mfma_f32_16x16x32_bf16 v[6:9], v[194:197], v[186:189], v[6:9]
	v_mfma_f32_16x16x32_bf16 v[2:5], v[202:205], v[186:189], v[2:5]
	v_mfma_f32_16x16x32_bf16 v[54:57], v[198:201], v[166:169], v[54:57]
	v_mfma_f32_16x16x32_bf16 v[50:53], v[206:209], v[166:169], v[50:53]
	v_mfma_f32_16x16x32_bf16 v[38:41], v[198:201], v[174:177], v[38:41]
	v_mfma_f32_16x16x32_bf16 v[34:37], v[206:209], v[174:177], v[34:37]
	v_mfma_f32_16x16x32_bf16 v[22:25], v[198:201], v[182:185], v[22:25]
	v_mfma_f32_16x16x32_bf16 v[18:21], v[206:209], v[182:185], v[18:21]
	v_mfma_f32_16x16x32_bf16 v[6:9], v[198:201], v[190:193], v[6:9]
	v_mfma_f32_16x16x32_bf16 v[2:5], v[206:209], v[190:193], v[2:5]
	s_setprio 0
	s_barrier
	ds_read_b128 v[146:149], v144
	ds_read_b128 v[150:153], v144 offset:1024
	ds_read_b128 v[154:157], v144 offset:2048
	ds_read_b128 v[158:161], v144 offset:3072
	s_mov_b32 m0, s21
	v_add_u32_e32 v194, s50, v137
	ds_read_b128 v[162:165], v142 offset:32768
	ds_read_b128 v[166:169], v142 offset:33792
	ds_read_b128 v[170:173], v142 offset:34816
	ds_read_b128 v[174:177], v142 offset:35840
	ds_read_b128 v[178:181], v142 offset:36864
	ds_read_b128 v[182:185], v142 offset:37888
	ds_read_b128 v[186:189], v142 offset:38912
	ds_read_b128 v[190:193], v142 offset:39936
	global_load_lds_dwordx4 v194, s[4:5]
	v_add_u32_e32 v194, s50, v138
	s_mov_b32 m0, s22
	s_nop 0
	global_load_lds_dwordx4 v194, s[4:5]
	s_waitcnt lgkmcnt(8)
	s_barrier
	s_waitcnt lgkmcnt(0)
	s_setprio 1

	v_mfma_f32_16x16x32_bf16 v[122:125], v[146:149], v[162:165], v[122:125]
	v_mfma_f32_16x16x32_bf16 v[126:129], v[154:157], v[162:165], v[126:129]
	v_mfma_f32_16x16x32_bf16 v[110:113], v[146:149], v[170:173], v[110:113]
	v_mfma_f32_16x16x32_bf16 v[106:109], v[154:157], v[170:173], v[106:109]
	v_mfma_f32_16x16x32_bf16 v[94:97], v[146:149], v[178:181], v[94:97]
	v_mfma_f32_16x16x32_bf16 v[90:93], v[154:157], v[178:181], v[90:93]
	v_mfma_f32_16x16x32_bf16 v[78:81], v[146:149], v[186:189], v[78:81]
	v_mfma_f32_16x16x32_bf16 v[74:77], v[154:157], v[186:189], v[74:77]
	v_mfma_f32_16x16x32_bf16 v[122:125], v[150:153], v[166:169], v[122:125]
	v_mfma_f32_16x16x32_bf16 v[126:129], v[158:161], v[166:169], v[126:129]
	v_mfma_f32_16x16x32_bf16 v[110:113], v[150:153], v[174:177], v[110:113]
	v_mfma_f32_16x16x32_bf16 v[106:109], v[158:161], v[174:177], v[106:109]
	v_mfma_f32_16x16x32_bf16 v[94:97], v[150:153], v[182:185], v[94:97]
	v_mfma_f32_16x16x32_bf16 v[90:93], v[158:161], v[182:185], v[90:93]
	v_mfma_f32_16x16x32_bf16 v[78:81], v[150:153], v[190:193], v[78:81]
	v_mfma_f32_16x16x32_bf16 v[74:77], v[158:161], v[190:193], v[74:77]
	s_setprio 0
	s_barrier
	s_or_b32 s50, s48, 0x80
	s_add_i32 s51, s37, s17
	v_add_u32_e32 v210, s50, v1
	s_mov_b32 m0, s51
	ds_read_b128 v[194:197], v145
	ds_read_b128 v[198:201], v145 offset:1024
	ds_read_b128 v[202:205], v145 offset:2048
	ds_read_b128 v[206:209], v145 offset:3072
	global_load_lds_dwordx4 v210, s[6:7]
	v_add_u32_e32 v210, s50, v134
	s_add_i32 m0, s51, 0x2000
	s_nop 0
	global_load_lds_dwordx4 v210, s[6:7]
	s_barrier
	s_waitcnt lgkmcnt(0)
	s_setprio 1

	v_mfma_f32_16x16x32_bf16 v[118:121], v[194:197], v[162:165], v[118:121]
	v_mfma_f32_16x16x32_bf16 v[114:117], v[202:205], v[162:165], v[114:117]
	v_mfma_f32_16x16x32_bf16 v[102:105], v[194:197], v[170:173], v[102:105]
	v_mfma_f32_16x16x32_bf16 v[98:101], v[202:205], v[170:173], v[98:101]
	v_mfma_f32_16x16x32_bf16 v[86:89], v[194:197], v[178:181], v[86:89]
	v_mfma_f32_16x16x32_bf16 v[82:85], v[202:205], v[178:181], v[82:85]
	v_mfma_f32_16x16x32_bf16 v[70:73], v[194:197], v[186:189], v[70:73]
	v_mfma_f32_16x16x32_bf16 v[66:69], v[202:205], v[186:189], v[66:69]
	v_mfma_f32_16x16x32_bf16 v[118:121], v[198:201], v[166:169], v[118:121]
	v_mfma_f32_16x16x32_bf16 v[114:117], v[206:209], v[166:169], v[114:117]
	v_mfma_f32_16x16x32_bf16 v[102:105], v[198:201], v[174:177], v[102:105]
	v_mfma_f32_16x16x32_bf16 v[98:101], v[206:209], v[174:177], v[98:101]
	v_mfma_f32_16x16x32_bf16 v[86:89], v[198:201], v[182:185], v[86:89]
	v_mfma_f32_16x16x32_bf16 v[82:85], v[206:209], v[182:185], v[82:85]
	v_mfma_f32_16x16x32_bf16 v[70:73], v[198:201], v[190:193], v[70:73]
	v_mfma_f32_16x16x32_bf16 v[66:69], v[206:209], v[190:193], v[66:69]
	s_setprio 0
	s_mov_b32 m0, s24
	v_add_u32_e32 v210, s49, v135
	s_barrier
	ds_read_b128 v[162:165], v142 offset:49152
	ds_read_b128 v[166:169], v142 offset:50176
	ds_read_b128 v[170:173], v142 offset:51200
	ds_read_b128 v[174:177], v142 offset:52224
	ds_read_b128 v[178:181], v142 offset:53248
	ds_read_b128 v[182:185], v142 offset:54272
	ds_read_b128 v[186:189], v142 offset:55296
	ds_read_b128 v[190:193], v142 offset:56320
	global_load_lds_dwordx4 v210, s[4:5]
	v_add_u32_e32 v210, s49, v136
	s_mov_b32 m0, s25
	s_nop 0
	global_load_lds_dwordx4 v210, s[4:5]
	s_barrier
	s_waitcnt lgkmcnt(0)
	s_setprio 1

	v_mfma_f32_16x16x32_bf16 v[62:65], v[146:149], v[162:165], v[62:65]
	v_mfma_f32_16x16x32_bf16 v[58:61], v[154:157], v[162:165], v[58:61]
	v_mfma_f32_16x16x32_bf16 v[46:49], v[146:149], v[170:173], v[46:49]
	v_mfma_f32_16x16x32_bf16 v[42:45], v[154:157], v[170:173], v[42:45]
	v_mfma_f32_16x16x32_bf16 v[30:33], v[146:149], v[178:181], v[30:33]
	v_mfma_f32_16x16x32_bf16 v[26:29], v[154:157], v[178:181], v[26:29]
	v_mfma_f32_16x16x32_bf16 v[14:17], v[146:149], v[186:189], v[14:17]
	v_mfma_f32_16x16x32_bf16 v[10:13], v[154:157], v[186:189], v[10:13]
	v_mfma_f32_16x16x32_bf16 v[62:65], v[150:153], v[166:169], v[62:65]
	v_mfma_f32_16x16x32_bf16 v[58:61], v[158:161], v[166:169], v[58:61]
	v_mfma_f32_16x16x32_bf16 v[46:49], v[150:153], v[174:177], v[46:49]
	v_mfma_f32_16x16x32_bf16 v[42:45], v[158:161], v[174:177], v[42:45]
	v_mfma_f32_16x16x32_bf16 v[30:33], v[150:153], v[182:185], v[30:33]
	v_mfma_f32_16x16x32_bf16 v[26:29], v[158:161], v[182:185], v[26:29]
	v_mfma_f32_16x16x32_bf16 v[14:17], v[150:153], v[190:193], v[14:17]
	v_mfma_f32_16x16x32_bf16 v[10:13], v[158:161], v[190:193], v[10:13]
	s_setprio 0
	s_barrier
	s_add_i32 s48, s48, 0x80080
	s_add_i32 s49, s38, s17
	v_add_u32_e32 v146, s48, v1
	s_mov_b32 m0, s49
	s_nop 0
	global_load_lds_dwordx4 v146, s[6:7]
	v_add_u32_e32 v146, s48, v134
	s_add_i32 m0, s49, 0x2000
	s_nop 0
	global_load_lds_dwordx4 v146, s[6:7]
	s_waitcnt vmcnt(6)
	s_barrier
	s_setprio 1
	v_mfma_f32_16x16x32_bf16 v[54:57], v[194:197], v[162:165], v[54:57]
	v_mfma_f32_16x16x32_bf16 v[50:53], v[202:205], v[162:165], v[50:53]
	v_mfma_f32_16x16x32_bf16 v[38:41], v[194:197], v[170:173], v[38:41]
	v_mfma_f32_16x16x32_bf16 v[34:37], v[202:205], v[170:173], v[34:37]
	v_mfma_f32_16x16x32_bf16 v[22:25], v[194:197], v[178:181], v[22:25]
	v_mfma_f32_16x16x32_bf16 v[18:21], v[202:205], v[178:181], v[18:21]
	v_mfma_f32_16x16x32_bf16 v[6:9], v[194:197], v[186:189], v[6:9]
	v_mfma_f32_16x16x32_bf16 v[2:5], v[202:205], v[186:189], v[2:5]
	v_mfma_f32_16x16x32_bf16 v[54:57], v[198:201], v[166:169], v[54:57]
	v_mfma_f32_16x16x32_bf16 v[50:53], v[206:209], v[166:169], v[50:53]
	v_mfma_f32_16x16x32_bf16 v[38:41], v[198:201], v[174:177], v[38:41]
	v_mfma_f32_16x16x32_bf16 v[34:37], v[206:209], v[174:177], v[34:37]
	v_mfma_f32_16x16x32_bf16 v[22:25], v[198:201], v[182:185], v[22:25]
	v_mfma_f32_16x16x32_bf16 v[18:21], v[206:209], v[182:185], v[18:21]
	v_mfma_f32_16x16x32_bf16 v[6:9], v[198:201], v[190:193], v[6:9]
	v_mfma_f32_16x16x32_bf16 v[2:5], v[206:209], v[190:193], v[2:5]
	s_setprio 0
	s_add_i32 s47, s47, 2
	s_addk_i32 s45, 0x100
	s_addk_i32 s46, 0x100
	s_cmp_ge_i32 s47, s26
	s_barrier
	s_cbranch_scc0 .LBB0_451
	s_branch .LBB0_446

.LBB0_464:
	ds_read_b128 v[152:155], v146
	ds_read_b128 v[156:159], v146 offset:1024
	ds_read_b128 v[160:163], v146 offset:2048
	ds_read_b128 v[164:167], v146 offset:3072
	s_add_i32 s46, s43, 0x80
	s_cmp_eq_u32 s30, s45
	s_cselect_b32 s48, s16, s46
	s_cselect_b32 s46, s17, s44
	s_or_b32 s47, s48, 0x80
	s_mov_b32 m0, s34
	v_add_u32_e32 v66, s43, v141
	ds_read_b128 v[168:171], v147
	ds_read_b128 v[172:175], v147 offset:1024
	ds_read_b128 v[176:179], v147 offset:2048
	ds_read_b128 v[180:183], v147 offset:3072
	ds_read_b128 v[184:187], v147 offset:4096
	ds_read_b128 v[188:191], v147 offset:5120
	ds_read_b128 v[192:195], v147 offset:6144
	ds_read_b128 v[196:199], v147 offset:7168
	global_load_lds_dwordx4 v66, s[4:5]
	v_add_u32_e32 v66, s43, v142
	s_mov_b32 m0, s35
	s_nop 0
	global_load_lds_dwordx4 v66, s[4:5]
	s_waitcnt lgkmcnt(8)
	s_barrier
	s_waitcnt lgkmcnt(0)
	s_setprio 1

	v_mfma_scale_f32_16x16x128_f8f6f4 v[126:129], v[152:159], v[168:175], v[126:129], v149, v148 op_sel_hi:[0,0,0]
	v_mfma_scale_f32_16x16x128_f8f6f4 v[122:125], v[160:167], v[168:175], v[122:125], v149, v148 op_sel_hi:[0,0,0]
	v_mfma_scale_f32_16x16x128_f8f6f4 v[134:137], v[152:159], v[176:183], v[110:113], v149, v148 op_sel_hi:[0,0,0]
	v_mfma_scale_f32_16x16x128_f8f6f4 v[200:203], v[160:167], v[176:183], v[106:109], v149, v148 op_sel_hi:[0,0,0]
	v_mfma_scale_f32_16x16x128_f8f6f4 v[204:207], v[152:159], v[184:191], v[94:97], v149, v148 op_sel_hi:[0,0,0]
	v_mfma_scale_f32_16x16x128_f8f6f4 v[208:211], v[160:167], v[184:191], v[90:93], v149, v148 op_sel_hi:[0,0,0]
	v_mfma_scale_f32_16x16x128_f8f6f4 v[212:215], v[152:159], v[192:199], v[78:81], v149, v148 op_sel_hi:[0,0,0]
	v_mfma_scale_f32_16x16x128_f8f6f4 v[216:219], v[160:167], v[192:199], v[74:77], v149, v148 op_sel_hi:[0,0,0]
	s_setprio 0
	s_barrier
	s_mov_b32 m0, s36
	v_add_u32_e32 v66, s46, v1
	s_nop 2
	ds_read_b128 v[74:77], v150
	ds_read_b128 v[78:81], v150 offset:1024
	ds_read_b128 v[90:93], v150 offset:2048
	ds_read_b128 v[94:97], v150 offset:3072
	global_load_lds_dwordx4 v66, s[10:11]
	v_add_u32_e32 v66, s46, v138
	s_add_i32 m0, s36, 0x2000
	s_nop 0
	global_load_lds_dwordx4 v66, s[10:11]
	s_barrier
	s_waitcnt lgkmcnt(0)
	s_setprio 1

	v_mfma_scale_f32_16x16x128_f8f6f4 v[118:121], v[74:81], v[168:175], v[118:121], v149, v148 op_sel_hi:[0,0,0]
	v_mfma_scale_f32_16x16x128_f8f6f4 v[114:117], v[90:97], v[168:175], v[114:117], v149, v148 op_sel_hi:[0,0,0]
	v_mfma_scale_f32_16x16x128_f8f6f4 v[168:171], v[74:81], v[176:183], v[102:105], v149, v148 op_sel_hi:[0,0,0]
	v_mfma_scale_f32_16x16x128_f8f6f4 v[172:175], v[90:97], v[176:183], v[98:101], v149, v148 op_sel_hi:[0,0,0]
	v_mfma_scale_f32_16x16x128_f8f6f4 v[176:179], v[74:81], v[184:191], v[86:89], v149, v148 op_sel_hi:[0,0,0]
	v_mfma_scale_f32_16x16x128_f8f6f4 v[180:183], v[90:97], v[184:191], v[82:85], v149, v148 op_sel_hi:[0,0,0]
	v_mfma_scale_f32_16x16x128_f8f6f4 v[184:187], v[74:81], v[192:199], v[70:73], v149, v148 op_sel_hi:[0,0,0]
	v_mfma_scale_f32_16x16x128_f8f6f4 v[188:191], v[90:97], v[192:199], v[10:13], v149, v148 op_sel_hi:[0,0,0]
	s_setprio 0
	s_mov_b32 m0, s21
	s_nop 4
	v_add_u32_e32 v10, s48, v139
	s_barrier
	ds_read_b128 v[66:69], v147 offset:16384
	ds_read_b128 v[70:73], v147 offset:17408
	ds_read_b128 v[82:85], v147 offset:18432
	ds_read_b128 v[86:89], v147 offset:19456
	ds_read_b128 v[98:101], v147 offset:20480
	ds_read_b128 v[102:105], v147 offset:21504
	ds_read_b128 v[106:109], v147 offset:22528
	ds_read_b128 v[110:113], v147 offset:23552
	global_load_lds_dwordx4 v10, s[4:5]
	v_add_u32_e32 v10, s48, v140
	s_mov_b32 m0, s22
	s_nop 0
	global_load_lds_dwordx4 v10, s[4:5]
	s_barrier
	s_waitcnt lgkmcnt(0)
	s_setprio 1

	v_mfma_scale_f32_16x16x128_f8f6f4 v[62:65], v[152:159], v[66:73], v[62:65], v149, v148 op_sel_hi:[0,0,0]
	v_mfma_scale_f32_16x16x128_f8f6f4 v[58:61], v[160:167], v[66:73], v[58:61], v149, v148 op_sel_hi:[0,0,0]
	v_mfma_scale_f32_16x16x128_f8f6f4 v[232:235], v[160:167], v[106:113], v[232:235], v149, v148 op_sel_hi:[0,0,0]
	v_mfma_scale_f32_16x16x128_f8f6f4 v[192:195], v[152:159], v[82:89], v[46:49], v149, v148 op_sel_hi:[0,0,0]
	v_mfma_scale_f32_16x16x128_f8f6f4 v[196:199], v[160:167], v[82:89], v[42:45], v149, v148 op_sel_hi:[0,0,0]
	v_mfma_scale_f32_16x16x128_f8f6f4 v[220:223], v[152:159], v[98:105], v[30:33], v149, v148 op_sel_hi:[0,0,0]
	v_mfma_scale_f32_16x16x128_f8f6f4 v[224:227], v[160:167], v[98:105], v[26:29], v149, v148 op_sel_hi:[0,0,0]
	v_mfma_scale_f32_16x16x128_f8f6f4 v[228:231], v[152:159], v[106:113], v[14:17], v149, v148 op_sel_hi:[0,0,0]
	s_setprio 0
	s_barrier
	s_add_i32 s49, s46, 0x40000
	s_add_i32 s50, s31, s19
	v_add_u32_e32 v10, s49, v1
	s_mov_b32 m0, s50
	s_nop 0
	global_load_lds_dwordx4 v10, s[10:11]
	v_add_u32_e32 v10, s49, v138
	s_add_i32 m0, s50, 0x2000
	s_nop 0
	global_load_lds_dwordx4 v10, s[10:11]
	s_waitcnt vmcnt(6)
	s_barrier
	s_setprio 1
	v_mfma_scale_f32_16x16x128_f8f6f4 v[54:57], v[74:81], v[66:73], v[54:57], v149, v148 op_sel_hi:[0,0,0]
	v_mfma_scale_f32_16x16x128_f8f6f4 v[50:53], v[90:97], v[66:73], v[50:53], v149, v148 op_sel_hi:[0,0,0]
	v_mfma_scale_f32_16x16x128_f8f6f4 v[236:239], v[74:81], v[82:89], v[38:41], v149, v148 op_sel_hi:[0,0,0]
	v_mfma_scale_f32_16x16x128_f8f6f4 v[240:243], v[90:97], v[82:89], v[34:37], v149, v148 op_sel_hi:[0,0,0]
	v_mfma_scale_f32_16x16x128_f8f6f4 v[244:247], v[74:81], v[98:105], v[22:25], v149, v148 op_sel_hi:[0,0,0]
	v_mfma_scale_f32_16x16x128_f8f6f4 v[248:251], v[90:97], v[98:105], v[18:21], v149, v148 op_sel_hi:[0,0,0]
	v_mfma_scale_f32_16x16x128_f8f6f4 v[130:133], v[74:81], v[106:113], v[6:9], v149, v148 op_sel_hi:[0,0,0]
	v_mfma_scale_f32_16x16x128_f8f6f4 v[66:69], v[90:97], v[106:113], v[2:5], v149, v148 op_sel_hi:[0,0,0]
	s_setprio 0
	s_add_i32 s49, 0, 0x18000
	v_add_u32_e32 v10, s49, v145
	s_barrier
	s_nop 2
	ds_read_b128 v[2:5], v10
	ds_read_b128 v[6:9], v10 offset:1024
	ds_read_b128 v[18:21], v10 offset:2048
	ds_read_b128 v[22:25], v10 offset:3072
	s_mov_b32 m0, s23
	v_add_u32_e32 v70, s48, v141
	ds_read_b128 v[10:13], v147 offset:32768
	ds_read_b128 v[14:17], v147 offset:33792
	ds_read_b128 v[26:29], v147 offset:34816
	ds_read_b128 v[30:33], v147 offset:35840
	ds_read_b128 v[34:37], v147 offset:36864
	ds_read_b128 v[38:41], v147 offset:37888
	ds_read_b128 v[42:45], v147 offset:38912
	ds_read_b128 v[46:49], v147 offset:39936
	global_load_lds_dwordx4 v70, s[4:5]
	v_add_u32_e32 v70, s48, v142
	s_mov_b32 m0, s24
	s_nop 0
	global_load_lds_dwordx4 v70, s[4:5]
	s_waitcnt lgkmcnt(8)
	s_barrier
	s_waitcnt lgkmcnt(0)
	s_setprio 1

	v_mfma_scale_f32_16x16x128_f8f6f4 v[126:129], v[2:9], v[10:17], v[126:129], v149, v148 op_sel_hi:[0,0,0]
	v_mfma_scale_f32_16x16x128_f8f6f4 v[122:125], v[18:25], v[10:17], v[122:125], v149, v148 op_sel_hi:[0,0,0]
	v_mfma_scale_f32_16x16x128_f8f6f4 v[110:113], v[2:9], v[26:33], v[134:137], v149, v148 op_sel_hi:[0,0,0]
	v_mfma_scale_f32_16x16x128_f8f6f4 v[106:109], v[18:25], v[26:33], v[200:203], v149, v148 op_sel_hi:[0,0,0]
	v_mfma_scale_f32_16x16x128_f8f6f4 v[94:97], v[2:9], v[34:41], v[204:207], v149, v148 op_sel_hi:[0,0,0]
	v_mfma_scale_f32_16x16x128_f8f6f4 v[90:93], v[18:25], v[34:41], v[208:211], v149, v148 op_sel_hi:[0,0,0]
	v_mfma_scale_f32_16x16x128_f8f6f4 v[78:81], v[2:9], v[42:49], v[212:215], v149, v148 op_sel_hi:[0,0,0]
	v_mfma_scale_f32_16x16x128_f8f6f4 v[74:77], v[18:25], v[42:49], v[216:219], v149, v148 op_sel_hi:[0,0,0]
	s_setprio 0
	s_barrier
	s_add_i32 s48, 0, 0x1c000
	v_add_u32_e32 v70, s48, v145
	s_or_b32 s50, s46, 0x80
	s_add_i32 s49, s49, s19
	ds_read_b128 v[152:155], v70
	ds_read_b128 v[156:159], v70 offset:1024
	ds_read_b128 v[160:163], v70 offset:2048
	ds_read_b128 v[164:167], v70 offset:3072
	v_add_u32_e32 v70, s50, v1
	s_mov_b32 m0, s49
	s_nop 0
	global_load_lds_dwordx4 v70, s[10:11]
	v_add_u32_e32 v70, s50, v138
	s_add_i32 m0, s49, 0x2000
	s_nop 0
	global_load_lds_dwordx4 v70, s[10:11]
	s_barrier
	s_waitcnt lgkmcnt(0)
	s_setprio 1

	v_mfma_scale_f32_16x16x128_f8f6f4 v[118:121], v[152:159], v[10:17], v[118:121], v149, v148 op_sel_hi:[0,0,0]
	v_mfma_scale_f32_16x16x128_f8f6f4 v[114:117], v[160:167], v[10:17], v[114:117], v149, v148 op_sel_hi:[0,0,0]
	v_mfma_scale_f32_16x16x128_f8f6f4 v[102:105], v[152:159], v[26:33], v[168:171], v149, v148 op_sel_hi:[0,0,0]
	v_mfma_scale_f32_16x16x128_f8f6f4 v[98:101], v[160:167], v[26:33], v[172:175], v149, v148 op_sel_hi:[0,0,0]
	v_mfma_scale_f32_16x16x128_f8f6f4 v[86:89], v[152:159], v[34:41], v[176:179], v149, v148 op_sel_hi:[0,0,0]
	v_mfma_scale_f32_16x16x128_f8f6f4 v[82:85], v[160:167], v[34:41], v[180:183], v149, v148 op_sel_hi:[0,0,0]
	v_mfma_scale_f32_16x16x128_f8f6f4 v[70:73], v[152:159], v[42:49], v[184:187], v149, v148 op_sel_hi:[0,0,0]
	v_mfma_scale_f32_16x16x128_f8f6f4 v[10:13], v[160:167], v[42:49], v[188:191], v149, v148 op_sel_hi:[0,0,0]
	s_setprio 0
	s_mov_b32 m0, s26
	v_add_u32_e32 v14, s47, v139
	s_barrier
	ds_read_b128 v[34:37], v147 offset:49152
	ds_read_b128 v[38:41], v147 offset:50176
	ds_read_b128 v[168:171], v147 offset:51200
	ds_read_b128 v[172:175], v147 offset:52224
	ds_read_b128 v[176:179], v147 offset:53248
	ds_read_b128 v[180:183], v147 offset:54272
	ds_read_b128 v[184:187], v147 offset:55296
	ds_read_b128 v[188:191], v147 offset:56320
	global_load_lds_dwordx4 v14, s[4:5]
	v_add_u32_e32 v14, s47, v140
	s_mov_b32 m0, s27
	s_nop 0
	global_load_lds_dwordx4 v14, s[4:5]
	s_barrier
	s_waitcnt lgkmcnt(0)
	s_setprio 1

	v_mfma_scale_f32_16x16x128_f8f6f4 v[62:65], v[2:9], v[34:41], v[62:65], v149, v148 op_sel_hi:[0,0,0]
	v_mfma_scale_f32_16x16x128_f8f6f4 v[58:61], v[18:25], v[34:41], v[58:61], v149, v148 op_sel_hi:[0,0,0]
	v_mfma_scale_f32_16x16x128_f8f6f4 v[46:49], v[2:9], v[168:175], v[192:195], v149, v148 op_sel_hi:[0,0,0]
	v_mfma_scale_f32_16x16x128_f8f6f4 v[42:45], v[18:25], v[168:175], v[196:199], v149, v148 op_sel_hi:[0,0,0]
	v_mfma_scale_f32_16x16x128_f8f6f4 v[30:33], v[2:9], v[176:183], v[220:223], v149, v148 op_sel_hi:[0,0,0]
	v_mfma_scale_f32_16x16x128_f8f6f4 v[26:29], v[18:25], v[176:183], v[224:227], v149, v148 op_sel_hi:[0,0,0]
	v_mfma_scale_f32_16x16x128_f8f6f4 v[14:17], v[2:9], v[184:191], v[228:231], v149, v148 op_sel_hi:[0,0,0]
	v_mfma_scale_f32_16x16x128_f8f6f4 v[232:235], v[18:25], v[184:191], v[232:235], v149, v148 op_sel_hi:[0,0,0]
	s_setprio 0
	s_barrier
	s_add_i32 s46, s46, 0x40080
	s_add_i32 s47, s48, s19
	v_add_u32_e32 v2, s46, v1
	s_mov_b32 m0, s47
	s_nop 0
	global_load_lds_dwordx4 v2, s[10:11]
	v_add_u32_e32 v2, s46, v138
	s_add_i32 m0, s47, 0x2000
	s_nop 0
	global_load_lds_dwordx4 v2, s[10:11]
	s_waitcnt vmcnt(6)
	s_barrier
	s_setprio 1
	v_mfma_scale_f32_16x16x128_f8f6f4 v[54:57], v[152:159], v[34:41], v[54:57], v149, v148 op_sel_hi:[0,0,0]
	v_mfma_scale_f32_16x16x128_f8f6f4 v[50:53], v[160:167], v[34:41], v[50:53], v149, v148 op_sel_hi:[0,0,0]
	v_mfma_scale_f32_16x16x128_f8f6f4 v[38:41], v[152:159], v[168:175], v[236:239], v149, v148 op_sel_hi:[0,0,0]
	v_mfma_scale_f32_16x16x128_f8f6f4 v[34:37], v[160:167], v[168:175], v[240:243], v149, v148 op_sel_hi:[0,0,0]
	v_mfma_scale_f32_16x16x128_f8f6f4 v[22:25], v[152:159], v[176:183], v[244:247], v149, v148 op_sel_hi:[0,0,0]
	v_mfma_scale_f32_16x16x128_f8f6f4 v[18:21], v[160:167], v[176:183], v[248:251], v149, v148 op_sel_hi:[0,0,0]
	v_mfma_scale_f32_16x16x128_f8f6f4 v[6:9], v[152:159], v[184:191], v[130:133], v149, v148 op_sel_hi:[0,0,0]
	v_mfma_scale_f32_16x16x128_f8f6f4 v[2:5], v[160:167], v[184:191], v[66:69], v149, v148 op_sel_hi:[0,0,0]
	s_setprio 0
	s_add_i32 s45, s45, 2
	s_addk_i32 s43, 0x100
	s_addk_i32 s44, 0x100
	s_cmp_ge_i32 s45, s28
	s_barrier
	s_cbranch_scc0 .LBB0_464
	s_branch .LBB0_466

.LBB0_620:
	ds_read_b128 v[146:149], v141
	ds_read_b128 v[150:153], v141 offset:1024
	ds_read_b128 v[154:157], v141 offset:2048
	ds_read_b128 v[158:161], v141 offset:3072
	s_add_i32 s50, s47, 0x80
	s_cmp_eq_u32 s30, s49
	s_cselect_b32 s52, s16, s50
	s_cselect_b32 s50, s17, s48
	s_or_b32 s51, s52, 0x80
	s_mov_b32 m0, s31
	v_add_u32_e32 v194, s47, v131
	ds_read_b128 v[162:165], v142
	ds_read_b128 v[166:169], v142 offset:1024
	ds_read_b128 v[170:173], v142 offset:2048
	ds_read_b128 v[174:177], v142 offset:3072
	ds_read_b128 v[178:181], v142 offset:4096
	ds_read_b128 v[182:185], v142 offset:5120
	ds_read_b128 v[186:189], v142 offset:6144
	ds_read_b128 v[190:193], v142 offset:7168
	global_load_lds_dwordx4 v194, s[6:7]
	v_add_u32_e32 v194, s47, v133
	s_mov_b32 m0, s33
	s_nop 0
	global_load_lds_dwordx4 v194, s[6:7]
	s_waitcnt lgkmcnt(8)
	s_barrier
	s_waitcnt lgkmcnt(0)
	s_setprio 1

	v_mfma_f32_16x16x32_bf16 v[122:125], v[146:149], v[162:165], v[122:125]
	v_mfma_f32_16x16x32_bf16 v[126:129], v[154:157], v[162:165], v[126:129]
	v_mfma_f32_16x16x32_bf16 v[110:113], v[146:149], v[170:173], v[110:113]
	v_mfma_f32_16x16x32_bf16 v[106:109], v[154:157], v[170:173], v[106:109]
	v_mfma_f32_16x16x32_bf16 v[94:97], v[146:149], v[178:181], v[94:97]
	v_mfma_f32_16x16x32_bf16 v[90:93], v[154:157], v[178:181], v[90:93]
	v_mfma_f32_16x16x32_bf16 v[78:81], v[146:149], v[186:189], v[78:81]
	v_mfma_f32_16x16x32_bf16 v[74:77], v[154:157], v[186:189], v[74:77]
	v_mfma_f32_16x16x32_bf16 v[122:125], v[150:153], v[166:169], v[122:125]
	v_mfma_f32_16x16x32_bf16 v[126:129], v[158:161], v[166:169], v[126:129]
	v_mfma_f32_16x16x32_bf16 v[110:113], v[150:153], v[174:177], v[110:113]
	v_mfma_f32_16x16x32_bf16 v[106:109], v[158:161], v[174:177], v[106:109]
	v_mfma_f32_16x16x32_bf16 v[94:97], v[150:153], v[182:185], v[94:97]
	v_mfma_f32_16x16x32_bf16 v[90:93], v[158:161], v[182:185], v[90:93]
	v_mfma_f32_16x16x32_bf16 v[78:81], v[150:153], v[190:193], v[78:81]
	v_mfma_f32_16x16x32_bf16 v[74:77], v[158:161], v[190:193], v[74:77]
	s_setprio 0
	s_barrier
	s_mov_b32 m0, s35
	v_add_u32_e32 v210, s50, v1
	ds_read_b128 v[194:197], v143
	ds_read_b128 v[198:201], v143 offset:1024
	ds_read_b128 v[202:205], v143 offset:2048
	ds_read_b128 v[206:209], v143 offset:3072
	global_load_lds_dwordx4 v210, s[10:11]
	v_add_u32_e32 v210, s50, v138
	s_mov_b32 m0, s36
	s_nop 0
	global_load_lds_dwordx4 v210, s[10:11]
	s_barrier
	s_waitcnt lgkmcnt(0)
	s_setprio 1

	v_mfma_f32_16x16x32_bf16 v[118:121], v[194:197], v[162:165], v[118:121]
	v_mfma_f32_16x16x32_bf16 v[114:117], v[202:205], v[162:165], v[114:117]
	v_mfma_f32_16x16x32_bf16 v[102:105], v[194:197], v[170:173], v[102:105]
	v_mfma_f32_16x16x32_bf16 v[98:101], v[202:205], v[170:173], v[98:101]
	v_mfma_f32_16x16x32_bf16 v[86:89], v[194:197], v[178:181], v[86:89]
	v_mfma_f32_16x16x32_bf16 v[82:85], v[202:205], v[178:181], v[82:85]
	v_mfma_f32_16x16x32_bf16 v[70:73], v[194:197], v[186:189], v[70:73]
	v_mfma_f32_16x16x32_bf16 v[66:69], v[202:205], v[186:189], v[66:69]
	v_mfma_f32_16x16x32_bf16 v[118:121], v[198:201], v[166:169], v[118:121]
	v_mfma_f32_16x16x32_bf16 v[114:117], v[206:209], v[166:169], v[114:117]
	v_mfma_f32_16x16x32_bf16 v[102:105], v[198:201], v[174:177], v[102:105]
	v_mfma_f32_16x16x32_bf16 v[98:101], v[206:209], v[174:177], v[98:101]
	v_mfma_f32_16x16x32_bf16 v[86:89], v[198:201], v[182:185], v[86:89]
	v_mfma_f32_16x16x32_bf16 v[82:85], v[206:209], v[182:185], v[82:85]
	v_mfma_f32_16x16x32_bf16 v[70:73], v[198:201], v[190:193], v[70:73]
	v_mfma_f32_16x16x32_bf16 v[66:69], v[206:209], v[190:193], v[66:69]
	s_setprio 0
	s_mov_b32 m0, s21
	v_add_u32_e32 v210, s52, v130
	s_barrier
	ds_read_b128 v[162:165], v142 offset:16384
	ds_read_b128 v[166:169], v142 offset:17408
	ds_read_b128 v[170:173], v142 offset:18432
	ds_read_b128 v[174:177], v142 offset:19456
	ds_read_b128 v[178:181], v142 offset:20480
	ds_read_b128 v[182:185], v142 offset:21504
	ds_read_b128 v[186:189], v142 offset:22528
	ds_read_b128 v[190:193], v142 offset:23552
	global_load_lds_dwordx4 v210, s[6:7]
	v_add_u32_e32 v210, s52, v132
	s_mov_b32 m0, s22
	s_nop 0
	global_load_lds_dwordx4 v210, s[6:7]
	s_barrier
	s_waitcnt lgkmcnt(0)
	s_setprio 1

	v_mfma_f32_16x16x32_bf16 v[62:65], v[146:149], v[162:165], v[62:65]
	v_mfma_f32_16x16x32_bf16 v[58:61], v[154:157], v[162:165], v[58:61]
	v_mfma_f32_16x16x32_bf16 v[46:49], v[146:149], v[170:173], v[46:49]
	v_mfma_f32_16x16x32_bf16 v[42:45], v[154:157], v[170:173], v[42:45]
	v_mfma_f32_16x16x32_bf16 v[30:33], v[146:149], v[178:181], v[30:33]
	v_mfma_f32_16x16x32_bf16 v[26:29], v[154:157], v[178:181], v[26:29]
	v_mfma_f32_16x16x32_bf16 v[14:17], v[146:149], v[186:189], v[14:17]
	v_mfma_f32_16x16x32_bf16 v[10:13], v[154:157], v[186:189], v[10:13]
	v_mfma_f32_16x16x32_bf16 v[62:65], v[150:153], v[166:169], v[62:65]
	v_mfma_f32_16x16x32_bf16 v[58:61], v[158:161], v[166:169], v[58:61]
	v_mfma_f32_16x16x32_bf16 v[46:49], v[150:153], v[174:177], v[46:49]
	v_mfma_f32_16x16x32_bf16 v[42:45], v[158:161], v[174:177], v[42:45]
	v_mfma_f32_16x16x32_bf16 v[30:33], v[150:153], v[182:185], v[30:33]
	v_mfma_f32_16x16x32_bf16 v[26:29], v[158:161], v[182:185], v[26:29]
	v_mfma_f32_16x16x32_bf16 v[14:17], v[150:153], v[190:193], v[14:17]
	v_mfma_f32_16x16x32_bf16 v[10:13], v[158:161], v[190:193], v[10:13]
	s_setprio 0
	s_barrier
	s_add_i32 s53, s50, 0x20000
	s_mov_b32 m0, s37
	v_add_u32_e32 v146, s53, v1
	global_load_lds_dwordx4 v146, s[10:11]
	v_add_u32_e32 v146, s53, v138
	s_mov_b32 m0, s38
	s_nop 0
	global_load_lds_dwordx4 v146, s[10:11]
	s_waitcnt vmcnt(6)
	s_barrier
	s_setprio 1
	v_mfma_f32_16x16x32_bf16 v[54:57], v[194:197], v[162:165], v[54:57]
	v_mfma_f32_16x16x32_bf16 v[50:53], v[202:205], v[162:165], v[50:53]
	v_mfma_f32_16x16x32_bf16 v[38:41], v[194:197], v[170:173], v[38:41]
	v_mfma_f32_16x16x32_bf16 v[34:37], v[202:205], v[170:173], v[34:37]
	v_mfma_f32_16x16x32_bf16 v[22:25], v[194:197], v[178:181], v[22:25]
	v_mfma_f32_16x16x32_bf16 v[18:21], v[202:205], v[178:181], v[18:21]
	v_mfma_f32_16x16x32_bf16 v[6:9], v[194:197], v[186:189], v[6:9]
	v_mfma_f32_16x16x32_bf16 v[2:5], v[202:205], v[186:189], v[2:5]
	v_mfma_f32_16x16x32_bf16 v[54:57], v[198:201], v[166:169], v[54:57]
	v_mfma_f32_16x16x32_bf16 v[50:53], v[206:209], v[166:169], v[50:53]
	v_mfma_f32_16x16x32_bf16 v[38:41], v[198:201], v[174:177], v[38:41]
	v_mfma_f32_16x16x32_bf16 v[34:37], v[206:209], v[174:177], v[34:37]
	v_mfma_f32_16x16x32_bf16 v[22:25], v[198:201], v[182:185], v[22:25]
	v_mfma_f32_16x16x32_bf16 v[18:21], v[206:209], v[182:185], v[18:21]
	v_mfma_f32_16x16x32_bf16 v[6:9], v[198:201], v[190:193], v[6:9]
	v_mfma_f32_16x16x32_bf16 v[2:5], v[206:209], v[190:193], v[2:5]
	s_setprio 0
	s_barrier
	ds_read_b128 v[146:149], v144
	ds_read_b128 v[150:153], v144 offset:1024
	ds_read_b128 v[154:157], v144 offset:2048
	ds_read_b128 v[158:161], v144 offset:3072
	s_mov_b32 m0, s23
	v_add_u32_e32 v194, s52, v131
	ds_read_b128 v[162:165], v142 offset:32768
	ds_read_b128 v[166:169], v142 offset:33792
	ds_read_b128 v[170:173], v142 offset:34816
	ds_read_b128 v[174:177], v142 offset:35840
	ds_read_b128 v[178:181], v142 offset:36864
	ds_read_b128 v[182:185], v142 offset:37888
	ds_read_b128 v[186:189], v142 offset:38912
	ds_read_b128 v[190:193], v142 offset:39936
	global_load_lds_dwordx4 v194, s[6:7]
	v_add_u32_e32 v194, s52, v133
	s_mov_b32 m0, s24
	s_nop 0
	global_load_lds_dwordx4 v194, s[6:7]
	s_waitcnt lgkmcnt(8)
	s_barrier
	s_waitcnt lgkmcnt(0)
	s_setprio 1

	v_mfma_f32_16x16x32_bf16 v[122:125], v[146:149], v[162:165], v[122:125]
	v_mfma_f32_16x16x32_bf16 v[126:129], v[154:157], v[162:165], v[126:129]
	v_mfma_f32_16x16x32_bf16 v[110:113], v[146:149], v[170:173], v[110:113]
	v_mfma_f32_16x16x32_bf16 v[106:109], v[154:157], v[170:173], v[106:109]
	v_mfma_f32_16x16x32_bf16 v[94:97], v[146:149], v[178:181], v[94:97]
	v_mfma_f32_16x16x32_bf16 v[90:93], v[154:157], v[178:181], v[90:93]
	v_mfma_f32_16x16x32_bf16 v[78:81], v[146:149], v[186:189], v[78:81]
	v_mfma_f32_16x16x32_bf16 v[74:77], v[154:157], v[186:189], v[74:77]
	v_mfma_f32_16x16x32_bf16 v[122:125], v[150:153], v[166:169], v[122:125]
	v_mfma_f32_16x16x32_bf16 v[126:129], v[158:161], v[166:169], v[126:129]
	v_mfma_f32_16x16x32_bf16 v[110:113], v[150:153], v[174:177], v[110:113]
	v_mfma_f32_16x16x32_bf16 v[106:109], v[158:161], v[174:177], v[106:109]
	v_mfma_f32_16x16x32_bf16 v[94:97], v[150:153], v[182:185], v[94:97]
	v_mfma_f32_16x16x32_bf16 v[90:93], v[158:161], v[182:185], v[90:93]
	v_mfma_f32_16x16x32_bf16 v[78:81], v[150:153], v[190:193], v[78:81]
	v_mfma_f32_16x16x32_bf16 v[74:77], v[158:161], v[190:193], v[74:77]
	s_setprio 0
	s_barrier
	s_or_b32 s52, s50, 0x80
	s_add_i32 s53, s39, s19
	v_add_u32_e32 v210, s52, v1
	s_mov_b32 m0, s53
	ds_read_b128 v[194:197], v145
	ds_read_b128 v[198:201], v145 offset:1024
	ds_read_b128 v[202:205], v145 offset:2048
	ds_read_b128 v[206:209], v145 offset:3072
	global_load_lds_dwordx4 v210, s[10:11]
	v_add_u32_e32 v210, s52, v138
	s_add_i32 m0, s53, 0x2000
	s_nop 0
	global_load_lds_dwordx4 v210, s[10:11]
	s_barrier
	s_waitcnt lgkmcnt(0)
	s_setprio 1

	v_mfma_f32_16x16x32_bf16 v[118:121], v[194:197], v[162:165], v[118:121]
	v_mfma_f32_16x16x32_bf16 v[114:117], v[202:205], v[162:165], v[114:117]
	v_mfma_f32_16x16x32_bf16 v[102:105], v[194:197], v[170:173], v[102:105]
	v_mfma_f32_16x16x32_bf16 v[98:101], v[202:205], v[170:173], v[98:101]
	v_mfma_f32_16x16x32_bf16 v[86:89], v[194:197], v[178:181], v[86:89]
	v_mfma_f32_16x16x32_bf16 v[82:85], v[202:205], v[178:181], v[82:85]
	v_mfma_f32_16x16x32_bf16 v[70:73], v[194:197], v[186:189], v[70:73]
	v_mfma_f32_16x16x32_bf16 v[66:69], v[202:205], v[186:189], v[66:69]
	v_mfma_f32_16x16x32_bf16 v[118:121], v[198:201], v[166:169], v[118:121]
	v_mfma_f32_16x16x32_bf16 v[114:117], v[206:209], v[166:169], v[114:117]
	v_mfma_f32_16x16x32_bf16 v[102:105], v[198:201], v[174:177], v[102:105]
	v_mfma_f32_16x16x32_bf16 v[98:101], v[206:209], v[174:177], v[98:101]
	v_mfma_f32_16x16x32_bf16 v[86:89], v[198:201], v[182:185], v[86:89]
	v_mfma_f32_16x16x32_bf16 v[82:85], v[206:209], v[182:185], v[82:85]
	v_mfma_f32_16x16x32_bf16 v[70:73], v[198:201], v[190:193], v[70:73]
	v_mfma_f32_16x16x32_bf16 v[66:69], v[206:209], v[190:193], v[66:69]
	s_setprio 0
	s_mov_b32 m0, s26
	v_add_u32_e32 v210, s51, v130
	s_barrier
	ds_read_b128 v[162:165], v142 offset:49152
	ds_read_b128 v[166:169], v142 offset:50176
	ds_read_b128 v[170:173], v142 offset:51200
	ds_read_b128 v[174:177], v142 offset:52224
	ds_read_b128 v[178:181], v142 offset:53248
	ds_read_b128 v[182:185], v142 offset:54272
	ds_read_b128 v[186:189], v142 offset:55296
	ds_read_b128 v[190:193], v142 offset:56320
	global_load_lds_dwordx4 v210, s[6:7]
	v_add_u32_e32 v210, s51, v132
	s_mov_b32 m0, s27
	s_nop 0
	global_load_lds_dwordx4 v210, s[6:7]
	s_barrier
	s_waitcnt lgkmcnt(0)
	s_setprio 1

	v_mfma_f32_16x16x32_bf16 v[62:65], v[146:149], v[162:165], v[62:65]
	v_mfma_f32_16x16x32_bf16 v[58:61], v[154:157], v[162:165], v[58:61]
	v_mfma_f32_16x16x32_bf16 v[46:49], v[146:149], v[170:173], v[46:49]
	v_mfma_f32_16x16x32_bf16 v[42:45], v[154:157], v[170:173], v[42:45]
	v_mfma_f32_16x16x32_bf16 v[30:33], v[146:149], v[178:181], v[30:33]
	v_mfma_f32_16x16x32_bf16 v[26:29], v[154:157], v[178:181], v[26:29]
	v_mfma_f32_16x16x32_bf16 v[14:17], v[146:149], v[186:189], v[14:17]
	v_mfma_f32_16x16x32_bf16 v[10:13], v[154:157], v[186:189], v[10:13]
	v_mfma_f32_16x16x32_bf16 v[62:65], v[150:153], v[166:169], v[62:65]
	v_mfma_f32_16x16x32_bf16 v[58:61], v[158:161], v[166:169], v[58:61]
	v_mfma_f32_16x16x32_bf16 v[46:49], v[150:153], v[174:177], v[46:49]
	v_mfma_f32_16x16x32_bf16 v[42:45], v[158:161], v[174:177], v[42:45]
	v_mfma_f32_16x16x32_bf16 v[30:33], v[150:153], v[182:185], v[30:33]
	v_mfma_f32_16x16x32_bf16 v[26:29], v[158:161], v[182:185], v[26:29]
	v_mfma_f32_16x16x32_bf16 v[14:17], v[150:153], v[190:193], v[14:17]
	v_mfma_f32_16x16x32_bf16 v[10:13], v[158:161], v[190:193], v[10:13]
	s_setprio 0
	s_barrier
	s_add_i32 s50, s50, 0x20080
	s_add_i32 s51, s40, s19
	v_add_u32_e32 v146, s50, v1
	s_mov_b32 m0, s51
	s_nop 0
	global_load_lds_dwordx4 v146, s[10:11]
	v_add_u32_e32 v146, s50, v138
	s_add_i32 m0, s51, 0x2000
	s_nop 0
	global_load_lds_dwordx4 v146, s[10:11]
	s_waitcnt vmcnt(6)
	s_barrier
	s_setprio 1
	v_mfma_f32_16x16x32_bf16 v[54:57], v[194:197], v[162:165], v[54:57]
	v_mfma_f32_16x16x32_bf16 v[50:53], v[202:205], v[162:165], v[50:53]
	v_mfma_f32_16x16x32_bf16 v[38:41], v[194:197], v[170:173], v[38:41]
	v_mfma_f32_16x16x32_bf16 v[34:37], v[202:205], v[170:173], v[34:37]
	v_mfma_f32_16x16x32_bf16 v[22:25], v[194:197], v[178:181], v[22:25]
	v_mfma_f32_16x16x32_bf16 v[18:21], v[202:205], v[178:181], v[18:21]
	v_mfma_f32_16x16x32_bf16 v[6:9], v[194:197], v[186:189], v[6:9]
	v_mfma_f32_16x16x32_bf16 v[2:5], v[202:205], v[186:189], v[2:5]
	v_mfma_f32_16x16x32_bf16 v[54:57], v[198:201], v[166:169], v[54:57]
	v_mfma_f32_16x16x32_bf16 v[50:53], v[206:209], v[166:169], v[50:53]
	v_mfma_f32_16x16x32_bf16 v[38:41], v[198:201], v[174:177], v[38:41]
	v_mfma_f32_16x16x32_bf16 v[34:37], v[206:209], v[174:177], v[34:37]
	v_mfma_f32_16x16x32_bf16 v[22:25], v[198:201], v[182:185], v[22:25]
	v_mfma_f32_16x16x32_bf16 v[18:21], v[206:209], v[182:185], v[18:21]
	v_mfma_f32_16x16x32_bf16 v[6:9], v[198:201], v[190:193], v[6:9]
	v_mfma_f32_16x16x32_bf16 v[2:5], v[206:209], v[190:193], v[2:5]
	s_setprio 0
	s_add_i32 s49, s49, 2
	s_addk_i32 s47, 0x100
	s_addk_i32 s48, 0x100
	s_cmp_ge_i32 s49, s28
	s_barrier
	s_cbranch_scc0 .LBB0_620
	s_branch .LBB0_615

.LBB0_638:
	s_add_i32 s47, s4, 0x80
	s_cmp_eq_u32 s38, s7
	s_cselect_b32 s49, s2, s47
	s_cselect_b32 s47, s3, s5
	s_add_i32 s50, 0, 0x10000
	v_add_u32_e32 v146, s50, v159
	ds_read_b128 v[138:141], v146
	ds_read_b128 v[142:145], v146 offset:1024
	ds_read_b128 v[166:169], v146 offset:2048
	ds_read_b128 v[170:173], v146 offset:3072
	s_or_b32 s48, s49, 0x80
	v_add_u32_e32 v146, s4, v131
	s_add_i32 m0, s28, 0xc000
	ds_read_b128 v[174:177], v163
	ds_read_b128 v[178:181], v163 offset:1024
	ds_read_b128 v[182:185], v163 offset:2048
	ds_read_b128 v[186:189], v163 offset:3072
	ds_read_b128 v[190:193], v163 offset:4096
	ds_read_b128 v[194:197], v163 offset:5120
	ds_read_b128 v[198:201], v163 offset:6144
	ds_read_b128 v[202:205], v163 offset:7168
	global_load_lds_dwordx4 v146, s[10:11]
	v_add_u32_e32 v146, s4, v133
	s_add_i32 m0, s28, 0xe000
	s_nop 0
	global_load_lds_dwordx4 v146, s[10:11]
	s_waitcnt lgkmcnt(8)
	s_barrier
	s_waitcnt lgkmcnt(0)
	s_setprio 1

	v_mfma_f32_16x16x32_bf16 v[126:129], v[138:141], v[174:177], v[126:129]
	v_mfma_f32_16x16x32_bf16 v[122:125], v[166:169], v[174:177], v[122:125]
	v_mfma_f32_16x16x32_bf16 v[110:113], v[138:141], v[182:185], v[110:113]
	v_mfma_f32_16x16x32_bf16 v[106:109], v[166:169], v[182:185], v[106:109]
	v_mfma_f32_16x16x32_bf16 v[94:97], v[138:141], v[190:193], v[94:97]
	v_mfma_f32_16x16x32_bf16 v[90:93], v[166:169], v[190:193], v[90:93]
	v_mfma_f32_16x16x32_bf16 v[78:81], v[138:141], v[198:201], v[78:81]
	v_mfma_f32_16x16x32_bf16 v[74:77], v[166:169], v[198:201], v[74:77]
	v_mfma_f32_16x16x32_bf16 v[126:129], v[142:145], v[178:181], v[126:129]
	v_mfma_f32_16x16x32_bf16 v[122:125], v[170:173], v[178:181], v[122:125]
	v_mfma_f32_16x16x32_bf16 v[110:113], v[142:145], v[186:189], v[110:113]
	v_mfma_f32_16x16x32_bf16 v[106:109], v[170:173], v[186:189], v[106:109]
	v_mfma_f32_16x16x32_bf16 v[94:97], v[142:145], v[194:197], v[94:97]
	v_mfma_f32_16x16x32_bf16 v[90:93], v[170:173], v[194:197], v[90:93]
	v_mfma_f32_16x16x32_bf16 v[78:81], v[142:145], v[202:205], v[78:81]
	v_mfma_f32_16x16x32_bf16 v[74:77], v[170:173], v[202:205], v[74:77]
	s_setprio 0
	s_barrier
	s_add_i32 s50, s50, s27
	v_add_u32_e32 v146, s47, v1
	s_mov_b32 m0, s50
	ds_read_b128 v[206:209], v164
	ds_read_b128 v[210:213], v164 offset:1024
	ds_read_b128 v[214:217], v164 offset:2048
	ds_read_b128 v[218:221], v164 offset:3072
	global_load_lds_dwordx4 v146, s[14:15]
	v_add_u32_e32 v146, s47, v147
	s_add_i32 m0, s50, 0x2000
	s_nop 0
	global_load_lds_dwordx4 v146, s[14:15]
	s_barrier
	s_waitcnt lgkmcnt(0)
	s_setprio 1

	v_mfma_f32_16x16x32_bf16 v[118:121], v[206:209], v[174:177], v[118:121]
	v_mfma_f32_16x16x32_bf16 v[114:117], v[214:217], v[174:177], v[114:117]
	v_mfma_f32_16x16x32_bf16 v[102:105], v[206:209], v[182:185], v[102:105]
	v_mfma_f32_16x16x32_bf16 v[98:101], v[214:217], v[182:185], v[98:101]
	v_mfma_f32_16x16x32_bf16 v[86:89], v[206:209], v[190:193], v[86:89]
	v_mfma_f32_16x16x32_bf16 v[82:85], v[214:217], v[190:193], v[82:85]
	v_mfma_f32_16x16x32_bf16 v[70:73], v[206:209], v[198:201], v[70:73]
	v_mfma_f32_16x16x32_bf16 v[66:69], v[214:217], v[198:201], v[66:69]
	v_mfma_f32_16x16x32_bf16 v[118:121], v[210:213], v[178:181], v[118:121]
	v_mfma_f32_16x16x32_bf16 v[114:117], v[218:221], v[178:181], v[114:117]
	v_mfma_f32_16x16x32_bf16 v[102:105], v[210:213], v[186:189], v[102:105]
	v_mfma_f32_16x16x32_bf16 v[98:101], v[218:221], v[186:189], v[98:101]
	v_mfma_f32_16x16x32_bf16 v[86:89], v[210:213], v[194:197], v[86:89]
	v_mfma_f32_16x16x32_bf16 v[82:85], v[218:221], v[194:197], v[82:85]
	v_mfma_f32_16x16x32_bf16 v[70:73], v[210:213], v[202:205], v[70:73]
	v_mfma_f32_16x16x32_bf16 v[66:69], v[218:221], v[202:205], v[66:69]
	s_setprio 0
	s_mov_b32 m0, s28
	v_add_u32_e32 v146, s49, v130
	s_barrier
	ds_read_b128 v[174:177], v163 offset:16384
	ds_read_b128 v[178:181], v163 offset:17408
	ds_read_b128 v[182:185], v163 offset:18432
	ds_read_b128 v[186:189], v163 offset:19456
	ds_read_b128 v[190:193], v163 offset:20480
	ds_read_b128 v[194:197], v163 offset:21504
	ds_read_b128 v[198:201], v163 offset:22528
	ds_read_b128 v[202:205], v163 offset:23552
	global_load_lds_dwordx4 v146, s[10:11]
	v_add_u32_e32 v146, s49, v132
	s_mov_b32 m0, s29
	s_nop 0
	global_load_lds_dwordx4 v146, s[10:11]
	s_barrier
	s_waitcnt lgkmcnt(0)
	s_setprio 1

	v_mfma_f32_16x16x32_bf16 v[62:65], v[138:141], v[174:177], v[62:65]
	v_mfma_f32_16x16x32_bf16 v[58:61], v[166:169], v[174:177], v[58:61]
	v_mfma_f32_16x16x32_bf16 v[46:49], v[138:141], v[182:185], v[46:49]
	v_mfma_f32_16x16x32_bf16 v[42:45], v[166:169], v[182:185], v[42:45]
	v_mfma_f32_16x16x32_bf16 v[30:33], v[138:141], v[190:193], v[30:33]
	v_mfma_f32_16x16x32_bf16 v[26:29], v[166:169], v[190:193], v[26:29]
	v_mfma_f32_16x16x32_bf16 v[14:17], v[138:141], v[198:201], v[14:17]
	v_mfma_f32_16x16x32_bf16 v[10:13], v[166:169], v[198:201], v[10:13]
	v_mfma_f32_16x16x32_bf16 v[62:65], v[142:145], v[178:181], v[62:65]
	v_mfma_f32_16x16x32_bf16 v[58:61], v[170:173], v[178:181], v[58:61]
	v_mfma_f32_16x16x32_bf16 v[46:49], v[142:145], v[186:189], v[46:49]
	v_mfma_f32_16x16x32_bf16 v[42:45], v[170:173], v[186:189], v[42:45]
	v_mfma_f32_16x16x32_bf16 v[30:33], v[142:145], v[194:197], v[30:33]
	v_mfma_f32_16x16x32_bf16 v[26:29], v[170:173], v[194:197], v[26:29]
	v_mfma_f32_16x16x32_bf16 v[14:17], v[142:145], v[202:205], v[14:17]
	v_mfma_f32_16x16x32_bf16 v[10:13], v[170:173], v[202:205], v[10:13]
	s_setprio 0
	s_barrier
	s_add_i32 s50, s47, 0x10000
	s_add_i32 s51, s39, s27
	v_add_u32_e32 v138, s50, v1
	s_mov_b32 m0, s51
	s_nop 0
	global_load_lds_dwordx4 v138, s[14:15]
	v_add_u32_e32 v138, s50, v147
	s_add_i32 m0, s51, 0x2000
	s_nop 0
	global_load_lds_dwordx4 v138, s[14:15]
	s_waitcnt vmcnt(6)
	s_barrier
	s_setprio 1
	v_mfma_f32_16x16x32_bf16 v[54:57], v[206:209], v[174:177], v[54:57]
	v_mfma_f32_16x16x32_bf16 v[50:53], v[214:217], v[174:177], v[50:53]
	v_mfma_f32_16x16x32_bf16 v[38:41], v[206:209], v[182:185], v[38:41]
	v_mfma_f32_16x16x32_bf16 v[34:37], v[214:217], v[182:185], v[34:37]
	v_mfma_f32_16x16x32_bf16 v[22:25], v[206:209], v[190:193], v[22:25]
	v_mfma_f32_16x16x32_bf16 v[18:21], v[214:217], v[190:193], v[18:21]
	v_mfma_f32_16x16x32_bf16 v[6:9], v[206:209], v[198:201], v[6:9]
	v_mfma_f32_16x16x32_bf16 v[2:5], v[214:217], v[198:201], v[2:5]
	v_mfma_f32_16x16x32_bf16 v[54:57], v[210:213], v[178:181], v[54:57]
	v_mfma_f32_16x16x32_bf16 v[50:53], v[218:221], v[178:181], v[50:53]
	v_mfma_f32_16x16x32_bf16 v[38:41], v[210:213], v[186:189], v[38:41]
	v_mfma_f32_16x16x32_bf16 v[34:37], v[218:221], v[186:189], v[34:37]
	v_mfma_f32_16x16x32_bf16 v[22:25], v[210:213], v[194:197], v[22:25]
	v_mfma_f32_16x16x32_bf16 v[18:21], v[218:221], v[194:197], v[18:21]
	v_mfma_f32_16x16x32_bf16 v[6:9], v[210:213], v[202:205], v[6:9]
	v_mfma_f32_16x16x32_bf16 v[2:5], v[218:221], v[202:205], v[2:5]
	s_setprio 0
	s_add_i32 s50, 0, 0x18000
	v_add_u32_e32 v146, s50, v159
	s_barrier
	ds_read_b128 v[138:141], v146
	ds_read_b128 v[142:145], v146 offset:1024
	ds_read_b128 v[166:169], v146 offset:2048
	ds_read_b128 v[170:173], v146 offset:3072
	s_mov_b32 m0, s30
	v_add_u32_e32 v146, s49, v131
	ds_read_b128 v[174:177], v163 offset:32768
	ds_read_b128 v[178:181], v163 offset:33792
	ds_read_b128 v[182:185], v163 offset:34816
	ds_read_b128 v[186:189], v163 offset:35840
	ds_read_b128 v[190:193], v163 offset:36864
	ds_read_b128 v[194:197], v163 offset:37888
	ds_read_b128 v[198:201], v163 offset:38912
	ds_read_b128 v[202:205], v163 offset:39936
	global_load_lds_dwordx4 v146, s[10:11]
	v_add_u32_e32 v146, s49, v133
	s_mov_b32 m0, s31
	s_nop 0
	global_load_lds_dwordx4 v146, s[10:11]
	s_waitcnt lgkmcnt(8)
	s_barrier
	s_waitcnt lgkmcnt(0)
	s_setprio 1

	v_mfma_f32_16x16x32_bf16 v[126:129], v[138:141], v[174:177], v[126:129]
	v_mfma_f32_16x16x32_bf16 v[122:125], v[166:169], v[174:177], v[122:125]
	v_mfma_f32_16x16x32_bf16 v[110:113], v[138:141], v[182:185], v[110:113]
	v_mfma_f32_16x16x32_bf16 v[106:109], v[166:169], v[182:185], v[106:109]
	v_mfma_f32_16x16x32_bf16 v[94:97], v[138:141], v[190:193], v[94:97]
	v_mfma_f32_16x16x32_bf16 v[90:93], v[166:169], v[190:193], v[90:93]
	v_mfma_f32_16x16x32_bf16 v[78:81], v[138:141], v[198:201], v[78:81]
	v_mfma_f32_16x16x32_bf16 v[74:77], v[166:169], v[198:201], v[74:77]
	v_mfma_f32_16x16x32_bf16 v[126:129], v[142:145], v[178:181], v[126:129]
	v_mfma_f32_16x16x32_bf16 v[122:125], v[170:173], v[178:181], v[122:125]
	v_mfma_f32_16x16x32_bf16 v[110:113], v[142:145], v[186:189], v[110:113]
	v_mfma_f32_16x16x32_bf16 v[106:109], v[170:173], v[186:189], v[106:109]
	v_mfma_f32_16x16x32_bf16 v[94:97], v[142:145], v[194:197], v[94:97]
	v_mfma_f32_16x16x32_bf16 v[90:93], v[170:173], v[194:197], v[90:93]
	v_mfma_f32_16x16x32_bf16 v[78:81], v[142:145], v[202:205], v[78:81]
	v_mfma_f32_16x16x32_bf16 v[74:77], v[170:173], v[202:205], v[74:77]
	s_setprio 0
	s_barrier
	s_add_i32 s49, 0, 0x1c000
	v_add_u32_e32 v146, s49, v159
	s_or_b32 s51, s47, 0x80
	s_add_i32 s50, s50, s27
	ds_read_b128 v[206:209], v146
	ds_read_b128 v[210:213], v146 offset:1024
	ds_read_b128 v[214:217], v146 offset:2048
	ds_read_b128 v[218:221], v146 offset:3072
	v_add_u32_e32 v146, s51, v1
	s_mov_b32 m0, s50
	s_nop 0
	global_load_lds_dwordx4 v146, s[14:15]
	v_add_u32_e32 v146, s51, v147
	s_add_i32 m0, s50, 0x2000
	s_nop 0
	global_load_lds_dwordx4 v146, s[14:15]
	s_barrier
	s_waitcnt lgkmcnt(0)
	s_setprio 1

	v_mfma_f32_16x16x32_bf16 v[118:121], v[206:209], v[174:177], v[118:121]
	v_mfma_f32_16x16x32_bf16 v[114:117], v[214:217], v[174:177], v[114:117]
	v_mfma_f32_16x16x32_bf16 v[102:105], v[206:209], v[182:185], v[102:105]
	v_mfma_f32_16x16x32_bf16 v[98:101], v[214:217], v[182:185], v[98:101]
	v_mfma_f32_16x16x32_bf16 v[86:89], v[206:209], v[190:193], v[86:89]
	v_mfma_f32_16x16x32_bf16 v[82:85], v[214:217], v[190:193], v[82:85]
	v_mfma_f32_16x16x32_bf16 v[70:73], v[206:209], v[198:201], v[70:73]
	v_mfma_f32_16x16x32_bf16 v[66:69], v[214:217], v[198:201], v[66:69]
	v_mfma_f32_16x16x32_bf16 v[118:121], v[210:213], v[178:181], v[118:121]
	v_mfma_f32_16x16x32_bf16 v[114:117], v[218:221], v[178:181], v[114:117]
	v_mfma_f32_16x16x32_bf16 v[102:105], v[210:213], v[186:189], v[102:105]
	v_mfma_f32_16x16x32_bf16 v[98:101], v[218:221], v[186:189], v[98:101]
	v_mfma_f32_16x16x32_bf16 v[86:89], v[210:213], v[194:197], v[86:89]
	v_mfma_f32_16x16x32_bf16 v[82:85], v[218:221], v[194:197], v[82:85]
	v_mfma_f32_16x16x32_bf16 v[70:73], v[210:213], v[202:205], v[70:73]
	v_mfma_f32_16x16x32_bf16 v[66:69], v[218:221], v[202:205], v[66:69]
	s_setprio 0
	s_mov_b32 m0, s36
	v_add_u32_e32 v146, s48, v130
	s_barrier
	ds_read_b128 v[174:177], v163 offset:49152
	ds_read_b128 v[178:181], v163 offset:50176
	ds_read_b128 v[182:185], v163 offset:51200
	ds_read_b128 v[186:189], v163 offset:52224
	ds_read_b128 v[190:193], v163 offset:53248
	ds_read_b128 v[194:197], v163 offset:54272
	ds_read_b128 v[198:201], v163 offset:55296
	ds_read_b128 v[202:205], v163 offset:56320
	global_load_lds_dwordx4 v146, s[10:11]
	v_add_u32_e32 v146, s48, v132
	s_mov_b32 m0, s37
	s_nop 0
	global_load_lds_dwordx4 v146, s[10:11]
	s_barrier
	s_waitcnt lgkmcnt(0)
	s_setprio 1

	v_mfma_f32_16x16x32_bf16 v[62:65], v[138:141], v[174:177], v[62:65]
	v_mfma_f32_16x16x32_bf16 v[58:61], v[166:169], v[174:177], v[58:61]
	v_mfma_f32_16x16x32_bf16 v[46:49], v[138:141], v[182:185], v[46:49]
	v_mfma_f32_16x16x32_bf16 v[42:45], v[166:169], v[182:185], v[42:45]
	v_mfma_f32_16x16x32_bf16 v[30:33], v[138:141], v[190:193], v[30:33]
	v_mfma_f32_16x16x32_bf16 v[26:29], v[166:169], v[190:193], v[26:29]
	v_mfma_f32_16x16x32_bf16 v[14:17], v[138:141], v[198:201], v[14:17]
	v_mfma_f32_16x16x32_bf16 v[10:13], v[166:169], v[198:201], v[10:13]
	v_mfma_f32_16x16x32_bf16 v[62:65], v[142:145], v[178:181], v[62:65]
	v_mfma_f32_16x16x32_bf16 v[58:61], v[170:173], v[178:181], v[58:61]
	v_mfma_f32_16x16x32_bf16 v[46:49], v[142:145], v[186:189], v[46:49]
	v_mfma_f32_16x16x32_bf16 v[42:45], v[170:173], v[186:189], v[42:45]
	v_mfma_f32_16x16x32_bf16 v[30:33], v[142:145], v[194:197], v[30:33]
	v_mfma_f32_16x16x32_bf16 v[26:29], v[170:173], v[194:197], v[26:29]
	v_mfma_f32_16x16x32_bf16 v[14:17], v[142:145], v[202:205], v[14:17]
	v_mfma_f32_16x16x32_bf16 v[10:13], v[170:173], v[202:205], v[10:13]
	s_setprio 0
	s_barrier
	s_add_i32 s47, s47, 0x10080
	s_add_i32 s48, s49, s27
	v_add_u32_e32 v138, s47, v1
	s_mov_b32 m0, s48
	s_nop 0
	global_load_lds_dwordx4 v138, s[14:15]
	v_add_u32_e32 v138, s47, v147
	s_add_i32 m0, s48, 0x2000
	s_nop 0
	global_load_lds_dwordx4 v138, s[14:15]
	s_waitcnt vmcnt(6)
	s_barrier
	s_setprio 1
	v_mfma_f32_16x16x32_bf16 v[54:57], v[206:209], v[174:177], v[54:57]
	v_mfma_f32_16x16x32_bf16 v[50:53], v[214:217], v[174:177], v[50:53]
	v_mfma_f32_16x16x32_bf16 v[38:41], v[206:209], v[182:185], v[38:41]
	v_mfma_f32_16x16x32_bf16 v[34:37], v[214:217], v[182:185], v[34:37]
	v_mfma_f32_16x16x32_bf16 v[22:25], v[206:209], v[190:193], v[22:25]
	v_mfma_f32_16x16x32_bf16 v[18:21], v[214:217], v[190:193], v[18:21]
	v_mfma_f32_16x16x32_bf16 v[6:9], v[206:209], v[198:201], v[6:9]
	v_mfma_f32_16x16x32_bf16 v[2:5], v[214:217], v[198:201], v[2:5]
	v_mfma_f32_16x16x32_bf16 v[54:57], v[210:213], v[178:181], v[54:57]
	v_mfma_f32_16x16x32_bf16 v[50:53], v[218:221], v[178:181], v[50:53]
	v_mfma_f32_16x16x32_bf16 v[38:41], v[210:213], v[186:189], v[38:41]
	v_mfma_f32_16x16x32_bf16 v[34:37], v[218:221], v[186:189], v[34:37]
	v_mfma_f32_16x16x32_bf16 v[22:25], v[210:213], v[194:197], v[22:25]
	v_mfma_f32_16x16x32_bf16 v[18:21], v[218:221], v[194:197], v[18:21]
	v_mfma_f32_16x16x32_bf16 v[6:9], v[210:213], v[202:205], v[6:9]
	v_mfma_f32_16x16x32_bf16 v[2:5], v[218:221], v[202:205], v[2:5]
	s_setprio 0
	s_add_i32 s7, s7, 2
	s_addk_i32 s4, 0x100
	s_addk_i32 s5, 0x100
	s_cmp_ge_i32 s7, s34
	s_barrier
	s_cbranch_scc0 .LBB0_638
	s_branch .LBB0_629

.LBB0_1154:
	ds_read_b128 v[146:149], v141
	ds_read_b128 v[150:153], v141 offset:1024
	ds_read_b128 v[154:157], v141 offset:2048
	ds_read_b128 v[158:161], v141 offset:3072
	s_add_i32 s44, s41, 0x80
	s_cmp_eq_u32 s24, s43
	s_cselect_b32 s46, s10, s44
	s_cselect_b32 s44, s11, s42
	s_or_b32 s45, s46, 0x80
	s_mov_b32 m0, s25
	v_add_u32_e32 v194, s41, v137
	ds_read_b128 v[162:165], v142
	ds_read_b128 v[166:169], v142 offset:1024
	ds_read_b128 v[170:173], v142 offset:2048
	ds_read_b128 v[174:177], v142 offset:3072
	ds_read_b128 v[178:181], v142 offset:4096
	ds_read_b128 v[182:185], v142 offset:5120
	ds_read_b128 v[186:189], v142 offset:6144
	ds_read_b128 v[190:193], v142 offset:7168
	global_load_lds_dwordx4 v194, s[4:5]
	v_add_u32_e32 v194, s41, v138
	s_mov_b32 m0, s26
	s_nop 0
	global_load_lds_dwordx4 v194, s[4:5]
	s_waitcnt lgkmcnt(8)
	s_barrier
	s_waitcnt lgkmcnt(0)
	s_setprio 1

	v_mfma_f32_16x16x32_bf16 v[122:125], v[146:149], v[162:165], v[122:125]
	v_mfma_f32_16x16x32_bf16 v[126:129], v[154:157], v[162:165], v[126:129]
	v_mfma_f32_16x16x32_bf16 v[110:113], v[146:149], v[170:173], v[110:113]
	v_mfma_f32_16x16x32_bf16 v[106:109], v[154:157], v[170:173], v[106:109]
	v_mfma_f32_16x16x32_bf16 v[94:97], v[146:149], v[178:181], v[94:97]
	v_mfma_f32_16x16x32_bf16 v[90:93], v[154:157], v[178:181], v[90:93]
	v_mfma_f32_16x16x32_bf16 v[78:81], v[146:149], v[186:189], v[78:81]
	v_mfma_f32_16x16x32_bf16 v[74:77], v[154:157], v[186:189], v[74:77]
	v_mfma_f32_16x16x32_bf16 v[122:125], v[150:153], v[166:169], v[122:125]
	v_mfma_f32_16x16x32_bf16 v[126:129], v[158:161], v[166:169], v[126:129]
	v_mfma_f32_16x16x32_bf16 v[110:113], v[150:153], v[174:177], v[110:113]
	v_mfma_f32_16x16x32_bf16 v[106:109], v[158:161], v[174:177], v[106:109]
	v_mfma_f32_16x16x32_bf16 v[94:97], v[150:153], v[182:185], v[94:97]
	v_mfma_f32_16x16x32_bf16 v[90:93], v[158:161], v[182:185], v[90:93]
	v_mfma_f32_16x16x32_bf16 v[78:81], v[150:153], v[190:193], v[78:81]
	v_mfma_f32_16x16x32_bf16 v[74:77], v[158:161], v[190:193], v[74:77]
	s_setprio 0
	s_barrier
	s_mov_b32 m0, s28
	v_add_u32_e32 v210, s44, v1
	ds_read_b128 v[194:197], v143
	ds_read_b128 v[198:201], v143 offset:1024
	ds_read_b128 v[202:205], v143 offset:2048
	ds_read_b128 v[206:209], v143 offset:3072
	global_load_lds_dwordx4 v210, s[6:7]
	v_add_u32_e32 v210, s44, v134
	s_mov_b32 m0, s29
	s_nop 0
	global_load_lds_dwordx4 v210, s[6:7]
	s_barrier
	s_waitcnt lgkmcnt(0)
	s_setprio 1

	v_mfma_f32_16x16x32_bf16 v[118:121], v[194:197], v[162:165], v[118:121]
	v_mfma_f32_16x16x32_bf16 v[114:117], v[202:205], v[162:165], v[114:117]
	v_mfma_f32_16x16x32_bf16 v[102:105], v[194:197], v[170:173], v[102:105]
	v_mfma_f32_16x16x32_bf16 v[98:101], v[202:205], v[170:173], v[98:101]
	v_mfma_f32_16x16x32_bf16 v[86:89], v[194:197], v[178:181], v[86:89]
	v_mfma_f32_16x16x32_bf16 v[82:85], v[202:205], v[178:181], v[82:85]
	v_mfma_f32_16x16x32_bf16 v[70:73], v[194:197], v[186:189], v[70:73]
	v_mfma_f32_16x16x32_bf16 v[66:69], v[202:205], v[186:189], v[66:69]
	v_mfma_f32_16x16x32_bf16 v[118:121], v[198:201], v[166:169], v[118:121]
	v_mfma_f32_16x16x32_bf16 v[114:117], v[206:209], v[166:169], v[114:117]
	v_mfma_f32_16x16x32_bf16 v[102:105], v[198:201], v[174:177], v[102:105]
	v_mfma_f32_16x16x32_bf16 v[98:101], v[206:209], v[174:177], v[98:101]
	v_mfma_f32_16x16x32_bf16 v[86:89], v[198:201], v[182:185], v[86:89]
	v_mfma_f32_16x16x32_bf16 v[82:85], v[206:209], v[182:185], v[82:85]
	v_mfma_f32_16x16x32_bf16 v[70:73], v[198:201], v[190:193], v[70:73]
	v_mfma_f32_16x16x32_bf16 v[66:69], v[206:209], v[190:193], v[66:69]
	s_setprio 0
	s_mov_b32 m0, s15
	v_add_u32_e32 v210, s46, v135
	s_barrier
	ds_read_b128 v[162:165], v142 offset:16384
	ds_read_b128 v[166:169], v142 offset:17408
	ds_read_b128 v[170:173], v142 offset:18432
	ds_read_b128 v[174:177], v142 offset:19456
	ds_read_b128 v[178:181], v142 offset:20480
	ds_read_b128 v[182:185], v142 offset:21504
	ds_read_b128 v[186:189], v142 offset:22528
	ds_read_b128 v[190:193], v142 offset:23552
	global_load_lds_dwordx4 v210, s[4:5]
	v_add_u32_e32 v210, s46, v136
	s_mov_b32 m0, s16
	s_nop 0
	global_load_lds_dwordx4 v210, s[4:5]
	s_barrier
	s_waitcnt lgkmcnt(0)
	s_setprio 1

	v_mfma_f32_16x16x32_bf16 v[62:65], v[146:149], v[162:165], v[62:65]
	v_mfma_f32_16x16x32_bf16 v[58:61], v[154:157], v[162:165], v[58:61]
	v_mfma_f32_16x16x32_bf16 v[46:49], v[146:149], v[170:173], v[46:49]
	v_mfma_f32_16x16x32_bf16 v[42:45], v[154:157], v[170:173], v[42:45]
	v_mfma_f32_16x16x32_bf16 v[30:33], v[146:149], v[178:181], v[30:33]
	v_mfma_f32_16x16x32_bf16 v[26:29], v[154:157], v[178:181], v[26:29]
	v_mfma_f32_16x16x32_bf16 v[14:17], v[146:149], v[186:189], v[14:17]
	v_mfma_f32_16x16x32_bf16 v[10:13], v[154:157], v[186:189], v[10:13]
	v_mfma_f32_16x16x32_bf16 v[62:65], v[150:153], v[166:169], v[62:65]
	v_mfma_f32_16x16x32_bf16 v[58:61], v[158:161], v[166:169], v[58:61]
	v_mfma_f32_16x16x32_bf16 v[46:49], v[150:153], v[174:177], v[46:49]
	v_mfma_f32_16x16x32_bf16 v[42:45], v[158:161], v[174:177], v[42:45]
	v_mfma_f32_16x16x32_bf16 v[30:33], v[150:153], v[182:185], v[30:33]
	v_mfma_f32_16x16x32_bf16 v[26:29], v[158:161], v[182:185], v[26:29]
	v_mfma_f32_16x16x32_bf16 v[14:17], v[150:153], v[190:193], v[14:17]
	v_mfma_f32_16x16x32_bf16 v[10:13], v[158:161], v[190:193], v[10:13]
	s_setprio 0
	s_barrier
	s_add_i32 s47, s44, 0x18000
	s_mov_b32 m0, s30
	v_add_u32_e32 v146, s47, v1
	global_load_lds_dwordx4 v146, s[6:7]
	v_add_u32_e32 v146, s47, v134
	s_mov_b32 m0, s31
	s_nop 0
	global_load_lds_dwordx4 v146, s[6:7]
	s_waitcnt vmcnt(6)
	s_barrier
	s_setprio 1
	v_mfma_f32_16x16x32_bf16 v[54:57], v[194:197], v[162:165], v[54:57]
	v_mfma_f32_16x16x32_bf16 v[50:53], v[202:205], v[162:165], v[50:53]
	v_mfma_f32_16x16x32_bf16 v[38:41], v[194:197], v[170:173], v[38:41]
	v_mfma_f32_16x16x32_bf16 v[34:37], v[202:205], v[170:173], v[34:37]
	v_mfma_f32_16x16x32_bf16 v[22:25], v[194:197], v[178:181], v[22:25]
	v_mfma_f32_16x16x32_bf16 v[18:21], v[202:205], v[178:181], v[18:21]
	v_mfma_f32_16x16x32_bf16 v[6:9], v[194:197], v[186:189], v[6:9]
	v_mfma_f32_16x16x32_bf16 v[2:5], v[202:205], v[186:189], v[2:5]
	v_mfma_f32_16x16x32_bf16 v[54:57], v[198:201], v[166:169], v[54:57]
	v_mfma_f32_16x16x32_bf16 v[50:53], v[206:209], v[166:169], v[50:53]
	v_mfma_f32_16x16x32_bf16 v[38:41], v[198:201], v[174:177], v[38:41]
	v_mfma_f32_16x16x32_bf16 v[34:37], v[206:209], v[174:177], v[34:37]
	v_mfma_f32_16x16x32_bf16 v[22:25], v[198:201], v[182:185], v[22:25]
	v_mfma_f32_16x16x32_bf16 v[18:21], v[206:209], v[182:185], v[18:21]
	v_mfma_f32_16x16x32_bf16 v[6:9], v[198:201], v[190:193], v[6:9]
	v_mfma_f32_16x16x32_bf16 v[2:5], v[206:209], v[190:193], v[2:5]
	s_setprio 0
	s_barrier
	ds_read_b128 v[146:149], v144
	ds_read_b128 v[150:153], v144 offset:1024
	ds_read_b128 v[154:157], v144 offset:2048
	ds_read_b128 v[158:161], v144 offset:3072
	s_mov_b32 m0, s17
	v_add_u32_e32 v194, s46, v137
	ds_read_b128 v[162:165], v142 offset:32768
	ds_read_b128 v[166:169], v142 offset:33792
	ds_read_b128 v[170:173], v142 offset:34816
	ds_read_b128 v[174:177], v142 offset:35840
	ds_read_b128 v[178:181], v142 offset:36864
	ds_read_b128 v[182:185], v142 offset:37888
	ds_read_b128 v[186:189], v142 offset:38912
	ds_read_b128 v[190:193], v142 offset:39936
	global_load_lds_dwordx4 v194, s[4:5]
	v_add_u32_e32 v194, s46, v138
	s_mov_b32 m0, s18
	s_nop 0
	global_load_lds_dwordx4 v194, s[4:5]
	s_waitcnt lgkmcnt(8)
	s_barrier
	s_waitcnt lgkmcnt(0)
	s_setprio 1

	v_mfma_f32_16x16x32_bf16 v[122:125], v[146:149], v[162:165], v[122:125]
	v_mfma_f32_16x16x32_bf16 v[126:129], v[154:157], v[162:165], v[126:129]
	v_mfma_f32_16x16x32_bf16 v[110:113], v[146:149], v[170:173], v[110:113]
	v_mfma_f32_16x16x32_bf16 v[106:109], v[154:157], v[170:173], v[106:109]
	v_mfma_f32_16x16x32_bf16 v[94:97], v[146:149], v[178:181], v[94:97]
	v_mfma_f32_16x16x32_bf16 v[90:93], v[154:157], v[178:181], v[90:93]
	v_mfma_f32_16x16x32_bf16 v[78:81], v[146:149], v[186:189], v[78:81]
	v_mfma_f32_16x16x32_bf16 v[74:77], v[154:157], v[186:189], v[74:77]
	v_mfma_f32_16x16x32_bf16 v[122:125], v[150:153], v[166:169], v[122:125]
	v_mfma_f32_16x16x32_bf16 v[126:129], v[158:161], v[166:169], v[126:129]
	v_mfma_f32_16x16x32_bf16 v[110:113], v[150:153], v[174:177], v[110:113]
	v_mfma_f32_16x16x32_bf16 v[106:109], v[158:161], v[174:177], v[106:109]
	v_mfma_f32_16x16x32_bf16 v[94:97], v[150:153], v[182:185], v[94:97]
	v_mfma_f32_16x16x32_bf16 v[90:93], v[158:161], v[182:185], v[90:93]
	v_mfma_f32_16x16x32_bf16 v[78:81], v[150:153], v[190:193], v[78:81]
	v_mfma_f32_16x16x32_bf16 v[74:77], v[158:161], v[190:193], v[74:77]
	s_setprio 0
	s_barrier
	s_or_b32 s46, s44, 0x80
	s_add_i32 s47, s33, s13
	v_add_u32_e32 v210, s46, v1
	s_mov_b32 m0, s47
	ds_read_b128 v[194:197], v145
	ds_read_b128 v[198:201], v145 offset:1024
	ds_read_b128 v[202:205], v145 offset:2048
	ds_read_b128 v[206:209], v145 offset:3072
	global_load_lds_dwordx4 v210, s[6:7]
	v_add_u32_e32 v210, s46, v134
	s_add_i32 m0, s47, 0x2000
	s_nop 0
	global_load_lds_dwordx4 v210, s[6:7]
	s_barrier
	s_waitcnt lgkmcnt(0)
	s_setprio 1

	v_mfma_f32_16x16x32_bf16 v[118:121], v[194:197], v[162:165], v[118:121]
	v_mfma_f32_16x16x32_bf16 v[114:117], v[202:205], v[162:165], v[114:117]
	v_mfma_f32_16x16x32_bf16 v[102:105], v[194:197], v[170:173], v[102:105]
	v_mfma_f32_16x16x32_bf16 v[98:101], v[202:205], v[170:173], v[98:101]
	v_mfma_f32_16x16x32_bf16 v[86:89], v[194:197], v[178:181], v[86:89]
	v_mfma_f32_16x16x32_bf16 v[82:85], v[202:205], v[178:181], v[82:85]
	v_mfma_f32_16x16x32_bf16 v[70:73], v[194:197], v[186:189], v[70:73]
	v_mfma_f32_16x16x32_bf16 v[66:69], v[202:205], v[186:189], v[66:69]
	v_mfma_f32_16x16x32_bf16 v[118:121], v[198:201], v[166:169], v[118:121]
	v_mfma_f32_16x16x32_bf16 v[114:117], v[206:209], v[166:169], v[114:117]
	v_mfma_f32_16x16x32_bf16 v[102:105], v[198:201], v[174:177], v[102:105]
	v_mfma_f32_16x16x32_bf16 v[98:101], v[206:209], v[174:177], v[98:101]
	v_mfma_f32_16x16x32_bf16 v[86:89], v[198:201], v[182:185], v[86:89]
	v_mfma_f32_16x16x32_bf16 v[82:85], v[206:209], v[182:185], v[82:85]
	v_mfma_f32_16x16x32_bf16 v[70:73], v[198:201], v[190:193], v[70:73]
	v_mfma_f32_16x16x32_bf16 v[66:69], v[206:209], v[190:193], v[66:69]
	s_setprio 0
	s_mov_b32 m0, s20
	v_add_u32_e32 v210, s45, v135
	s_barrier
	ds_read_b128 v[162:165], v142 offset:49152
	ds_read_b128 v[166:169], v142 offset:50176
	ds_read_b128 v[170:173], v142 offset:51200
	ds_read_b128 v[174:177], v142 offset:52224
	ds_read_b128 v[178:181], v142 offset:53248
	ds_read_b128 v[182:185], v142 offset:54272
	ds_read_b128 v[186:189], v142 offset:55296
	ds_read_b128 v[190:193], v142 offset:56320
	global_load_lds_dwordx4 v210, s[4:5]
	v_add_u32_e32 v210, s45, v136
	s_mov_b32 m0, s21
	s_nop 0
	global_load_lds_dwordx4 v210, s[4:5]
	s_barrier
	s_waitcnt lgkmcnt(0)
	s_setprio 1

	v_mfma_f32_16x16x32_bf16 v[62:65], v[146:149], v[162:165], v[62:65]
	v_mfma_f32_16x16x32_bf16 v[58:61], v[154:157], v[162:165], v[58:61]
	v_mfma_f32_16x16x32_bf16 v[46:49], v[146:149], v[170:173], v[46:49]
	v_mfma_f32_16x16x32_bf16 v[42:45], v[154:157], v[170:173], v[42:45]
	v_mfma_f32_16x16x32_bf16 v[30:33], v[146:149], v[178:181], v[30:33]
	v_mfma_f32_16x16x32_bf16 v[26:29], v[154:157], v[178:181], v[26:29]
	v_mfma_f32_16x16x32_bf16 v[14:17], v[146:149], v[186:189], v[14:17]
	v_mfma_f32_16x16x32_bf16 v[10:13], v[154:157], v[186:189], v[10:13]
	v_mfma_f32_16x16x32_bf16 v[62:65], v[150:153], v[166:169], v[62:65]
	v_mfma_f32_16x16x32_bf16 v[58:61], v[158:161], v[166:169], v[58:61]
	v_mfma_f32_16x16x32_bf16 v[46:49], v[150:153], v[174:177], v[46:49]
	v_mfma_f32_16x16x32_bf16 v[42:45], v[158:161], v[174:177], v[42:45]
	v_mfma_f32_16x16x32_bf16 v[30:33], v[150:153], v[182:185], v[30:33]
	v_mfma_f32_16x16x32_bf16 v[26:29], v[158:161], v[182:185], v[26:29]
	v_mfma_f32_16x16x32_bf16 v[14:17], v[150:153], v[190:193], v[14:17]
	v_mfma_f32_16x16x32_bf16 v[10:13], v[158:161], v[190:193], v[10:13]
	s_setprio 0
	s_barrier
	s_add_i32 s44, s44, 0x18080
	s_add_i32 s45, s34, s13
	v_add_u32_e32 v146, s44, v1
	s_mov_b32 m0, s45
	s_nop 0
	global_load_lds_dwordx4 v146, s[6:7]
	v_add_u32_e32 v146, s44, v134
	s_add_i32 m0, s45, 0x2000
	s_nop 0
	global_load_lds_dwordx4 v146, s[6:7]
	s_waitcnt vmcnt(6)
	s_barrier
	s_setprio 1
	v_mfma_f32_16x16x32_bf16 v[54:57], v[194:197], v[162:165], v[54:57]
	v_mfma_f32_16x16x32_bf16 v[50:53], v[202:205], v[162:165], v[50:53]
	v_mfma_f32_16x16x32_bf16 v[38:41], v[194:197], v[170:173], v[38:41]
	v_mfma_f32_16x16x32_bf16 v[34:37], v[202:205], v[170:173], v[34:37]
	v_mfma_f32_16x16x32_bf16 v[22:25], v[194:197], v[178:181], v[22:25]
	v_mfma_f32_16x16x32_bf16 v[18:21], v[202:205], v[178:181], v[18:21]
	v_mfma_f32_16x16x32_bf16 v[6:9], v[194:197], v[186:189], v[6:9]
	v_mfma_f32_16x16x32_bf16 v[2:5], v[202:205], v[186:189], v[2:5]
	v_mfma_f32_16x16x32_bf16 v[54:57], v[198:201], v[166:169], v[54:57]
	v_mfma_f32_16x16x32_bf16 v[50:53], v[206:209], v[166:169], v[50:53]
	v_mfma_f32_16x16x32_bf16 v[38:41], v[198:201], v[174:177], v[38:41]
	v_mfma_f32_16x16x32_bf16 v[34:37], v[206:209], v[174:177], v[34:37]
	v_mfma_f32_16x16x32_bf16 v[22:25], v[198:201], v[182:185], v[22:25]
	v_mfma_f32_16x16x32_bf16 v[18:21], v[206:209], v[182:185], v[18:21]
	v_mfma_f32_16x16x32_bf16 v[6:9], v[198:201], v[190:193], v[6:9]
	v_mfma_f32_16x16x32_bf16 v[2:5], v[206:209], v[190:193], v[2:5]
	s_setprio 0
	s_add_i32 s43, s43, 2
	s_addk_i32 s41, 0x100
	s_addk_i32 s42, 0x100
	s_cmp_ge_i32 s43, s22
	s_barrier
	s_cbranch_scc0 .LBB0_1154
	s_branch .LBB0_1149

.LBB0_1522:
	ds_read_b128 v[130:133], v162
	ds_read_b128 v[134:137], v162 offset:1024
	ds_read_b128 v[146:149], v162 offset:2048
	ds_read_b128 v[150:153], v162 offset:3072
	s_add_i32 s55, s52, 0x80
	s_cmp_eq_u32 s42, s54
	s_cselect_b32 s57, s4, s55
	s_cselect_b32 s55, s5, s53
	s_or_b32 s56, s57, 0x80
	s_mov_b32 m0, s44
	v_add_u32_e32 v66, s52, v157
	ds_read_b128 v[168:171], v163
	ds_read_b128 v[172:175], v163 offset:1024
	ds_read_b128 v[176:179], v163 offset:2048
	ds_read_b128 v[180:183], v163 offset:3072
	ds_read_b128 v[184:187], v163 offset:4096
	ds_read_b128 v[188:191], v163 offset:5120
	ds_read_b128 v[192:195], v163 offset:6144
	ds_read_b128 v[196:199], v163 offset:7168
	global_load_lds_dwordx4 v66, s[12:13]
	v_add_u32_e32 v66, s52, v158
	s_mov_b32 m0, s45
	s_nop 0
	global_load_lds_dwordx4 v66, s[12:13]
	s_waitcnt lgkmcnt(8)
	s_barrier
	s_waitcnt lgkmcnt(0)
	s_setprio 1

	v_mfma_scale_f32_16x16x128_f8f6f4 v[118:121], v[130:137], v[168:175], v[118:121], v165, v164 op_sel_hi:[0,0,0]
	v_mfma_scale_f32_16x16x128_f8f6f4 v[122:125], v[146:153], v[168:175], v[122:125], v165, v164 op_sel_hi:[0,0,0]
	v_mfma_scale_f32_16x16x128_f8f6f4 v[138:141], v[130:137], v[176:183], v[110:113], v165, v164 op_sel_hi:[0,0,0]
	v_mfma_scale_f32_16x16x128_f8f6f4 v[200:203], v[146:153], v[176:183], v[102:105], v165, v164 op_sel_hi:[0,0,0]
	v_mfma_scale_f32_16x16x128_f8f6f4 v[204:207], v[130:137], v[184:191], v[94:97], v165, v164 op_sel_hi:[0,0,0]
	v_mfma_scale_f32_16x16x128_f8f6f4 v[208:211], v[146:153], v[184:191], v[90:93], v165, v164 op_sel_hi:[0,0,0]
	v_mfma_scale_f32_16x16x128_f8f6f4 v[212:215], v[130:137], v[192:199], v[78:81], v165, v164 op_sel_hi:[0,0,0]
	v_mfma_scale_f32_16x16x128_f8f6f4 v[216:219], v[146:153], v[192:199], v[74:77], v165, v164 op_sel_hi:[0,0,0]
	s_setprio 0
	s_barrier
	s_add_i32 s58, s43, s31
	v_add_u32_e32 v66, s55, v1
	s_mov_b32 m0, s58
	s_nop 1
	ds_read_b128 v[74:77], v166
	ds_read_b128 v[78:81], v166 offset:1024
	ds_read_b128 v[90:93], v166 offset:2048
	ds_read_b128 v[94:97], v166 offset:3072
	global_load_lds_dwordx4 v66, s[10:11]
	v_add_u32_e32 v66, s55, v154
	s_add_i32 m0, s58, 0x2000
	s_nop 0
	global_load_lds_dwordx4 v66, s[10:11]
	s_barrier
	s_waitcnt lgkmcnt(0)
	s_setprio 1

	v_mfma_scale_f32_16x16x128_f8f6f4 v[126:129], v[74:81], v[168:175], v[126:129], v165, v164 op_sel_hi:[0,0,0]
	v_mfma_scale_f32_16x16x128_f8f6f4 v[114:117], v[90:97], v[168:175], v[114:117], v165, v164 op_sel_hi:[0,0,0]
	v_mfma_scale_f32_16x16x128_f8f6f4 v[168:171], v[74:81], v[176:183], v[106:109], v165, v164 op_sel_hi:[0,0,0]
	v_mfma_scale_f32_16x16x128_f8f6f4 v[172:175], v[90:97], v[176:183], v[98:101], v165, v164 op_sel_hi:[0,0,0]
	v_mfma_scale_f32_16x16x128_f8f6f4 v[176:179], v[74:81], v[184:191], v[86:89], v165, v164 op_sel_hi:[0,0,0]
	v_mfma_scale_f32_16x16x128_f8f6f4 v[180:183], v[90:97], v[184:191], v[82:85], v165, v164 op_sel_hi:[0,0,0]
	v_mfma_scale_f32_16x16x128_f8f6f4 v[184:187], v[74:81], v[192:199], v[70:73], v165, v164 op_sel_hi:[0,0,0]
	v_mfma_scale_f32_16x16x128_f8f6f4 v[188:191], v[90:97], v[192:199], v[10:13], v165, v164 op_sel_hi:[0,0,0]
	s_setprio 0
	s_mov_b32 m0, s33
	s_nop 4
	v_add_u32_e32 v10, s57, v155
	s_barrier
	ds_read_b128 v[66:69], v163 offset:16384
	ds_read_b128 v[70:73], v163 offset:17408
	ds_read_b128 v[82:85], v163 offset:18432
	ds_read_b128 v[86:89], v163 offset:19456
	ds_read_b128 v[98:101], v163 offset:20480
	ds_read_b128 v[102:105], v163 offset:21504
	ds_read_b128 v[106:109], v163 offset:22528
	ds_read_b128 v[110:113], v163 offset:23552
	global_load_lds_dwordx4 v10, s[12:13]
	v_add_u32_e32 v10, s57, v156
	s_mov_b32 m0, s34
	s_nop 0
	global_load_lds_dwordx4 v10, s[12:13]
	s_barrier
	s_waitcnt lgkmcnt(0)
	s_setprio 1

	v_mfma_scale_f32_16x16x128_f8f6f4 v[62:65], v[130:137], v[66:73], v[62:65], v165, v164 op_sel_hi:[0,0,0]
	v_mfma_scale_f32_16x16x128_f8f6f4 v[58:61], v[146:153], v[66:73], v[58:61], v165, v164 op_sel_hi:[0,0,0]
	v_mfma_scale_f32_16x16x128_f8f6f4 v[232:235], v[146:153], v[106:113], v[232:235], v165, v164 op_sel_hi:[0,0,0]
	v_mfma_scale_f32_16x16x128_f8f6f4 v[192:195], v[130:137], v[82:89], v[46:49], v165, v164 op_sel_hi:[0,0,0]
	v_mfma_scale_f32_16x16x128_f8f6f4 v[196:199], v[146:153], v[82:89], v[42:45], v165, v164 op_sel_hi:[0,0,0]
	v_mfma_scale_f32_16x16x128_f8f6f4 v[220:223], v[130:137], v[98:105], v[30:33], v165, v164 op_sel_hi:[0,0,0]
	v_mfma_scale_f32_16x16x128_f8f6f4 v[224:227], v[146:153], v[98:105], v[26:29], v165, v164 op_sel_hi:[0,0,0]
	v_mfma_scale_f32_16x16x128_f8f6f4 v[228:231], v[130:137], v[106:113], v[14:17], v165, v164 op_sel_hi:[0,0,0]
	s_setprio 0
	s_barrier
	s_add_i32 s58, s55, 0x40000
	s_add_i32 s59, s46, s31
	v_add_u32_e32 v10, s58, v1
	s_mov_b32 m0, s59
	s_nop 0
	global_load_lds_dwordx4 v10, s[10:11]
	v_add_u32_e32 v10, s58, v154
	s_add_i32 m0, s59, 0x2000
	s_nop 0
	global_load_lds_dwordx4 v10, s[10:11]
	s_waitcnt vmcnt(6)
	s_barrier
	s_setprio 1
	v_mfma_scale_f32_16x16x128_f8f6f4 v[54:57], v[74:81], v[66:73], v[54:57], v165, v164 op_sel_hi:[0,0,0]
	v_mfma_scale_f32_16x16x128_f8f6f4 v[50:53], v[90:97], v[66:73], v[50:53], v165, v164 op_sel_hi:[0,0,0]
	v_mfma_scale_f32_16x16x128_f8f6f4 v[236:239], v[74:81], v[82:89], v[38:41], v165, v164 op_sel_hi:[0,0,0]
	v_mfma_scale_f32_16x16x128_f8f6f4 v[240:243], v[90:97], v[82:89], v[34:37], v165, v164 op_sel_hi:[0,0,0]
	v_mfma_scale_f32_16x16x128_f8f6f4 v[244:247], v[74:81], v[98:105], v[22:25], v165, v164 op_sel_hi:[0,0,0]
	v_mfma_scale_f32_16x16x128_f8f6f4 v[248:251], v[90:97], v[98:105], v[18:21], v165, v164 op_sel_hi:[0,0,0]
	v_mfma_scale_f32_16x16x128_f8f6f4 v[142:145], v[74:81], v[106:113], v[6:9], v165, v164 op_sel_hi:[0,0,0]
	v_mfma_scale_f32_16x16x128_f8f6f4 v[66:69], v[90:97], v[106:113], v[2:5], v165, v164 op_sel_hi:[0,0,0]
	s_setprio 0
	s_add_i32 s58, 0, 0x18000
	v_add_u32_e32 v10, s58, v161
	s_barrier
	s_nop 2
	ds_read_b128 v[2:5], v10
	ds_read_b128 v[6:9], v10 offset:1024
	ds_read_b128 v[18:21], v10 offset:2048
	ds_read_b128 v[22:25], v10 offset:3072
	s_mov_b32 m0, s35
	v_add_u32_e32 v70, s57, v157
	ds_read_b128 v[10:13], v163 offset:32768
	ds_read_b128 v[14:17], v163 offset:33792
	ds_read_b128 v[26:29], v163 offset:34816
	ds_read_b128 v[30:33], v163 offset:35840
	ds_read_b128 v[34:37], v163 offset:36864
	ds_read_b128 v[38:41], v163 offset:37888
	ds_read_b128 v[42:45], v163 offset:38912
	ds_read_b128 v[46:49], v163 offset:39936
	global_load_lds_dwordx4 v70, s[12:13]
	v_add_u32_e32 v70, s57, v158
	s_mov_b32 m0, s36
	s_nop 0
	global_load_lds_dwordx4 v70, s[12:13]
	s_waitcnt lgkmcnt(8)
	s_barrier
	s_waitcnt lgkmcnt(0)
	s_setprio 1

	v_mfma_scale_f32_16x16x128_f8f6f4 v[118:121], v[2:9], v[10:17], v[118:121], v165, v164 op_sel_hi:[0,0,0]
	v_mfma_scale_f32_16x16x128_f8f6f4 v[122:125], v[18:25], v[10:17], v[122:125], v165, v164 op_sel_hi:[0,0,0]
	v_mfma_scale_f32_16x16x128_f8f6f4 v[110:113], v[2:9], v[26:33], v[138:141], v165, v164 op_sel_hi:[0,0,0]
	v_mfma_scale_f32_16x16x128_f8f6f4 v[102:105], v[18:25], v[26:33], v[200:203], v165, v164 op_sel_hi:[0,0,0]
	v_mfma_scale_f32_16x16x128_f8f6f4 v[94:97], v[2:9], v[34:41], v[204:207], v165, v164 op_sel_hi:[0,0,0]
	v_mfma_scale_f32_16x16x128_f8f6f4 v[90:93], v[18:25], v[34:41], v[208:211], v165, v164 op_sel_hi:[0,0,0]
	v_mfma_scale_f32_16x16x128_f8f6f4 v[78:81], v[2:9], v[42:49], v[212:215], v165, v164 op_sel_hi:[0,0,0]
	v_mfma_scale_f32_16x16x128_f8f6f4 v[74:77], v[18:25], v[42:49], v[216:219], v165, v164 op_sel_hi:[0,0,0]
	s_setprio 0
	s_barrier
	s_add_i32 s57, 0, 0x1c000
	v_add_u32_e32 v70, s57, v161
	s_or_b32 s59, s55, 0x80
	s_add_i32 s58, s58, s31
	ds_read_b128 v[130:133], v70
	ds_read_b128 v[134:137], v70 offset:1024
	ds_read_b128 v[146:149], v70 offset:2048
	ds_read_b128 v[150:153], v70 offset:3072
	v_add_u32_e32 v70, s59, v1
	s_mov_b32 m0, s58
	s_nop 0
	global_load_lds_dwordx4 v70, s[10:11]
	v_add_u32_e32 v70, s59, v154
	s_add_i32 m0, s58, 0x2000
	s_nop 0
	global_load_lds_dwordx4 v70, s[10:11]
	s_barrier
	s_waitcnt lgkmcnt(0)
	s_setprio 1

	v_mfma_scale_f32_16x16x128_f8f6f4 v[126:129], v[130:137], v[10:17], v[126:129], v165, v164 op_sel_hi:[0,0,0]
	v_mfma_scale_f32_16x16x128_f8f6f4 v[114:117], v[146:153], v[10:17], v[114:117], v165, v164 op_sel_hi:[0,0,0]
	v_mfma_scale_f32_16x16x128_f8f6f4 v[106:109], v[130:137], v[26:33], v[168:171], v165, v164 op_sel_hi:[0,0,0]
	v_mfma_scale_f32_16x16x128_f8f6f4 v[98:101], v[146:153], v[26:33], v[172:175], v165, v164 op_sel_hi:[0,0,0]
	v_mfma_scale_f32_16x16x128_f8f6f4 v[86:89], v[130:137], v[34:41], v[176:179], v165, v164 op_sel_hi:[0,0,0]
	v_mfma_scale_f32_16x16x128_f8f6f4 v[82:85], v[146:153], v[34:41], v[180:183], v165, v164 op_sel_hi:[0,0,0]
	v_mfma_scale_f32_16x16x128_f8f6f4 v[70:73], v[130:137], v[42:49], v[184:187], v165, v164 op_sel_hi:[0,0,0]
	v_mfma_scale_f32_16x16x128_f8f6f4 v[10:13], v[146:153], v[42:49], v[188:191], v165, v164 op_sel_hi:[0,0,0]
	s_setprio 0
	s_mov_b32 m0, s38
	v_add_u32_e32 v14, s56, v155
	s_barrier
	ds_read_b128 v[34:37], v163 offset:49152
	ds_read_b128 v[38:41], v163 offset:50176
	ds_read_b128 v[168:171], v163 offset:51200
	ds_read_b128 v[172:175], v163 offset:52224
	ds_read_b128 v[176:179], v163 offset:53248
	ds_read_b128 v[180:183], v163 offset:54272
	ds_read_b128 v[184:187], v163 offset:55296
	ds_read_b128 v[188:191], v163 offset:56320
	global_load_lds_dwordx4 v14, s[12:13]
	v_add_u32_e32 v14, s56, v156
	s_mov_b32 m0, s39
	s_nop 0
	global_load_lds_dwordx4 v14, s[12:13]
	s_barrier
	s_waitcnt lgkmcnt(0)
	s_setprio 1

	v_mfma_scale_f32_16x16x128_f8f6f4 v[62:65], v[2:9], v[34:41], v[62:65], v165, v164 op_sel_hi:[0,0,0]
	v_mfma_scale_f32_16x16x128_f8f6f4 v[58:61], v[18:25], v[34:41], v[58:61], v165, v164 op_sel_hi:[0,0,0]
	v_mfma_scale_f32_16x16x128_f8f6f4 v[46:49], v[2:9], v[168:175], v[192:195], v165, v164 op_sel_hi:[0,0,0]
	v_mfma_scale_f32_16x16x128_f8f6f4 v[42:45], v[18:25], v[168:175], v[196:199], v165, v164 op_sel_hi:[0,0,0]
	v_mfma_scale_f32_16x16x128_f8f6f4 v[30:33], v[2:9], v[176:183], v[220:223], v165, v164 op_sel_hi:[0,0,0]
	v_mfma_scale_f32_16x16x128_f8f6f4 v[26:29], v[18:25], v[176:183], v[224:227], v165, v164 op_sel_hi:[0,0,0]
	v_mfma_scale_f32_16x16x128_f8f6f4 v[14:17], v[2:9], v[184:191], v[228:231], v165, v164 op_sel_hi:[0,0,0]
	v_mfma_scale_f32_16x16x128_f8f6f4 v[232:235], v[18:25], v[184:191], v[232:235], v165, v164 op_sel_hi:[0,0,0]
	s_setprio 0
	s_barrier
	s_add_i32 s55, s55, 0x40080
	s_add_i32 s56, s57, s31
	v_add_u32_e32 v2, s55, v1
	s_mov_b32 m0, s56
	s_nop 0
	global_load_lds_dwordx4 v2, s[10:11]
	v_add_u32_e32 v2, s55, v154
	s_add_i32 m0, s56, 0x2000
	s_nop 0
	global_load_lds_dwordx4 v2, s[10:11]
	s_waitcnt vmcnt(6)
	s_barrier
	s_setprio 1
	v_mfma_scale_f32_16x16x128_f8f6f4 v[54:57], v[130:137], v[34:41], v[54:57], v165, v164 op_sel_hi:[0,0,0]
	v_mfma_scale_f32_16x16x128_f8f6f4 v[50:53], v[146:153], v[34:41], v[50:53], v165, v164 op_sel_hi:[0,0,0]
	v_mfma_scale_f32_16x16x128_f8f6f4 v[38:41], v[130:137], v[168:175], v[236:239], v165, v164 op_sel_hi:[0,0,0]
	v_mfma_scale_f32_16x16x128_f8f6f4 v[34:37], v[146:153], v[168:175], v[240:243], v165, v164 op_sel_hi:[0,0,0]
	v_mfma_scale_f32_16x16x128_f8f6f4 v[22:25], v[130:137], v[176:183], v[244:247], v165, v164 op_sel_hi:[0,0,0]
	v_mfma_scale_f32_16x16x128_f8f6f4 v[18:21], v[146:153], v[176:183], v[248:251], v165, v164 op_sel_hi:[0,0,0]
	v_mfma_scale_f32_16x16x128_f8f6f4 v[6:9], v[130:137], v[184:191], v[142:145], v165, v164 op_sel_hi:[0,0,0]
	v_mfma_scale_f32_16x16x128_f8f6f4 v[2:5], v[146:153], v[184:191], v[66:69], v165, v164 op_sel_hi:[0,0,0]
	s_setprio 0
	s_add_i32 s54, s54, 2
	s_addk_i32 s52, 0x100
	s_addk_i32 s53, 0x100
	s_cmp_ge_i32 s54, s40
	s_barrier
	s_cbranch_scc0 .LBB0_1522
	v_readlane_b32 s54, v254, 20
	v_readlane_b32 s55, v254, 21
	v_readlane_b32 s57, v254, 22
	v_readlane_b32 s56, v254, 23
	v_mov_b64_e32 v[220:221], 0x400
	s_branch .LBB0_1513

.LBB0_1840:
	s_add_i32 s74, s73, 0x80
	s_and_b64 s[30:31], s[10:11], exec
	s_cselect_b32 s31, 0, s74
	s_add_i32 s74, s74, s70
	s_or_b32 s30, s31, 0x80
	s_waitcnt lgkmcnt(8)
	s_barrier
	s_waitcnt lgkmcnt(0)
	s_and_b64 s[10:11], s[10:11], exec
	s_cselect_b32 s10, s71, s74
	s_add_i32 s11, s10, 0x80
	s_setprio 1
	s_waitcnt lgkmcnt(0)
	v_mfma_scale_f32_16x16x128_f8f6f4 v[170:173], v[2:9], v[42:49], v[170:173], v193, v193 op_sel_hi:[0,0,0]
	v_mfma_scale_f32_16x16x128_f8f6f4 v[162:165], v[10:17], v[42:49], v[162:165], v193, v193 op_sel_hi:[0,0,0]
	v_mfma_scale_f32_16x16x128_f8f6f4 v[154:157], v[2:9], v[34:41], v[154:157], v193, v193 op_sel_hi:[0,0,0]
	v_mfma_scale_f32_16x16x128_f8f6f4 v[146:149], v[10:17], v[34:41], v[146:149], v193, v193 op_sel_hi:[0,0,0]
	v_mfma_scale_f32_16x16x128_f8f6f4 v[138:141], v[2:9], v[26:33], v[138:141], v193, v193 op_sel_hi:[0,0,0]
	v_mfma_scale_f32_16x16x128_f8f6f4 v[130:133], v[10:17], v[26:33], v[130:133], v193, v193 op_sel_hi:[0,0,0]
	v_mfma_scale_f32_16x16x128_f8f6f4 v[122:125], v[2:9], v[18:25], v[122:125], v193, v193 op_sel_hi:[0,0,0]
	v_mfma_scale_f32_16x16x128_f8f6f4 v[114:117], v[10:17], v[18:25], v[114:117], v193, v193 op_sel_hi:[0,0,0]
	s_setprio 0
	s_barrier
	s_mov_b32 m0, s38
	v_add_u32_e32 v216, s59, v189
	v_add_u32_e32 v220, s10, v181
	ds_read_b128 v[204:207], v216
	ds_read_b128 v[208:211], v216 offset:1024
	ds_read_b128 v[212:215], v216 offset:2048
	ds_read_b128 v[216:219], v216 offset:3072
	global_load_lds_dwordx4 v220, s[20:21]
	v_add_u32_e32 v220, s10, v182
	s_mov_b32 m0, s39
	s_nop 0
	global_load_lds_dwordx4 v220, s[20:21]
	s_barrier
	s_waitcnt lgkmcnt(0)
	s_setprio 1

	v_mfma_scale_f32_16x16x128_f8f6f4 v[174:177], v[204:211], v[42:49], v[174:177], v193, v193 op_sel_hi:[0,0,0]
	v_mfma_scale_f32_16x16x128_f8f6f4 v[166:169], v[212:219], v[42:49], v[166:169], v193, v193 op_sel_hi:[0,0,0]
	v_mfma_scale_f32_16x16x128_f8f6f4 v[158:161], v[204:211], v[34:41], v[158:161], v193, v193 op_sel_hi:[0,0,0]
	v_mfma_scale_f32_16x16x128_f8f6f4 v[150:153], v[212:219], v[34:41], v[150:153], v193, v193 op_sel_hi:[0,0,0]
	v_mfma_scale_f32_16x16x128_f8f6f4 v[142:145], v[204:211], v[26:33], v[142:145], v193, v193 op_sel_hi:[0,0,0]
	v_mfma_scale_f32_16x16x128_f8f6f4 v[134:137], v[212:219], v[26:33], v[134:137], v193, v193 op_sel_hi:[0,0,0]
	v_mfma_scale_f32_16x16x128_f8f6f4 v[126:129], v[204:211], v[18:25], v[126:129], v193, v193 op_sel_hi:[0,0,0]
	v_mfma_scale_f32_16x16x128_f8f6f4 v[118:121], v[212:219], v[18:25], v[118:121], v193, v193 op_sel_hi:[0,0,0]
	s_setprio 0
	s_mov_b32 m0, s37
	v_add_u32_e32 v220, s31, v183
	s_barrier
	ds_read_b128 v[18:21], v194 offset:16384
	ds_read_b128 v[22:25], v194 offset:17408
	ds_read_b128 v[26:29], v194 offset:18432
	ds_read_b128 v[30:33], v194 offset:19456
	ds_read_b128 v[34:37], v194 offset:20480
	ds_read_b128 v[38:41], v194 offset:21504
	ds_read_b128 v[42:45], v194 offset:22528
	ds_read_b128 v[46:49], v194 offset:23552
	global_load_lds_dwordx4 v220, s[18:19]
	v_add_u32_e32 v220, s31, v184
	s_mov_b32 m0, s40
	s_nop 0
	global_load_lds_dwordx4 v220, s[18:19]
	s_barrier
	s_waitcnt lgkmcnt(0)
	s_setprio 1

	v_mfma_scale_f32_16x16x128_f8f6f4 v[110:113], v[2:9], v[18:25], v[110:113], v193, v193 op_sel_hi:[0,0,0]
	v_mfma_scale_f32_16x16x128_f8f6f4 v[102:105], v[10:17], v[18:25], v[102:105], v193, v193 op_sel_hi:[0,0,0]
	v_mfma_scale_f32_16x16x128_f8f6f4 v[94:97], v[2:9], v[26:33], v[94:97], v193, v193 op_sel_hi:[0,0,0]
	v_mfma_scale_f32_16x16x128_f8f6f4 v[86:89], v[10:17], v[26:33], v[86:89], v193, v193 op_sel_hi:[0,0,0]
	v_mfma_scale_f32_16x16x128_f8f6f4 v[78:81], v[2:9], v[34:41], v[78:81], v193, v193 op_sel_hi:[0,0,0]
	v_mfma_scale_f32_16x16x128_f8f6f4 v[70:73], v[10:17], v[34:41], v[70:73], v193, v193 op_sel_hi:[0,0,0]
	v_mfma_scale_f32_16x16x128_f8f6f4 v[62:65], v[2:9], v[42:49], v[62:65], v193, v193 op_sel_hi:[0,0,0]
	v_mfma_scale_f32_16x16x128_f8f6f4 v[54:57], v[10:17], v[42:49], v[54:57], v193, v193 op_sel_hi:[0,0,0]
	s_setprio 0
	s_barrier
	s_add_i32 s74, s10, 0x40000
	s_add_i32 s75, s59, s36
	v_add_u32_e32 v2, s74, v181
	s_mov_b32 m0, s75
	s_nop 0
	global_load_lds_dwordx4 v2, s[20:21]
	v_add_u32_e32 v2, s74, v182
	s_add_i32 m0, s75, 0x2000
	s_nop 0
	global_load_lds_dwordx4 v2, s[20:21]
	s_waitcnt vmcnt(6)
	s_barrier
	s_setprio 1
	v_mfma_scale_f32_16x16x128_f8f6f4 v[106:109], v[204:211], v[18:25], v[106:109], v193, v193 op_sel_hi:[0,0,0]
	v_mfma_scale_f32_16x16x128_f8f6f4 v[98:101], v[212:219], v[18:25], v[98:101], v193, v193 op_sel_hi:[0,0,0]
	v_mfma_scale_f32_16x16x128_f8f6f4 v[90:93], v[204:211], v[26:33], v[90:93], v193, v193 op_sel_hi:[0,0,0]
	v_mfma_scale_f32_16x16x128_f8f6f4 v[82:85], v[212:219], v[26:33], v[82:85], v193, v193 op_sel_hi:[0,0,0]
	v_mfma_scale_f32_16x16x128_f8f6f4 v[74:77], v[204:211], v[34:41], v[74:77], v193, v193 op_sel_hi:[0,0,0]
	v_mfma_scale_f32_16x16x128_f8f6f4 v[66:69], v[212:219], v[34:41], v[66:69], v193, v193 op_sel_hi:[0,0,0]
	v_mfma_scale_f32_16x16x128_f8f6f4 v[58:61], v[204:211], v[42:49], v[58:61], v193, v193 op_sel_hi:[0,0,0]
	v_mfma_scale_f32_16x16x128_f8f6f4 v[50:53], v[212:219], v[42:49], v[50:53], v193, v193 op_sel_hi:[0,0,0]
	s_setprio 0
	s_add_i32 s74, 0, 0x18000
	v_add_u32_e32 v14, s74, v189
	s_barrier
	ds_read_b128 v[2:5], v14
	ds_read_b128 v[6:9], v14 offset:1024
	ds_read_b128 v[10:13], v14 offset:2048
	ds_read_b128 v[14:17], v14 offset:3072
	s_mov_b32 m0, s41
	v_add_u32_e32 v204, s31, v185
	ds_read_b128 v[18:21], v194 offset:32768
	ds_read_b128 v[22:25], v194 offset:33792
	ds_read_b128 v[26:29], v194 offset:34816
	ds_read_b128 v[30:33], v194 offset:35840
	ds_read_b128 v[34:37], v194 offset:36864
	ds_read_b128 v[38:41], v194 offset:37888
	ds_read_b128 v[42:45], v194 offset:38912
	ds_read_b128 v[46:49], v194 offset:39936
	global_load_lds_dwordx4 v204, s[18:19]
	v_add_u32_e32 v204, s31, v186
	s_mov_b32 m0, s42
	s_nop 0
	global_load_lds_dwordx4 v204, s[18:19]
	s_waitcnt lgkmcnt(8)
	s_barrier
	s_waitcnt lgkmcnt(0)
	s_setprio 1

	v_mfma_scale_f32_16x16x128_f8f6f4 v[170:173], v[2:9], v[18:25], v[170:173], v193, v193 op_sel_hi:[0,0,0]
	v_mfma_scale_f32_16x16x128_f8f6f4 v[162:165], v[10:17], v[18:25], v[162:165], v193, v193 op_sel_hi:[0,0,0]
	v_mfma_scale_f32_16x16x128_f8f6f4 v[154:157], v[2:9], v[26:33], v[154:157], v193, v193 op_sel_hi:[0,0,0]
	v_mfma_scale_f32_16x16x128_f8f6f4 v[146:149], v[10:17], v[26:33], v[146:149], v193, v193 op_sel_hi:[0,0,0]
	v_mfma_scale_f32_16x16x128_f8f6f4 v[138:141], v[2:9], v[34:41], v[138:141], v193, v193 op_sel_hi:[0,0,0]
	v_mfma_scale_f32_16x16x128_f8f6f4 v[130:133], v[10:17], v[34:41], v[130:133], v193, v193 op_sel_hi:[0,0,0]
	v_mfma_scale_f32_16x16x128_f8f6f4 v[122:125], v[2:9], v[42:49], v[122:125], v193, v193 op_sel_hi:[0,0,0]
	v_mfma_scale_f32_16x16x128_f8f6f4 v[114:117], v[10:17], v[42:49], v[114:117], v193, v193 op_sel_hi:[0,0,0]
	s_setprio 0
	s_barrier
	s_add_i32 s31, 0, 0x1c000
	s_add_i32 s74, s74, s36
	v_add_u32_e32 v216, s31, v189
	v_add_u32_e32 v220, s11, v181
	s_mov_b32 m0, s74
	ds_read_b128 v[204:207], v216
	ds_read_b128 v[208:211], v216 offset:1024
	ds_read_b128 v[212:215], v216 offset:2048
	ds_read_b128 v[216:219], v216 offset:3072
	global_load_lds_dwordx4 v220, s[20:21]
	v_add_u32_e32 v220, s11, v182
	s_add_i32 m0, s74, 0x2000
	s_nop 0
	global_load_lds_dwordx4 v220, s[20:21]
	s_barrier
	s_waitcnt lgkmcnt(0)
	s_setprio 1

	v_mfma_scale_f32_16x16x128_f8f6f4 v[174:177], v[204:211], v[18:25], v[174:177], v193, v193 op_sel_hi:[0,0,0]
	v_mfma_scale_f32_16x16x128_f8f6f4 v[166:169], v[212:219], v[18:25], v[166:169], v193, v193 op_sel_hi:[0,0,0]
	v_mfma_scale_f32_16x16x128_f8f6f4 v[158:161], v[204:211], v[26:33], v[158:161], v193, v193 op_sel_hi:[0,0,0]
	v_mfma_scale_f32_16x16x128_f8f6f4 v[150:153], v[212:219], v[26:33], v[150:153], v193, v193 op_sel_hi:[0,0,0]
	v_mfma_scale_f32_16x16x128_f8f6f4 v[142:145], v[204:211], v[34:41], v[142:145], v193, v193 op_sel_hi:[0,0,0]
	v_mfma_scale_f32_16x16x128_f8f6f4 v[134:137], v[212:219], v[34:41], v[134:137], v193, v193 op_sel_hi:[0,0,0]
	v_mfma_scale_f32_16x16x128_f8f6f4 v[126:129], v[204:211], v[42:49], v[126:129], v193, v193 op_sel_hi:[0,0,0]
	v_mfma_scale_f32_16x16x128_f8f6f4 v[118:121], v[212:219], v[42:49], v[118:121], v193, v193 op_sel_hi:[0,0,0]
	s_setprio 0
	s_mov_b32 m0, s49
	v_add_u32_e32 v220, s30, v183
	s_barrier
	ds_read_b128 v[18:21], v194 offset:49152
	ds_read_b128 v[22:25], v194 offset:50176
	ds_read_b128 v[26:29], v194 offset:51200
	ds_read_b128 v[30:33], v194 offset:52224
	ds_read_b128 v[34:37], v194 offset:53248
	ds_read_b128 v[38:41], v194 offset:54272
	ds_read_b128 v[42:45], v194 offset:55296
	ds_read_b128 v[46:49], v194 offset:56320
	global_load_lds_dwordx4 v220, s[18:19]
	v_add_u32_e32 v220, s30, v184
	s_mov_b32 m0, s50
	s_nop 0
	global_load_lds_dwordx4 v220, s[18:19]
	s_barrier
	s_waitcnt lgkmcnt(0)
	s_setprio 1

	v_mfma_scale_f32_16x16x128_f8f6f4 v[110:113], v[2:9], v[18:25], v[110:113], v193, v193 op_sel_hi:[0,0,0]
	v_mfma_scale_f32_16x16x128_f8f6f4 v[102:105], v[10:17], v[18:25], v[102:105], v193, v193 op_sel_hi:[0,0,0]
	v_mfma_scale_f32_16x16x128_f8f6f4 v[94:97], v[2:9], v[26:33], v[94:97], v193, v193 op_sel_hi:[0,0,0]
	v_mfma_scale_f32_16x16x128_f8f6f4 v[86:89], v[10:17], v[26:33], v[86:89], v193, v193 op_sel_hi:[0,0,0]
	v_mfma_scale_f32_16x16x128_f8f6f4 v[78:81], v[2:9], v[34:41], v[78:81], v193, v193 op_sel_hi:[0,0,0]
	v_mfma_scale_f32_16x16x128_f8f6f4 v[70:73], v[10:17], v[34:41], v[70:73], v193, v193 op_sel_hi:[0,0,0]
	v_mfma_scale_f32_16x16x128_f8f6f4 v[62:65], v[2:9], v[42:49], v[62:65], v193, v193 op_sel_hi:[0,0,0]
	v_mfma_scale_f32_16x16x128_f8f6f4 v[54:57], v[10:17], v[42:49], v[54:57], v193, v193 op_sel_hi:[0,0,0]
	s_setprio 0
	s_barrier
	s_add_i32 s10, s10, 0x40080
	s_add_i32 s11, s31, s36
	v_add_u32_e32 v2, s10, v181
	s_mov_b32 m0, s11
	s_nop 0
	global_load_lds_dwordx4 v2, s[20:21]
	v_add_u32_e32 v2, s10, v182
	s_add_i32 m0, s11, 0x2000
	s_nop 0
	global_load_lds_dwordx4 v2, s[20:21]
	s_waitcnt vmcnt(6)
	s_barrier
	s_setprio 1
	v_mfma_scale_f32_16x16x128_f8f6f4 v[106:109], v[204:211], v[18:25], v[106:109], v193, v193 op_sel_hi:[0,0,0]
	v_mfma_scale_f32_16x16x128_f8f6f4 v[98:101], v[212:219], v[18:25], v[98:101], v193, v193 op_sel_hi:[0,0,0]
	v_mfma_scale_f32_16x16x128_f8f6f4 v[90:93], v[204:211], v[26:33], v[90:93], v193, v193 op_sel_hi:[0,0,0]
	v_mfma_scale_f32_16x16x128_f8f6f4 v[82:85], v[212:219], v[26:33], v[82:85], v193, v193 op_sel_hi:[0,0,0]
	v_mfma_scale_f32_16x16x128_f8f6f4 v[74:77], v[204:211], v[34:41], v[74:77], v193, v193 op_sel_hi:[0,0,0]
	v_mfma_scale_f32_16x16x128_f8f6f4 v[66:69], v[212:219], v[34:41], v[66:69], v193, v193 op_sel_hi:[0,0,0]
	v_mfma_scale_f32_16x16x128_f8f6f4 v[58:61], v[204:211], v[42:49], v[58:61], v193, v193 op_sel_hi:[0,0,0]
	v_mfma_scale_f32_16x16x128_f8f6f4 v[50:53], v[212:219], v[42:49], v[50:53], v193, v193 op_sel_hi:[0,0,0]
	s_setprio 0
	s_add_i32 s72, s72, 2
	s_addk_i32 s73, 0x100
	s_cmp_ge_i32 s72, s51
	s_barrier
	s_cbranch_scc1 .LBB0_1830

.LBB0_1864:
	s_add_i32 s58, s55, 0x80
	s_cmp_eq_u32 s44, s57
	s_cselect_b32 s60, s4, s58
	s_cselect_b32 s58, s5, s56
	s_add_i32 s61, 0, 0x10000
	v_add_u32_e32 v156, s61, v141
	ds_read_b128 v[144:147], v156
	ds_read_b128 v[148:151], v156 offset:1024
	ds_read_b128 v[152:155], v156 offset:2048
	ds_read_b128 v[156:159], v156 offset:3072
	s_or_b32 s59, s60, 0x80
	v_add_u32_e32 v192, s55, v137
	s_add_i32 m0, s33, 0xc000
	ds_read_b128 v[160:163], v142
	ds_read_b128 v[164:167], v142 offset:1024
	ds_read_b128 v[168:171], v142 offset:2048
	ds_read_b128 v[172:175], v142 offset:3072
	ds_read_b128 v[176:179], v142 offset:4096
	ds_read_b128 v[180:183], v142 offset:5120
	ds_read_b128 v[184:187], v142 offset:6144
	ds_read_b128 v[188:191], v142 offset:7168
	global_load_lds_dwordx4 v192, s[6:7]
	v_add_u32_e32 v192, s55, v138
	s_add_i32 m0, s33, 0xe000
	s_nop 0
	global_load_lds_dwordx4 v192, s[6:7]
	s_waitcnt lgkmcnt(8)
	s_barrier
	s_waitcnt lgkmcnt(0)
	s_setprio 1

	v_mfma_f32_16x16x32_bf16 v[122:125], v[144:147], v[160:163], v[122:125]
	v_mfma_f32_16x16x32_bf16 v[126:129], v[152:155], v[160:163], v[126:129]
	v_mfma_f32_16x16x32_bf16 v[110:113], v[144:147], v[168:171], v[110:113]
	v_mfma_f32_16x16x32_bf16 v[106:109], v[152:155], v[168:171], v[106:109]
	v_mfma_f32_16x16x32_bf16 v[94:97], v[144:147], v[176:179], v[94:97]
	v_mfma_f32_16x16x32_bf16 v[90:93], v[152:155], v[176:179], v[90:93]
	v_mfma_f32_16x16x32_bf16 v[78:81], v[144:147], v[184:187], v[78:81]
	v_mfma_f32_16x16x32_bf16 v[74:77], v[152:155], v[184:187], v[74:77]
	v_mfma_f32_16x16x32_bf16 v[122:125], v[148:151], v[164:167], v[122:125]
	v_mfma_f32_16x16x32_bf16 v[126:129], v[156:159], v[164:167], v[126:129]
	v_mfma_f32_16x16x32_bf16 v[110:113], v[148:151], v[172:175], v[110:113]
	v_mfma_f32_16x16x32_bf16 v[106:109], v[156:159], v[172:175], v[106:109]
	v_mfma_f32_16x16x32_bf16 v[94:97], v[148:151], v[180:183], v[94:97]
	v_mfma_f32_16x16x32_bf16 v[90:93], v[156:159], v[180:183], v[90:93]
	v_mfma_f32_16x16x32_bf16 v[78:81], v[148:151], v[188:191], v[78:81]
	v_mfma_f32_16x16x32_bf16 v[74:77], v[156:159], v[188:191], v[74:77]
	s_setprio 0
	s_barrier
	s_add_i32 s61, s61, s31
	v_add_u32_e32 v208, s58, v1
	s_mov_b32 m0, s61
	ds_read_b128 v[192:195], v143
	ds_read_b128 v[196:199], v143 offset:1024
	ds_read_b128 v[200:203], v143 offset:2048
	ds_read_b128 v[204:207], v143 offset:3072
	global_load_lds_dwordx4 v208, s[8:9]
	v_add_u32_e32 v208, s58, v134
	s_add_i32 m0, s61, 0x2000
	s_nop 0
	global_load_lds_dwordx4 v208, s[8:9]
	s_barrier
	s_waitcnt lgkmcnt(0)
	s_setprio 1

	v_mfma_f32_16x16x32_bf16 v[118:121], v[192:195], v[160:163], v[118:121]
	v_mfma_f32_16x16x32_bf16 v[114:117], v[200:203], v[160:163], v[114:117]
	v_mfma_f32_16x16x32_bf16 v[102:105], v[192:195], v[168:171], v[102:105]
	v_mfma_f32_16x16x32_bf16 v[98:101], v[200:203], v[168:171], v[98:101]
	v_mfma_f32_16x16x32_bf16 v[86:89], v[192:195], v[176:179], v[86:89]
	v_mfma_f32_16x16x32_bf16 v[82:85], v[200:203], v[176:179], v[82:85]
	v_mfma_f32_16x16x32_bf16 v[70:73], v[192:195], v[184:187], v[70:73]
	v_mfma_f32_16x16x32_bf16 v[66:69], v[200:203], v[184:187], v[66:69]
	v_mfma_f32_16x16x32_bf16 v[118:121], v[196:199], v[164:167], v[118:121]
	v_mfma_f32_16x16x32_bf16 v[114:117], v[204:207], v[164:167], v[114:117]
	v_mfma_f32_16x16x32_bf16 v[102:105], v[196:199], v[172:175], v[102:105]
	v_mfma_f32_16x16x32_bf16 v[98:101], v[204:207], v[172:175], v[98:101]
	v_mfma_f32_16x16x32_bf16 v[86:89], v[196:199], v[180:183], v[86:89]
	v_mfma_f32_16x16x32_bf16 v[82:85], v[204:207], v[180:183], v[82:85]
	v_mfma_f32_16x16x32_bf16 v[70:73], v[196:199], v[188:191], v[70:73]
	v_mfma_f32_16x16x32_bf16 v[66:69], v[204:207], v[188:191], v[66:69]
	s_setprio 0
	s_mov_b32 m0, s33
	v_add_u32_e32 v208, s60, v135
	s_barrier
	ds_read_b128 v[160:163], v142 offset:16384
	ds_read_b128 v[164:167], v142 offset:17408
	ds_read_b128 v[168:171], v142 offset:18432
	ds_read_b128 v[172:175], v142 offset:19456
	ds_read_b128 v[176:179], v142 offset:20480
	ds_read_b128 v[180:183], v142 offset:21504
	ds_read_b128 v[184:187], v142 offset:22528
	ds_read_b128 v[188:191], v142 offset:23552
	global_load_lds_dwordx4 v208, s[6:7]
	v_add_u32_e32 v208, s60, v136
	s_mov_b32 m0, s35
	s_nop 0
	global_load_lds_dwordx4 v208, s[6:7]
	s_barrier
	s_waitcnt lgkmcnt(0)
	s_setprio 1

	v_mfma_f32_16x16x32_bf16 v[62:65], v[144:147], v[160:163], v[62:65]
	v_mfma_f32_16x16x32_bf16 v[58:61], v[152:155], v[160:163], v[58:61]
	v_mfma_f32_16x16x32_bf16 v[46:49], v[144:147], v[168:171], v[46:49]
	v_mfma_f32_16x16x32_bf16 v[42:45], v[152:155], v[168:171], v[42:45]
	v_mfma_f32_16x16x32_bf16 v[30:33], v[144:147], v[176:179], v[30:33]
	v_mfma_f32_16x16x32_bf16 v[26:29], v[152:155], v[176:179], v[26:29]
	v_mfma_f32_16x16x32_bf16 v[14:17], v[144:147], v[184:187], v[14:17]
	v_mfma_f32_16x16x32_bf16 v[10:13], v[152:155], v[184:187], v[10:13]
	v_mfma_f32_16x16x32_bf16 v[62:65], v[148:151], v[164:167], v[62:65]
	v_mfma_f32_16x16x32_bf16 v[58:61], v[156:159], v[164:167], v[58:61]
	v_mfma_f32_16x16x32_bf16 v[46:49], v[148:151], v[172:175], v[46:49]
	v_mfma_f32_16x16x32_bf16 v[42:45], v[156:159], v[172:175], v[42:45]
	v_mfma_f32_16x16x32_bf16 v[30:33], v[148:151], v[180:183], v[30:33]
	v_mfma_f32_16x16x32_bf16 v[26:29], v[156:159], v[180:183], v[26:29]
	v_mfma_f32_16x16x32_bf16 v[14:17], v[148:151], v[188:191], v[14:17]
	v_mfma_f32_16x16x32_bf16 v[10:13], v[156:159], v[188:191], v[10:13]
	s_setprio 0
	s_barrier
	s_add_i32 s61, s58, 0x10000
	s_add_i32 s62, s45, s31
	v_add_u32_e32 v144, s61, v1
	s_mov_b32 m0, s62
	s_nop 0
	global_load_lds_dwordx4 v144, s[8:9]
	v_add_u32_e32 v144, s61, v134
	s_add_i32 m0, s62, 0x2000
	s_nop 0
	global_load_lds_dwordx4 v144, s[8:9]
	s_waitcnt vmcnt(6)
	s_barrier
	s_setprio 1
	v_mfma_f32_16x16x32_bf16 v[54:57], v[192:195], v[160:163], v[54:57]
	v_mfma_f32_16x16x32_bf16 v[50:53], v[200:203], v[160:163], v[50:53]
	v_mfma_f32_16x16x32_bf16 v[38:41], v[192:195], v[168:171], v[38:41]
	v_mfma_f32_16x16x32_bf16 v[34:37], v[200:203], v[168:171], v[34:37]
	v_mfma_f32_16x16x32_bf16 v[22:25], v[192:195], v[176:179], v[22:25]
	v_mfma_f32_16x16x32_bf16 v[18:21], v[200:203], v[176:179], v[18:21]
	v_mfma_f32_16x16x32_bf16 v[6:9], v[192:195], v[184:187], v[6:9]
	v_mfma_f32_16x16x32_bf16 v[2:5], v[200:203], v[184:187], v[2:5]
	v_mfma_f32_16x16x32_bf16 v[54:57], v[196:199], v[164:167], v[54:57]
	v_mfma_f32_16x16x32_bf16 v[50:53], v[204:207], v[164:167], v[50:53]
	v_mfma_f32_16x16x32_bf16 v[38:41], v[196:199], v[172:175], v[38:41]
	v_mfma_f32_16x16x32_bf16 v[34:37], v[204:207], v[172:175], v[34:37]
	v_mfma_f32_16x16x32_bf16 v[22:25], v[196:199], v[180:183], v[22:25]
	v_mfma_f32_16x16x32_bf16 v[18:21], v[204:207], v[180:183], v[18:21]
	v_mfma_f32_16x16x32_bf16 v[6:9], v[196:199], v[188:191], v[6:9]
	v_mfma_f32_16x16x32_bf16 v[2:5], v[204:207], v[188:191], v[2:5]
	s_setprio 0
	s_add_i32 s61, 0, 0x18000
	v_add_u32_e32 v156, s61, v141
	s_barrier
	ds_read_b128 v[144:147], v156
	ds_read_b128 v[148:151], v156 offset:1024
	ds_read_b128 v[152:155], v156 offset:2048
	ds_read_b128 v[156:159], v156 offset:3072
	s_mov_b32 m0, s36
	v_add_u32_e32 v192, s60, v137
	ds_read_b128 v[160:163], v142 offset:32768
	ds_read_b128 v[164:167], v142 offset:33792
	ds_read_b128 v[168:171], v142 offset:34816
	ds_read_b128 v[172:175], v142 offset:35840
	ds_read_b128 v[176:179], v142 offset:36864
	ds_read_b128 v[180:183], v142 offset:37888
	ds_read_b128 v[184:187], v142 offset:38912
	ds_read_b128 v[188:191], v142 offset:39936
	global_load_lds_dwordx4 v192, s[6:7]
	v_add_u32_e32 v192, s60, v138
	s_mov_b32 m0, s37
	s_nop 0
	global_load_lds_dwordx4 v192, s[6:7]
	s_waitcnt lgkmcnt(8)
	s_barrier
	s_waitcnt lgkmcnt(0)
	s_setprio 1

	v_mfma_f32_16x16x32_bf16 v[122:125], v[144:147], v[160:163], v[122:125]
	v_mfma_f32_16x16x32_bf16 v[126:129], v[152:155], v[160:163], v[126:129]
	v_mfma_f32_16x16x32_bf16 v[110:113], v[144:147], v[168:171], v[110:113]
	v_mfma_f32_16x16x32_bf16 v[106:109], v[152:155], v[168:171], v[106:109]
	v_mfma_f32_16x16x32_bf16 v[94:97], v[144:147], v[176:179], v[94:97]
	v_mfma_f32_16x16x32_bf16 v[90:93], v[152:155], v[176:179], v[90:93]
	v_mfma_f32_16x16x32_bf16 v[78:81], v[144:147], v[184:187], v[78:81]
	v_mfma_f32_16x16x32_bf16 v[74:77], v[152:155], v[184:187], v[74:77]
	v_mfma_f32_16x16x32_bf16 v[122:125], v[148:151], v[164:167], v[122:125]
	v_mfma_f32_16x16x32_bf16 v[126:129], v[156:159], v[164:167], v[126:129]
	v_mfma_f32_16x16x32_bf16 v[110:113], v[148:151], v[172:175], v[110:113]
	v_mfma_f32_16x16x32_bf16 v[106:109], v[156:159], v[172:175], v[106:109]
	v_mfma_f32_16x16x32_bf16 v[94:97], v[148:151], v[180:183], v[94:97]
	v_mfma_f32_16x16x32_bf16 v[90:93], v[156:159], v[180:183], v[90:93]
	v_mfma_f32_16x16x32_bf16 v[78:81], v[148:151], v[188:191], v[78:81]
	v_mfma_f32_16x16x32_bf16 v[74:77], v[156:159], v[188:191], v[74:77]
	s_setprio 0
	s_barrier
	s_add_i32 s60, 0, 0x1c000
	s_or_b32 s62, s58, 0x80
	s_add_i32 s61, s61, s31
	v_add_u32_e32 v204, s60, v141
	v_add_u32_e32 v208, s62, v1
	s_mov_b32 m0, s61
	ds_read_b128 v[192:195], v204
	ds_read_b128 v[196:199], v204 offset:1024
	ds_read_b128 v[200:203], v204 offset:2048
	ds_read_b128 v[204:207], v204 offset:3072
	global_load_lds_dwordx4 v208, s[8:9]
	v_add_u32_e32 v208, s62, v134
	s_add_i32 m0, s61, 0x2000
	s_nop 0
	global_load_lds_dwordx4 v208, s[8:9]
	s_barrier
	s_waitcnt lgkmcnt(0)
	s_setprio 1

	v_mfma_f32_16x16x32_bf16 v[118:121], v[192:195], v[160:163], v[118:121]
	v_mfma_f32_16x16x32_bf16 v[114:117], v[200:203], v[160:163], v[114:117]
	v_mfma_f32_16x16x32_bf16 v[102:105], v[192:195], v[168:171], v[102:105]
	v_mfma_f32_16x16x32_bf16 v[98:101], v[200:203], v[168:171], v[98:101]
	v_mfma_f32_16x16x32_bf16 v[86:89], v[192:195], v[176:179], v[86:89]
	v_mfma_f32_16x16x32_bf16 v[82:85], v[200:203], v[176:179], v[82:85]
	v_mfma_f32_16x16x32_bf16 v[70:73], v[192:195], v[184:187], v[70:73]
	v_mfma_f32_16x16x32_bf16 v[66:69], v[200:203], v[184:187], v[66:69]
	v_mfma_f32_16x16x32_bf16 v[118:121], v[196:199], v[164:167], v[118:121]
	v_mfma_f32_16x16x32_bf16 v[114:117], v[204:207], v[164:167], v[114:117]
	v_mfma_f32_16x16x32_bf16 v[102:105], v[196:199], v[172:175], v[102:105]
	v_mfma_f32_16x16x32_bf16 v[98:101], v[204:207], v[172:175], v[98:101]
	v_mfma_f32_16x16x32_bf16 v[86:89], v[196:199], v[180:183], v[86:89]
	v_mfma_f32_16x16x32_bf16 v[82:85], v[204:207], v[180:183], v[82:85]
	v_mfma_f32_16x16x32_bf16 v[70:73], v[196:199], v[188:191], v[70:73]
	v_mfma_f32_16x16x32_bf16 v[66:69], v[204:207], v[188:191], v[66:69]
	s_setprio 0
	s_mov_b32 m0, s40
	v_add_u32_e32 v208, s59, v135
	s_barrier
	ds_read_b128 v[160:163], v142 offset:49152
	ds_read_b128 v[164:167], v142 offset:50176
	ds_read_b128 v[168:171], v142 offset:51200
	ds_read_b128 v[172:175], v142 offset:52224
	ds_read_b128 v[176:179], v142 offset:53248
	ds_read_b128 v[180:183], v142 offset:54272
	ds_read_b128 v[184:187], v142 offset:55296
	ds_read_b128 v[188:191], v142 offset:56320
	global_load_lds_dwordx4 v208, s[6:7]
	v_add_u32_e32 v208, s59, v136
	s_mov_b32 m0, s41
	s_nop 0
	global_load_lds_dwordx4 v208, s[6:7]
	s_barrier
	s_waitcnt lgkmcnt(0)
	s_setprio 1

	v_mfma_f32_16x16x32_bf16 v[62:65], v[144:147], v[160:163], v[62:65]
	v_mfma_f32_16x16x32_bf16 v[58:61], v[152:155], v[160:163], v[58:61]
	v_mfma_f32_16x16x32_bf16 v[46:49], v[144:147], v[168:171], v[46:49]
	v_mfma_f32_16x16x32_bf16 v[42:45], v[152:155], v[168:171], v[42:45]
	v_mfma_f32_16x16x32_bf16 v[30:33], v[144:147], v[176:179], v[30:33]
	v_mfma_f32_16x16x32_bf16 v[26:29], v[152:155], v[176:179], v[26:29]
	v_mfma_f32_16x16x32_bf16 v[14:17], v[144:147], v[184:187], v[14:17]
	v_mfma_f32_16x16x32_bf16 v[10:13], v[152:155], v[184:187], v[10:13]
	v_mfma_f32_16x16x32_bf16 v[62:65], v[148:151], v[164:167], v[62:65]
	v_mfma_f32_16x16x32_bf16 v[58:61], v[156:159], v[164:167], v[58:61]
	v_mfma_f32_16x16x32_bf16 v[46:49], v[148:151], v[172:175], v[46:49]
	v_mfma_f32_16x16x32_bf16 v[42:45], v[156:159], v[172:175], v[42:45]
	v_mfma_f32_16x16x32_bf16 v[30:33], v[148:151], v[180:183], v[30:33]
	v_mfma_f32_16x16x32_bf16 v[26:29], v[156:159], v[180:183], v[26:29]
	v_mfma_f32_16x16x32_bf16 v[14:17], v[148:151], v[188:191], v[14:17]
	v_mfma_f32_16x16x32_bf16 v[10:13], v[156:159], v[188:191], v[10:13]
	s_setprio 0
	s_barrier
	s_add_i32 s58, s58, 0x10080
	s_add_i32 s59, s60, s31
	v_add_u32_e32 v144, s58, v1
	s_mov_b32 m0, s59
	s_nop 0
	global_load_lds_dwordx4 v144, s[8:9]
	v_add_u32_e32 v144, s58, v134
	s_add_i32 m0, s59, 0x2000
	s_nop 0
	global_load_lds_dwordx4 v144, s[8:9]
	s_waitcnt vmcnt(6)
	s_barrier
	s_setprio 1
	v_mfma_f32_16x16x32_bf16 v[54:57], v[192:195], v[160:163], v[54:57]
	v_mfma_f32_16x16x32_bf16 v[50:53], v[200:203], v[160:163], v[50:53]
	v_mfma_f32_16x16x32_bf16 v[38:41], v[192:195], v[168:171], v[38:41]
	v_mfma_f32_16x16x32_bf16 v[34:37], v[200:203], v[168:171], v[34:37]
	v_mfma_f32_16x16x32_bf16 v[22:25], v[192:195], v[176:179], v[22:25]
	v_mfma_f32_16x16x32_bf16 v[18:21], v[200:203], v[176:179], v[18:21]
	v_mfma_f32_16x16x32_bf16 v[6:9], v[192:195], v[184:187], v[6:9]
	v_mfma_f32_16x16x32_bf16 v[2:5], v[200:203], v[184:187], v[2:5]
	v_mfma_f32_16x16x32_bf16 v[54:57], v[196:199], v[164:167], v[54:57]
	v_mfma_f32_16x16x32_bf16 v[50:53], v[204:207], v[164:167], v[50:53]
	v_mfma_f32_16x16x32_bf16 v[38:41], v[196:199], v[172:175], v[38:41]
	v_mfma_f32_16x16x32_bf16 v[34:37], v[204:207], v[172:175], v[34:37]
	v_mfma_f32_16x16x32_bf16 v[22:25], v[196:199], v[180:183], v[22:25]
	v_mfma_f32_16x16x32_bf16 v[18:21], v[204:207], v[180:183], v[18:21]
	v_mfma_f32_16x16x32_bf16 v[6:9], v[196:199], v[188:191], v[6:9]
	v_mfma_f32_16x16x32_bf16 v[2:5], v[204:207], v[188:191], v[2:5]
	s_setprio 0
	s_add_i32 s57, s57, 2
	s_addk_i32 s55, 0x100
	s_addk_i32 s56, 0x100
	s_cmp_ge_i32 s57, s42
	s_barrier
	s_cbranch_scc0 .LBB0_1864
	v_readlane_b32 s57, v254, 22
	s_branch .LBB0_1855

.LBB0_1947:
	v_add_u32_e32 v66, s37, v138
	ds_read_b128 v[144:147], v66
	ds_read_b128 v[148:151], v66 offset:1024
	ds_read_b128 v[152:155], v66 offset:2048
	ds_read_b128 v[156:159], v66 offset:3072
	s_add_i32 s51, s48, 0x80
	s_and_b64 s[52:53], s[16:17], exec
	s_cselect_b32 s52, s46, s51
	s_or_b32 s51, s52, 0x80
	s_and_b64 s[16:17], s[16:17], exec
	s_cselect_b32 s16, s47, s49
	v_add_u32_e32 v66, s48, v135
	s_add_i32 m0, s21, 0xc000
	ds_read_b128 v[160:163], v141
	ds_read_b128 v[164:167], v141 offset:1024
	ds_read_b128 v[168:171], v141 offset:2048
	ds_read_b128 v[172:175], v141 offset:3072
	ds_read_b128 v[176:179], v141 offset:4096
	ds_read_b128 v[180:183], v141 offset:5120
	ds_read_b128 v[184:187], v141 offset:6144
	ds_read_b128 v[188:191], v141 offset:7168
	global_load_lds_dwordx4 v66, s[0:1]
	v_add_u32_e32 v66, s48, v136
	s_add_i32 m0, s21, 0xe000
	s_nop 0
	global_load_lds_dwordx4 v66, s[0:1]
	s_waitcnt lgkmcnt(8)
	s_barrier
	s_waitcnt lgkmcnt(0)
	s_setprio 1

	v_mfma_scale_f32_16x16x128_f8f6f4 v[122:125], v[144:151], v[160:167], v[122:125], v142, v142 op_sel_hi:[0,0,0]
	v_mfma_scale_f32_16x16x128_f8f6f4 v[126:129], v[152:159], v[160:167], v[126:129], v142, v142 op_sel_hi:[0,0,0]
	v_mfma_scale_f32_16x16x128_f8f6f4 v[192:195], v[144:151], v[168:175], v[110:113], v142, v142 op_sel_hi:[0,0,0]
	v_mfma_scale_f32_16x16x128_f8f6f4 v[196:199], v[152:159], v[168:175], v[106:109], v142, v142 op_sel_hi:[0,0,0]
	v_mfma_scale_f32_16x16x128_f8f6f4 v[200:203], v[144:151], v[176:183], v[94:97], v142, v142 op_sel_hi:[0,0,0]
	v_mfma_scale_f32_16x16x128_f8f6f4 v[204:207], v[152:159], v[176:183], v[90:93], v142, v142 op_sel_hi:[0,0,0]
	v_mfma_scale_f32_16x16x128_f8f6f4 v[208:211], v[144:151], v[184:191], v[78:81], v142, v142 op_sel_hi:[0,0,0]
	v_mfma_scale_f32_16x16x128_f8f6f4 v[212:215], v[152:159], v[184:191], v[74:77], v142, v142 op_sel_hi:[0,0,0]
	s_setprio 0
	s_barrier
	v_add_u32_e32 v66, s38, v138
	s_add_i32 s17, s37, s20
	s_nop 2
	ds_read_b128 v[74:77], v66
	ds_read_b128 v[78:81], v66 offset:1024
	ds_read_b128 v[90:93], v66 offset:2048
	ds_read_b128 v[94:97], v66 offset:3072
	v_add_u32_e32 v66, s16, v1
	s_mov_b32 m0, s17
	s_nop 0
	global_load_lds_dwordx4 v66, s[2:3]
	v_add_u32_e32 v66, s16, v132
	s_add_i32 m0, s17, 0x2000
	s_nop 0
	global_load_lds_dwordx4 v66, s[2:3]
	s_barrier
	s_waitcnt lgkmcnt(0)
	s_setprio 1

	v_mfma_scale_f32_16x16x128_f8f6f4 v[118:121], v[74:81], v[160:167], v[118:121], v142, v142 op_sel_hi:[0,0,0]
	v_mfma_scale_f32_16x16x128_f8f6f4 v[114:117], v[90:97], v[160:167], v[114:117], v142, v142 op_sel_hi:[0,0,0]
	v_mfma_scale_f32_16x16x128_f8f6f4 v[160:163], v[74:81], v[168:175], v[102:105], v142, v142 op_sel_hi:[0,0,0]
	v_mfma_scale_f32_16x16x128_f8f6f4 v[164:167], v[90:97], v[168:175], v[98:101], v142, v142 op_sel_hi:[0,0,0]
	v_mfma_scale_f32_16x16x128_f8f6f4 v[168:171], v[74:81], v[176:183], v[86:89], v142, v142 op_sel_hi:[0,0,0]
	v_mfma_scale_f32_16x16x128_f8f6f4 v[172:175], v[90:97], v[176:183], v[82:85], v142, v142 op_sel_hi:[0,0,0]
	v_mfma_scale_f32_16x16x128_f8f6f4 v[176:179], v[74:81], v[184:191], v[70:73], v142, v142 op_sel_hi:[0,0,0]
	v_mfma_scale_f32_16x16x128_f8f6f4 v[180:183], v[90:97], v[184:191], v[10:13], v142, v142 op_sel_hi:[0,0,0]
	s_setprio 0
	s_mov_b32 m0, s21
	s_nop 4
	v_add_u32_e32 v10, s52, v133
	s_barrier
	ds_read_b128 v[66:69], v141 offset:16384
	ds_read_b128 v[70:73], v141 offset:17408
	ds_read_b128 v[82:85], v141 offset:18432
	ds_read_b128 v[86:89], v141 offset:19456
	ds_read_b128 v[98:101], v141 offset:20480
	ds_read_b128 v[102:105], v141 offset:21504
	ds_read_b128 v[106:109], v141 offset:22528
	ds_read_b128 v[110:113], v141 offset:23552
	global_load_lds_dwordx4 v10, s[0:1]
	v_add_u32_e32 v10, s52, v134
	s_mov_b32 m0, s22
	s_nop 0
	global_load_lds_dwordx4 v10, s[0:1]
	s_barrier
	s_waitcnt lgkmcnt(0)
	s_setprio 1

	v_mfma_scale_f32_16x16x128_f8f6f4 v[62:65], v[144:151], v[66:73], v[62:65], v142, v142 op_sel_hi:[0,0,0]
	v_mfma_scale_f32_16x16x128_f8f6f4 v[58:61], v[152:159], v[66:73], v[58:61], v142, v142 op_sel_hi:[0,0,0]
	v_mfma_scale_f32_16x16x128_f8f6f4 v[228:231], v[152:159], v[106:113], v[228:231], v142, v142 op_sel_hi:[0,0,0]
	v_mfma_scale_f32_16x16x128_f8f6f4 v[184:187], v[144:151], v[82:89], v[46:49], v142, v142 op_sel_hi:[0,0,0]
	v_mfma_scale_f32_16x16x128_f8f6f4 v[188:191], v[152:159], v[82:89], v[42:45], v142, v142 op_sel_hi:[0,0,0]
	v_mfma_scale_f32_16x16x128_f8f6f4 v[216:219], v[144:151], v[98:105], v[30:33], v142, v142 op_sel_hi:[0,0,0]
	v_mfma_scale_f32_16x16x128_f8f6f4 v[220:223], v[152:159], v[98:105], v[26:29], v142, v142 op_sel_hi:[0,0,0]
	v_mfma_scale_f32_16x16x128_f8f6f4 v[224:227], v[144:151], v[106:113], v[14:17], v142, v142 op_sel_hi:[0,0,0]
	s_setprio 0
	s_barrier
	s_add_i32 s17, s16, 0x1000
	s_add_i32 s53, s38, s20
	v_add_u32_e32 v10, s17, v1
	s_mov_b32 m0, s53
	s_nop 0
	global_load_lds_dwordx4 v10, s[2:3]
	v_add_u32_e32 v10, s17, v132
	s_add_i32 m0, s53, 0x2000
	s_nop 0
	global_load_lds_dwordx4 v10, s[2:3]
	s_waitcnt vmcnt(6)
	s_barrier
	s_setprio 1
	v_mfma_scale_f32_16x16x128_f8f6f4 v[54:57], v[74:81], v[66:73], v[54:57], v142, v142 op_sel_hi:[0,0,0]
	v_mfma_scale_f32_16x16x128_f8f6f4 v[50:53], v[90:97], v[66:73], v[50:53], v142, v142 op_sel_hi:[0,0,0]
	v_mfma_scale_f32_16x16x128_f8f6f4 v[232:235], v[74:81], v[82:89], v[38:41], v142, v142 op_sel_hi:[0,0,0]
	v_mfma_scale_f32_16x16x128_f8f6f4 v[236:239], v[90:97], v[82:89], v[34:37], v142, v142 op_sel_hi:[0,0,0]
	v_mfma_scale_f32_16x16x128_f8f6f4 v[240:243], v[74:81], v[98:105], v[22:25], v142, v142 op_sel_hi:[0,0,0]
	v_mfma_scale_f32_16x16x128_f8f6f4 v[244:247], v[90:97], v[98:105], v[18:21], v142, v142 op_sel_hi:[0,0,0]
	v_mfma_scale_f32_16x16x128_f8f6f4 v[248:251], v[74:81], v[106:113], v[6:9], v142, v142 op_sel_hi:[0,0,0]
	v_mfma_scale_f32_16x16x128_f8f6f4 v[66:69], v[90:97], v[106:113], v[2:5], v142, v142 op_sel_hi:[0,0,0]
	s_setprio 0
	s_add_i32 s17, 0, 0x18000
	v_add_u32_e32 v10, s17, v138
	s_barrier
	s_nop 2
	ds_read_b128 v[2:5], v10
	ds_read_b128 v[6:9], v10 offset:1024
	ds_read_b128 v[18:21], v10 offset:2048
	ds_read_b128 v[22:25], v10 offset:3072
	s_mov_b32 m0, s23
	v_add_u32_e32 v70, s52, v135
	ds_read_b128 v[10:13], v141 offset:32768
	ds_read_b128 v[14:17], v141 offset:33792
	ds_read_b128 v[26:29], v141 offset:34816
	ds_read_b128 v[30:33], v141 offset:35840
	ds_read_b128 v[34:37], v141 offset:36864
	ds_read_b128 v[38:41], v141 offset:37888
	ds_read_b128 v[42:45], v141 offset:38912
	ds_read_b128 v[46:49], v141 offset:39936
	global_load_lds_dwordx4 v70, s[0:1]
	v_add_u32_e32 v70, s52, v136
	s_mov_b32 m0, s24
	s_nop 0
	global_load_lds_dwordx4 v70, s[0:1]
	s_waitcnt lgkmcnt(8)
	s_barrier
	s_waitcnt lgkmcnt(0)
	s_setprio 1

	v_mfma_scale_f32_16x16x128_f8f6f4 v[122:125], v[2:9], v[10:17], v[122:125], v142, v142 op_sel_hi:[0,0,0]
	v_mfma_scale_f32_16x16x128_f8f6f4 v[126:129], v[18:25], v[10:17], v[126:129], v142, v142 op_sel_hi:[0,0,0]
	v_mfma_scale_f32_16x16x128_f8f6f4 v[110:113], v[2:9], v[26:33], v[192:195], v142, v142 op_sel_hi:[0,0,0]
	v_mfma_scale_f32_16x16x128_f8f6f4 v[106:109], v[18:25], v[26:33], v[196:199], v142, v142 op_sel_hi:[0,0,0]
	v_mfma_scale_f32_16x16x128_f8f6f4 v[94:97], v[2:9], v[34:41], v[200:203], v142, v142 op_sel_hi:[0,0,0]
	v_mfma_scale_f32_16x16x128_f8f6f4 v[90:93], v[18:25], v[34:41], v[204:207], v142, v142 op_sel_hi:[0,0,0]
	v_mfma_scale_f32_16x16x128_f8f6f4 v[78:81], v[2:9], v[42:49], v[208:211], v142, v142 op_sel_hi:[0,0,0]
	v_mfma_scale_f32_16x16x128_f8f6f4 v[74:77], v[18:25], v[42:49], v[212:215], v142, v142 op_sel_hi:[0,0,0]
	s_setprio 0
	s_barrier
	s_add_i32 s52, 0, 0x1c000
	v_add_u32_e32 v70, s52, v138
	s_add_i32 s53, s16, 0x80
	s_add_i32 s17, s17, s20
	ds_read_b128 v[144:147], v70
	ds_read_b128 v[148:151], v70 offset:1024
	ds_read_b128 v[152:155], v70 offset:2048
	ds_read_b128 v[156:159], v70 offset:3072
	v_add_u32_e32 v70, s53, v1
	s_mov_b32 m0, s17
	s_nop 0
	global_load_lds_dwordx4 v70, s[2:3]
	v_add_u32_e32 v70, s53, v132
	s_add_i32 m0, s17, 0x2000
	s_nop 0
	global_load_lds_dwordx4 v70, s[2:3]
	s_barrier
	s_waitcnt lgkmcnt(0)
	s_setprio 1

	v_mfma_scale_f32_16x16x128_f8f6f4 v[118:121], v[144:151], v[10:17], v[118:121], v142, v142 op_sel_hi:[0,0,0]
	v_mfma_scale_f32_16x16x128_f8f6f4 v[114:117], v[152:159], v[10:17], v[114:117], v142, v142 op_sel_hi:[0,0,0]
	v_mfma_scale_f32_16x16x128_f8f6f4 v[102:105], v[144:151], v[26:33], v[160:163], v142, v142 op_sel_hi:[0,0,0]
	v_mfma_scale_f32_16x16x128_f8f6f4 v[98:101], v[152:159], v[26:33], v[164:167], v142, v142 op_sel_hi:[0,0,0]
	v_mfma_scale_f32_16x16x128_f8f6f4 v[86:89], v[144:151], v[34:41], v[168:171], v142, v142 op_sel_hi:[0,0,0]
	v_mfma_scale_f32_16x16x128_f8f6f4 v[82:85], v[152:159], v[34:41], v[172:175], v142, v142 op_sel_hi:[0,0,0]
	v_mfma_scale_f32_16x16x128_f8f6f4 v[70:73], v[144:151], v[42:49], v[176:179], v142, v142 op_sel_hi:[0,0,0]
	v_mfma_scale_f32_16x16x128_f8f6f4 v[10:13], v[152:159], v[42:49], v[180:183], v142, v142 op_sel_hi:[0,0,0]
	s_setprio 0
	s_mov_b32 m0, s26
	v_add_u32_e32 v14, s51, v133
	s_barrier
	ds_read_b128 v[34:37], v141 offset:49152
	ds_read_b128 v[38:41], v141 offset:50176
	ds_read_b128 v[160:163], v141 offset:51200
	ds_read_b128 v[164:167], v141 offset:52224
	ds_read_b128 v[168:171], v141 offset:53248
	ds_read_b128 v[172:175], v141 offset:54272
	ds_read_b128 v[176:179], v141 offset:55296
	ds_read_b128 v[180:183], v141 offset:56320
	global_load_lds_dwordx4 v14, s[0:1]
	v_add_u32_e32 v14, s51, v134
	s_mov_b32 m0, s27
	s_nop 0
	global_load_lds_dwordx4 v14, s[0:1]
	s_barrier
	s_waitcnt lgkmcnt(0)
	s_setprio 1

	v_mfma_scale_f32_16x16x128_f8f6f4 v[62:65], v[2:9], v[34:41], v[62:65], v142, v142 op_sel_hi:[0,0,0]
	v_mfma_scale_f32_16x16x128_f8f6f4 v[58:61], v[18:25], v[34:41], v[58:61], v142, v142 op_sel_hi:[0,0,0]
	v_mfma_scale_f32_16x16x128_f8f6f4 v[46:49], v[2:9], v[160:167], v[184:187], v142, v142 op_sel_hi:[0,0,0]
	v_mfma_scale_f32_16x16x128_f8f6f4 v[42:45], v[18:25], v[160:167], v[188:191], v142, v142 op_sel_hi:[0,0,0]
	v_mfma_scale_f32_16x16x128_f8f6f4 v[30:33], v[2:9], v[168:175], v[216:219], v142, v142 op_sel_hi:[0,0,0]
	v_mfma_scale_f32_16x16x128_f8f6f4 v[26:29], v[18:25], v[168:175], v[220:223], v142, v142 op_sel_hi:[0,0,0]
	v_mfma_scale_f32_16x16x128_f8f6f4 v[14:17], v[2:9], v[176:183], v[224:227], v142, v142 op_sel_hi:[0,0,0]
	v_mfma_scale_f32_16x16x128_f8f6f4 v[228:231], v[18:25], v[176:183], v[228:231], v142, v142 op_sel_hi:[0,0,0]
	s_setprio 0
	s_barrier
	s_addk_i32 s16, 0x1080
	s_add_i32 s17, s52, s20
	v_add_u32_e32 v2, s16, v1
	s_mov_b32 m0, s17
	s_nop 0
	global_load_lds_dwordx4 v2, s[2:3]
	v_add_u32_e32 v2, s16, v132
	s_add_i32 m0, s17, 0x2000
	s_nop 0
	global_load_lds_dwordx4 v2, s[2:3]
	s_waitcnt vmcnt(6)
	s_barrier
	s_setprio 1
	v_mfma_scale_f32_16x16x128_f8f6f4 v[54:57], v[144:151], v[34:41], v[54:57], v142, v142 op_sel_hi:[0,0,0]
	v_mfma_scale_f32_16x16x128_f8f6f4 v[50:53], v[152:159], v[34:41], v[50:53], v142, v142 op_sel_hi:[0,0,0]
	v_mfma_scale_f32_16x16x128_f8f6f4 v[38:41], v[144:151], v[160:167], v[232:235], v142, v142 op_sel_hi:[0,0,0]
	v_mfma_scale_f32_16x16x128_f8f6f4 v[34:37], v[152:159], v[160:167], v[236:239], v142, v142 op_sel_hi:[0,0,0]
	v_mfma_scale_f32_16x16x128_f8f6f4 v[22:25], v[144:151], v[168:175], v[240:243], v142, v142 op_sel_hi:[0,0,0]
	v_mfma_scale_f32_16x16x128_f8f6f4 v[18:21], v[152:159], v[168:175], v[244:247], v142, v142 op_sel_hi:[0,0,0]
	v_mfma_scale_f32_16x16x128_f8f6f4 v[6:9], v[144:151], v[176:183], v[248:251], v142, v142 op_sel_hi:[0,0,0]
	v_mfma_scale_f32_16x16x128_f8f6f4 v[2:5], v[152:159], v[176:183], v[66:69], v142, v142 op_sel_hi:[0,0,0]
	s_setprio 0
	s_add_i32 s50, s50, 2
	s_addk_i32 s48, 0x100
	s_addk_i32 s49, 0x100
	s_cmp_ge_i32 s50, s28
	s_barrier
	s_cbranch_scc1 .LBB0_1937

.LBB0_2037:
	v_add_u32_e32 v66, s37, v138
	ds_read_b128 v[144:147], v66
	ds_read_b128 v[148:151], v66 offset:1024
	ds_read_b128 v[152:155], v66 offset:2048
	ds_read_b128 v[156:159], v66 offset:3072
	s_add_i32 s51, s48, 0x80
	s_and_b64 s[52:53], s[16:17], exec
	s_cselect_b32 s52, s46, s51
	s_add_i32 s51, s52, 0x80
	s_and_b64 s[16:17], s[16:17], exec
	s_cselect_b32 s16, s47, s49
	v_add_u32_e32 v66, s48, v135
	s_add_i32 m0, s21, 0xc000
	ds_read_b128 v[160:163], v141
	ds_read_b128 v[164:167], v141 offset:1024
	ds_read_b128 v[168:171], v141 offset:2048
	ds_read_b128 v[172:175], v141 offset:3072
	ds_read_b128 v[176:179], v141 offset:4096
	ds_read_b128 v[180:183], v141 offset:5120
	ds_read_b128 v[184:187], v141 offset:6144
	ds_read_b128 v[188:191], v141 offset:7168
	global_load_lds_dwordx4 v66, s[0:1]
	v_add_u32_e32 v66, s48, v136
	s_add_i32 m0, s21, 0xe000
	s_nop 0
	global_load_lds_dwordx4 v66, s[0:1]
	s_waitcnt lgkmcnt(8)
	s_barrier
	s_waitcnt lgkmcnt(0)
	s_setprio 1

	v_mfma_scale_f32_16x16x128_f8f6f4 v[122:125], v[144:151], v[160:167], v[122:125], v142, v142 op_sel_hi:[0,0,0]
	v_mfma_scale_f32_16x16x128_f8f6f4 v[126:129], v[152:159], v[160:167], v[126:129], v142, v142 op_sel_hi:[0,0,0]
	v_mfma_scale_f32_16x16x128_f8f6f4 v[192:195], v[144:151], v[168:175], v[110:113], v142, v142 op_sel_hi:[0,0,0]
	v_mfma_scale_f32_16x16x128_f8f6f4 v[196:199], v[152:159], v[168:175], v[106:109], v142, v142 op_sel_hi:[0,0,0]
	v_mfma_scale_f32_16x16x128_f8f6f4 v[200:203], v[144:151], v[176:183], v[94:97], v142, v142 op_sel_hi:[0,0,0]
	v_mfma_scale_f32_16x16x128_f8f6f4 v[204:207], v[152:159], v[176:183], v[90:93], v142, v142 op_sel_hi:[0,0,0]
	v_mfma_scale_f32_16x16x128_f8f6f4 v[208:211], v[144:151], v[184:191], v[78:81], v142, v142 op_sel_hi:[0,0,0]
	v_mfma_scale_f32_16x16x128_f8f6f4 v[212:215], v[152:159], v[184:191], v[74:77], v142, v142 op_sel_hi:[0,0,0]
	s_setprio 0
	s_barrier
	v_add_u32_e32 v66, s38, v138
	s_add_i32 s17, s37, s20
	s_nop 2
	ds_read_b128 v[74:77], v66
	ds_read_b128 v[78:81], v66 offset:1024
	ds_read_b128 v[90:93], v66 offset:2048
	ds_read_b128 v[94:97], v66 offset:3072
	v_add_u32_e32 v66, s16, v1
	s_mov_b32 m0, s17
	s_nop 0
	global_load_lds_dwordx4 v66, s[2:3]
	v_add_u32_e32 v66, s16, v132
	s_add_i32 m0, s17, 0x2000
	s_nop 0
	global_load_lds_dwordx4 v66, s[2:3]
	s_barrier
	s_waitcnt lgkmcnt(0)
	s_setprio 1

	v_mfma_scale_f32_16x16x128_f8f6f4 v[118:121], v[74:81], v[160:167], v[118:121], v142, v142 op_sel_hi:[0,0,0]
	v_mfma_scale_f32_16x16x128_f8f6f4 v[114:117], v[90:97], v[160:167], v[114:117], v142, v142 op_sel_hi:[0,0,0]
	v_mfma_scale_f32_16x16x128_f8f6f4 v[160:163], v[74:81], v[168:175], v[102:105], v142, v142 op_sel_hi:[0,0,0]
	v_mfma_scale_f32_16x16x128_f8f6f4 v[164:167], v[90:97], v[168:175], v[98:101], v142, v142 op_sel_hi:[0,0,0]
	v_mfma_scale_f32_16x16x128_f8f6f4 v[168:171], v[74:81], v[176:183], v[86:89], v142, v142 op_sel_hi:[0,0,0]
	v_mfma_scale_f32_16x16x128_f8f6f4 v[172:175], v[90:97], v[176:183], v[82:85], v142, v142 op_sel_hi:[0,0,0]
	v_mfma_scale_f32_16x16x128_f8f6f4 v[176:179], v[74:81], v[184:191], v[70:73], v142, v142 op_sel_hi:[0,0,0]
	v_mfma_scale_f32_16x16x128_f8f6f4 v[180:183], v[90:97], v[184:191], v[10:13], v142, v142 op_sel_hi:[0,0,0]
	s_setprio 0
	s_mov_b32 m0, s21
	s_nop 4
	v_add_u32_e32 v10, s52, v133
	s_barrier
	ds_read_b128 v[66:69], v141 offset:16384
	ds_read_b128 v[70:73], v141 offset:17408
	ds_read_b128 v[82:85], v141 offset:18432
	ds_read_b128 v[86:89], v141 offset:19456
	ds_read_b128 v[98:101], v141 offset:20480
	ds_read_b128 v[102:105], v141 offset:21504
	ds_read_b128 v[106:109], v141 offset:22528
	ds_read_b128 v[110:113], v141 offset:23552
	global_load_lds_dwordx4 v10, s[0:1]
	v_add_u32_e32 v10, s52, v134
	s_mov_b32 m0, s22
	s_nop 0
	global_load_lds_dwordx4 v10, s[0:1]
	s_barrier
	s_waitcnt lgkmcnt(0)
	s_setprio 1

	v_mfma_scale_f32_16x16x128_f8f6f4 v[62:65], v[144:151], v[66:73], v[62:65], v142, v142 op_sel_hi:[0,0,0]
	v_mfma_scale_f32_16x16x128_f8f6f4 v[58:61], v[152:159], v[66:73], v[58:61], v142, v142 op_sel_hi:[0,0,0]
	v_mfma_scale_f32_16x16x128_f8f6f4 v[228:231], v[152:159], v[106:113], v[228:231], v142, v142 op_sel_hi:[0,0,0]
	v_mfma_scale_f32_16x16x128_f8f6f4 v[184:187], v[144:151], v[82:89], v[46:49], v142, v142 op_sel_hi:[0,0,0]
	v_mfma_scale_f32_16x16x128_f8f6f4 v[188:191], v[152:159], v[82:89], v[42:45], v142, v142 op_sel_hi:[0,0,0]
	v_mfma_scale_f32_16x16x128_f8f6f4 v[216:219], v[144:151], v[98:105], v[30:33], v142, v142 op_sel_hi:[0,0,0]
	v_mfma_scale_f32_16x16x128_f8f6f4 v[220:223], v[152:159], v[98:105], v[26:29], v142, v142 op_sel_hi:[0,0,0]
	v_mfma_scale_f32_16x16x128_f8f6f4 v[224:227], v[144:151], v[106:113], v[14:17], v142, v142 op_sel_hi:[0,0,0]
	s_setprio 0
	s_barrier
	s_add_i32 s17, s16, 0x1000
	s_add_i32 s53, s38, s20
	v_add_u32_e32 v10, s17, v1
	s_mov_b32 m0, s53
	s_nop 0
	global_load_lds_dwordx4 v10, s[2:3]
	v_add_u32_e32 v10, s17, v132
	s_add_i32 m0, s53, 0x2000
	s_nop 0
	global_load_lds_dwordx4 v10, s[2:3]
	s_waitcnt vmcnt(6)
	s_barrier
	s_setprio 1
	v_mfma_scale_f32_16x16x128_f8f6f4 v[54:57], v[74:81], v[66:73], v[54:57], v142, v142 op_sel_hi:[0,0,0]
	v_mfma_scale_f32_16x16x128_f8f6f4 v[50:53], v[90:97], v[66:73], v[50:53], v142, v142 op_sel_hi:[0,0,0]
	v_mfma_scale_f32_16x16x128_f8f6f4 v[232:235], v[74:81], v[82:89], v[38:41], v142, v142 op_sel_hi:[0,0,0]
	v_mfma_scale_f32_16x16x128_f8f6f4 v[236:239], v[90:97], v[82:89], v[34:37], v142, v142 op_sel_hi:[0,0,0]
	v_mfma_scale_f32_16x16x128_f8f6f4 v[240:243], v[74:81], v[98:105], v[22:25], v142, v142 op_sel_hi:[0,0,0]
	v_mfma_scale_f32_16x16x128_f8f6f4 v[244:247], v[90:97], v[98:105], v[18:21], v142, v142 op_sel_hi:[0,0,0]
	v_mfma_scale_f32_16x16x128_f8f6f4 v[248:251], v[74:81], v[106:113], v[6:9], v142, v142 op_sel_hi:[0,0,0]
	v_mfma_scale_f32_16x16x128_f8f6f4 v[66:69], v[90:97], v[106:113], v[2:5], v142, v142 op_sel_hi:[0,0,0]
	s_setprio 0
	s_add_i32 s17, 0, 0x18000
	v_add_u32_e32 v10, s17, v138
	s_barrier
	s_nop 2
	ds_read_b128 v[2:5], v10
	ds_read_b128 v[6:9], v10 offset:1024
	ds_read_b128 v[18:21], v10 offset:2048
	ds_read_b128 v[22:25], v10 offset:3072
	s_mov_b32 m0, s23
	v_add_u32_e32 v70, s52, v135
	ds_read_b128 v[10:13], v141 offset:32768
	ds_read_b128 v[14:17], v141 offset:33792
	ds_read_b128 v[26:29], v141 offset:34816
	ds_read_b128 v[30:33], v141 offset:35840
	ds_read_b128 v[34:37], v141 offset:36864
	ds_read_b128 v[38:41], v141 offset:37888
	ds_read_b128 v[42:45], v141 offset:38912
	ds_read_b128 v[46:49], v141 offset:39936
	global_load_lds_dwordx4 v70, s[0:1]
	v_add_u32_e32 v70, s52, v136
	s_mov_b32 m0, s24
	s_nop 0
	global_load_lds_dwordx4 v70, s[0:1]
	s_waitcnt lgkmcnt(8)
	s_barrier
	s_waitcnt lgkmcnt(0)
	s_setprio 1

	v_mfma_scale_f32_16x16x128_f8f6f4 v[122:125], v[2:9], v[10:17], v[122:125], v142, v142 op_sel_hi:[0,0,0]
	v_mfma_scale_f32_16x16x128_f8f6f4 v[126:129], v[18:25], v[10:17], v[126:129], v142, v142 op_sel_hi:[0,0,0]
	v_mfma_scale_f32_16x16x128_f8f6f4 v[110:113], v[2:9], v[26:33], v[192:195], v142, v142 op_sel_hi:[0,0,0]
	v_mfma_scale_f32_16x16x128_f8f6f4 v[106:109], v[18:25], v[26:33], v[196:199], v142, v142 op_sel_hi:[0,0,0]
	v_mfma_scale_f32_16x16x128_f8f6f4 v[94:97], v[2:9], v[34:41], v[200:203], v142, v142 op_sel_hi:[0,0,0]
	v_mfma_scale_f32_16x16x128_f8f6f4 v[90:93], v[18:25], v[34:41], v[204:207], v142, v142 op_sel_hi:[0,0,0]
	v_mfma_scale_f32_16x16x128_f8f6f4 v[78:81], v[2:9], v[42:49], v[208:211], v142, v142 op_sel_hi:[0,0,0]
	v_mfma_scale_f32_16x16x128_f8f6f4 v[74:77], v[18:25], v[42:49], v[212:215], v142, v142 op_sel_hi:[0,0,0]
	s_setprio 0
	s_barrier
	s_add_i32 s52, 0, 0x1c000
	v_add_u32_e32 v70, s52, v138
	s_add_i32 s53, s16, 0x80
	s_add_i32 s17, s17, s20
	ds_read_b128 v[144:147], v70
	ds_read_b128 v[148:151], v70 offset:1024
	ds_read_b128 v[152:155], v70 offset:2048
	ds_read_b128 v[156:159], v70 offset:3072
	v_add_u32_e32 v70, s53, v1
	s_mov_b32 m0, s17
	s_nop 0
	global_load_lds_dwordx4 v70, s[2:3]
	v_add_u32_e32 v70, s53, v132
	s_add_i32 m0, s17, 0x2000
	s_nop 0
	global_load_lds_dwordx4 v70, s[2:3]
	s_barrier
	s_waitcnt lgkmcnt(0)
	s_setprio 1

	v_mfma_scale_f32_16x16x128_f8f6f4 v[118:121], v[144:151], v[10:17], v[118:121], v142, v142 op_sel_hi:[0,0,0]
	v_mfma_scale_f32_16x16x128_f8f6f4 v[114:117], v[152:159], v[10:17], v[114:117], v142, v142 op_sel_hi:[0,0,0]
	v_mfma_scale_f32_16x16x128_f8f6f4 v[102:105], v[144:151], v[26:33], v[160:163], v142, v142 op_sel_hi:[0,0,0]
	v_mfma_scale_f32_16x16x128_f8f6f4 v[98:101], v[152:159], v[26:33], v[164:167], v142, v142 op_sel_hi:[0,0,0]
	v_mfma_scale_f32_16x16x128_f8f6f4 v[86:89], v[144:151], v[34:41], v[168:171], v142, v142 op_sel_hi:[0,0,0]
	v_mfma_scale_f32_16x16x128_f8f6f4 v[82:85], v[152:159], v[34:41], v[172:175], v142, v142 op_sel_hi:[0,0,0]
	v_mfma_scale_f32_16x16x128_f8f6f4 v[70:73], v[144:151], v[42:49], v[176:179], v142, v142 op_sel_hi:[0,0,0]
	v_mfma_scale_f32_16x16x128_f8f6f4 v[10:13], v[152:159], v[42:49], v[180:183], v142, v142 op_sel_hi:[0,0,0]
	s_setprio 0
	s_mov_b32 m0, s26
	v_add_u32_e32 v14, s51, v133
	s_barrier
	ds_read_b128 v[34:37], v141 offset:49152
	ds_read_b128 v[38:41], v141 offset:50176
	ds_read_b128 v[160:163], v141 offset:51200
	ds_read_b128 v[164:167], v141 offset:52224
	ds_read_b128 v[168:171], v141 offset:53248
	ds_read_b128 v[172:175], v141 offset:54272
	ds_read_b128 v[176:179], v141 offset:55296
	ds_read_b128 v[180:183], v141 offset:56320
	global_load_lds_dwordx4 v14, s[0:1]
	v_add_u32_e32 v14, s51, v134
	s_mov_b32 m0, s27
	s_nop 0
	global_load_lds_dwordx4 v14, s[0:1]
	s_barrier
	s_waitcnt lgkmcnt(0)
	s_setprio 1

	v_mfma_scale_f32_16x16x128_f8f6f4 v[62:65], v[2:9], v[34:41], v[62:65], v142, v142 op_sel_hi:[0,0,0]
	v_mfma_scale_f32_16x16x128_f8f6f4 v[58:61], v[18:25], v[34:41], v[58:61], v142, v142 op_sel_hi:[0,0,0]
	v_mfma_scale_f32_16x16x128_f8f6f4 v[46:49], v[2:9], v[160:167], v[184:187], v142, v142 op_sel_hi:[0,0,0]
	v_mfma_scale_f32_16x16x128_f8f6f4 v[42:45], v[18:25], v[160:167], v[188:191], v142, v142 op_sel_hi:[0,0,0]
	v_mfma_scale_f32_16x16x128_f8f6f4 v[30:33], v[2:9], v[168:175], v[216:219], v142, v142 op_sel_hi:[0,0,0]
	v_mfma_scale_f32_16x16x128_f8f6f4 v[26:29], v[18:25], v[168:175], v[220:223], v142, v142 op_sel_hi:[0,0,0]
	v_mfma_scale_f32_16x16x128_f8f6f4 v[14:17], v[2:9], v[176:183], v[224:227], v142, v142 op_sel_hi:[0,0,0]
	v_mfma_scale_f32_16x16x128_f8f6f4 v[228:231], v[18:25], v[176:183], v[228:231], v142, v142 op_sel_hi:[0,0,0]
	s_setprio 0
	s_barrier
	s_addk_i32 s16, 0x1080
	s_add_i32 s17, s52, s20
	v_add_u32_e32 v2, s16, v1
	s_mov_b32 m0, s17
	s_nop 0
	global_load_lds_dwordx4 v2, s[2:3]
	v_add_u32_e32 v2, s16, v132
	s_add_i32 m0, s17, 0x2000
	s_nop 0
	global_load_lds_dwordx4 v2, s[2:3]
	s_waitcnt vmcnt(6)
	s_barrier
	s_setprio 1
	v_mfma_scale_f32_16x16x128_f8f6f4 v[54:57], v[144:151], v[34:41], v[54:57], v142, v142 op_sel_hi:[0,0,0]
	v_mfma_scale_f32_16x16x128_f8f6f4 v[50:53], v[152:159], v[34:41], v[50:53], v142, v142 op_sel_hi:[0,0,0]
	v_mfma_scale_f32_16x16x128_f8f6f4 v[38:41], v[144:151], v[160:167], v[232:235], v142, v142 op_sel_hi:[0,0,0]
	v_mfma_scale_f32_16x16x128_f8f6f4 v[34:37], v[152:159], v[160:167], v[236:239], v142, v142 op_sel_hi:[0,0,0]
	v_mfma_scale_f32_16x16x128_f8f6f4 v[22:25], v[144:151], v[168:175], v[240:243], v142, v142 op_sel_hi:[0,0,0]
	v_mfma_scale_f32_16x16x128_f8f6f4 v[18:21], v[152:159], v[168:175], v[244:247], v142, v142 op_sel_hi:[0,0,0]
	v_mfma_scale_f32_16x16x128_f8f6f4 v[6:9], v[144:151], v[176:183], v[248:251], v142, v142 op_sel_hi:[0,0,0]
	v_mfma_scale_f32_16x16x128_f8f6f4 v[2:5], v[152:159], v[176:183], v[66:69], v142, v142 op_sel_hi:[0,0,0]
	s_setprio 0
	s_add_i32 s50, s50, 2
	s_addk_i32 s48, 0x100
	s_addk_i32 s49, 0x100
	s_cmp_ge_i32 s50, s28
	s_barrier
	s_cbranch_scc1 .LBB0_2027

.LBB0_2398:
	ds_read_b128 v[98:101], v212
	ds_read_b128 v[102:105], v212 offset:1024
	ds_read_b128 v[138:141], v212 offset:2048
	ds_read_b128 v[142:145], v212 offset:3072
	s_add_i32 s59, s56, 0x80
	s_cmp_eq_u32 s47, s58
	s_cselect_b32 s61, s34, s59
	s_cselect_b32 s59, s35, s57
	s_or_b32 s60, s61, 0x80
	v_add_u32_e32 v162, s56, v207
	s_add_i32 m0, s38, 0xc000
	ds_read_b128 v[146:149], v213
	ds_read_b128 v[150:153], v213 offset:1024
	ds_read_b128 v[154:157], v213 offset:2048
	ds_read_b128 v[158:161], v213 offset:3072
	ds_read_b128 v[170:173], v213 offset:4096
	ds_read_b128 v[174:177], v213 offset:5120
	ds_read_b128 v[178:181], v213 offset:6144
	ds_read_b128 v[182:185], v213 offset:7168
	global_load_lds_dwordx4 v162, s[4:5]
	v_add_u32_e32 v162, s56, v208
	s_add_i32 m0, s38, 0xe000
	s_nop 0
	global_load_lds_dwordx4 v162, s[4:5]
	s_waitcnt lgkmcnt(8)
	s_barrier
	s_waitcnt lgkmcnt(0)
	s_setprio 1

	v_mfma_scale_f32_16x16x128_f8f6f4 v[134:137], v[98:105], v[146:153], v[134:137], v214, v214 op_sel_hi:[0,0,0]
	v_mfma_scale_f32_16x16x128_f8f6f4 v[130:133], v[138:145], v[146:153], v[130:133], v214, v214 op_sel_hi:[0,0,0]
	v_mfma_scale_f32_16x16x128_f8f6f4 v[126:129], v[98:105], v[154:161], v[126:129], v214, v214 op_sel_hi:[0,0,0]
	v_mfma_scale_f32_16x16x128_f8f6f4 v[122:125], v[138:145], v[154:161], v[122:125], v214, v214 op_sel_hi:[0,0,0]
	v_mfma_scale_f32_16x16x128_f8f6f4 v[162:165], v[98:105], v[170:177], v[118:121], v214, v214 op_sel_hi:[0,0,0]
	v_mfma_scale_f32_16x16x128_f8f6f4 v[186:189], v[138:145], v[170:177], v[114:117], v214, v214 op_sel_hi:[0,0,0]
	v_mfma_scale_f32_16x16x128_f8f6f4 v[190:193], v[98:105], v[178:185], v[110:113], v214, v214 op_sel_hi:[0,0,0]
	v_mfma_scale_f32_16x16x128_f8f6f4 v[194:197], v[138:145], v[178:185], v[106:109], v214, v214 op_sel_hi:[0,0,0]
	s_setprio 0
	s_barrier
	s_add_i32 s62, s48, s36
	v_add_u32_e32 v198, s59, v1
	s_mov_b32 m0, s62
	s_nop 1
	ds_read_b128 v[106:109], v215
	ds_read_b128 v[110:113], v215 offset:1024
	ds_read_b128 v[114:117], v215 offset:2048
	ds_read_b128 v[118:121], v215 offset:3072
	global_load_lds_dwordx4 v198, s[6:7]
	v_add_u32_e32 v198, s59, v204
	s_add_i32 m0, s62, 0x2000
	s_nop 0
	global_load_lds_dwordx4 v198, s[6:7]
	s_barrier
	s_waitcnt lgkmcnt(0)
	s_setprio 1

	v_mfma_scale_f32_16x16x128_f8f6f4 v[198:201], v[106:113], v[146:153], v[62:65], v214, v214 op_sel_hi:[0,0,0]
	v_mfma_scale_f32_16x16x128_f8f6f4 v[146:149], v[114:121], v[146:153], v[58:61], v214, v214 op_sel_hi:[0,0,0]
	v_mfma_scale_f32_16x16x128_f8f6f4 v[150:153], v[106:113], v[154:161], v[54:57], v214, v214 op_sel_hi:[0,0,0]
	v_mfma_scale_f32_16x16x128_f8f6f4 v[154:157], v[114:121], v[154:161], v[50:53], v214, v214 op_sel_hi:[0,0,0]
	v_mfma_scale_f32_16x16x128_f8f6f4 v[158:161], v[106:113], v[170:177], v[46:49], v214, v214 op_sel_hi:[0,0,0]
	v_mfma_scale_f32_16x16x128_f8f6f4 v[170:173], v[114:121], v[170:177], v[42:45], v214, v214 op_sel_hi:[0,0,0]
	v_mfma_scale_f32_16x16x128_f8f6f4 v[174:177], v[106:113], v[178:185], v[38:41], v214, v214 op_sel_hi:[0,0,0]
	v_mfma_scale_f32_16x16x128_f8f6f4 v[178:181], v[114:121], v[178:185], v[34:37], v214, v214 op_sel_hi:[0,0,0]
	s_setprio 0
	s_mov_b32 m0, s38
	v_add_u32_e32 v182, s61, v205
	s_barrier
	s_nop 2
	ds_read_b128 v[34:37], v213 offset:16384
	ds_read_b128 v[38:41], v213 offset:17408
	ds_read_b128 v[42:45], v213 offset:18432
	ds_read_b128 v[46:49], v213 offset:19456
	ds_read_b128 v[50:53], v213 offset:20480
	ds_read_b128 v[54:57], v213 offset:21504
	ds_read_b128 v[58:61], v213 offset:22528
	ds_read_b128 v[62:65], v213 offset:23552
	global_load_lds_dwordx4 v182, s[4:5]
	v_add_u32_e32 v182, s61, v206
	s_mov_b32 m0, s39
	s_nop 0
	global_load_lds_dwordx4 v182, s[4:5]
	s_barrier
	s_waitcnt lgkmcnt(0)
	s_setprio 1

	v_mfma_scale_f32_16x16x128_f8f6f4 v[94:97], v[98:105], v[34:41], v[94:97], v214, v214 op_sel_hi:[0,0,0]
	v_mfma_scale_f32_16x16x128_f8f6f4 v[90:93], v[138:145], v[34:41], v[90:93], v214, v214 op_sel_hi:[0,0,0]
	v_mfma_scale_f32_16x16x128_f8f6f4 v[86:89], v[98:105], v[42:49], v[86:89], v214, v214 op_sel_hi:[0,0,0]
	v_mfma_scale_f32_16x16x128_f8f6f4 v[82:85], v[138:145], v[42:49], v[82:85], v214, v214 op_sel_hi:[0,0,0]
	v_mfma_scale_f32_16x16x128_f8f6f4 v[78:81], v[98:105], v[50:57], v[78:81], v214, v214 op_sel_hi:[0,0,0]
	v_mfma_scale_f32_16x16x128_f8f6f4 v[74:77], v[138:145], v[50:57], v[74:77], v214, v214 op_sel_hi:[0,0,0]
	v_mfma_scale_f32_16x16x128_f8f6f4 v[182:185], v[98:105], v[58:65], v[70:73], v214, v214 op_sel_hi:[0,0,0]
	v_mfma_scale_f32_16x16x128_f8f6f4 v[216:219], v[138:145], v[58:65], v[66:69], v214, v214 op_sel_hi:[0,0,0]
	s_setprio 0
	s_barrier
	s_add_i32 s62, s59, 0x40000
	s_add_i32 s63, s49, s36
	s_nop 2
	v_add_u32_e32 v66, s62, v1
	s_mov_b32 m0, s63
	s_nop 0
	global_load_lds_dwordx4 v66, s[6:7]
	v_add_u32_e32 v66, s62, v204
	s_add_i32 m0, s63, 0x2000
	s_nop 0
	global_load_lds_dwordx4 v66, s[6:7]
	s_waitcnt vmcnt(6)
	s_barrier
	s_setprio 1
	v_mfma_scale_f32_16x16x128_f8f6f4 v[220:223], v[106:113], v[34:41], v[30:33], v214, v214 op_sel_hi:[0,0,0]
	v_mfma_scale_f32_16x16x128_f8f6f4 v[224:227], v[114:121], v[34:41], v[26:29], v214, v214 op_sel_hi:[0,0,0]
	v_mfma_scale_f32_16x16x128_f8f6f4 v[228:231], v[106:113], v[42:49], v[22:25], v214, v214 op_sel_hi:[0,0,0]
	v_mfma_scale_f32_16x16x128_f8f6f4 v[232:235], v[114:121], v[42:49], v[18:21], v214, v214 op_sel_hi:[0,0,0]
	v_mfma_scale_f32_16x16x128_f8f6f4 v[236:239], v[106:113], v[50:57], v[14:17], v214, v214 op_sel_hi:[0,0,0]
	v_mfma_scale_f32_16x16x128_f8f6f4 v[240:243], v[114:121], v[50:57], v[10:13], v214, v214 op_sel_hi:[0,0,0]
	v_mfma_scale_f32_16x16x128_f8f6f4 v[244:247], v[106:113], v[58:65], v[6:9], v214, v214 op_sel_hi:[0,0,0]
	v_mfma_scale_f32_16x16x128_f8f6f4 v[248:251], v[114:121], v[58:65], v[2:5], v214, v214 op_sel_hi:[0,0,0]
	s_setprio 0
	s_add_i32 s62, 0, 0x18000
	s_nop 1
	v_add_u32_e32 v14, s62, v211
	s_barrier
	s_nop 0
	ds_read_b128 v[2:5], v14
	ds_read_b128 v[6:9], v14 offset:1024
	ds_read_b128 v[10:13], v14 offset:2048
	ds_read_b128 v[14:17], v14 offset:3072
	s_mov_b32 m0, s41
	v_add_u32_e32 v42, s61, v207
	ds_read_b128 v[18:21], v213 offset:32768
	ds_read_b128 v[22:25], v213 offset:33792
	ds_read_b128 v[26:29], v213 offset:34816
	ds_read_b128 v[30:33], v213 offset:35840
	ds_read_b128 v[34:37], v213 offset:36864
	ds_read_b128 v[38:41], v213 offset:37888
	ds_read_b128 v[66:69], v213 offset:38912
	ds_read_b128 v[70:73], v213 offset:39936
	global_load_lds_dwordx4 v42, s[4:5]
	v_add_u32_e32 v42, s61, v208
	s_mov_b32 m0, s42
	s_nop 0
	global_load_lds_dwordx4 v42, s[4:5]
	s_waitcnt lgkmcnt(8)
	s_barrier
	s_waitcnt lgkmcnt(0)
	s_setprio 1

	v_mfma_scale_f32_16x16x128_f8f6f4 v[134:137], v[2:9], v[18:25], v[134:137], v214, v214 op_sel_hi:[0,0,0]
	v_mfma_scale_f32_16x16x128_f8f6f4 v[130:133], v[10:17], v[18:25], v[130:133], v214, v214 op_sel_hi:[0,0,0]
	v_mfma_scale_f32_16x16x128_f8f6f4 v[126:129], v[2:9], v[26:33], v[126:129], v214, v214 op_sel_hi:[0,0,0]
	v_mfma_scale_f32_16x16x128_f8f6f4 v[122:125], v[10:17], v[26:33], v[122:125], v214, v214 op_sel_hi:[0,0,0]
	v_mfma_scale_f32_16x16x128_f8f6f4 v[118:121], v[2:9], v[34:41], v[162:165], v214, v214 op_sel_hi:[0,0,0]
	v_mfma_scale_f32_16x16x128_f8f6f4 v[114:117], v[10:17], v[34:41], v[186:189], v214, v214 op_sel_hi:[0,0,0]
	v_mfma_scale_f32_16x16x128_f8f6f4 v[110:113], v[2:9], v[66:73], v[190:193], v214, v214 op_sel_hi:[0,0,0]
	v_mfma_scale_f32_16x16x128_f8f6f4 v[106:109], v[10:17], v[66:73], v[194:197], v214, v214 op_sel_hi:[0,0,0]
	s_setprio 0
	s_barrier
	s_add_i32 s61, 0, 0x1c000
	v_add_u32_e32 v42, s61, v211
	s_or_b32 s63, s59, 0x80
	s_add_i32 s62, s62, s36
	ds_read_b128 v[98:101], v42
	ds_read_b128 v[102:105], v42 offset:1024
	ds_read_b128 v[138:141], v42 offset:2048
	ds_read_b128 v[142:145], v42 offset:3072
	v_add_u32_e32 v42, s63, v1
	s_mov_b32 m0, s62
	s_nop 0
	global_load_lds_dwordx4 v42, s[6:7]
	v_add_u32_e32 v42, s63, v204
	s_add_i32 m0, s62, 0x2000
	s_nop 0
	global_load_lds_dwordx4 v42, s[6:7]
	s_barrier
	s_waitcnt lgkmcnt(0)
	s_setprio 1

	v_mfma_scale_f32_16x16x128_f8f6f4 v[62:65], v[98:105], v[18:25], v[198:201], v214, v214 op_sel_hi:[0,0,0]
	v_mfma_scale_f32_16x16x128_f8f6f4 v[58:61], v[138:145], v[18:25], v[146:149], v214, v214 op_sel_hi:[0,0,0]
	v_mfma_scale_f32_16x16x128_f8f6f4 v[54:57], v[98:105], v[26:33], v[150:153], v214, v214 op_sel_hi:[0,0,0]
	v_mfma_scale_f32_16x16x128_f8f6f4 v[50:53], v[138:145], v[26:33], v[154:157], v214, v214 op_sel_hi:[0,0,0]
	v_mfma_scale_f32_16x16x128_f8f6f4 v[46:49], v[98:105], v[34:41], v[158:161], v214, v214 op_sel_hi:[0,0,0]
	v_mfma_scale_f32_16x16x128_f8f6f4 v[42:45], v[138:145], v[34:41], v[170:173], v214, v214 op_sel_hi:[0,0,0]
	v_mfma_scale_f32_16x16x128_f8f6f4 v[38:41], v[98:105], v[66:73], v[174:177], v214, v214 op_sel_hi:[0,0,0]
	v_mfma_scale_f32_16x16x128_f8f6f4 v[34:37], v[138:145], v[66:73], v[178:181], v214, v214 op_sel_hi:[0,0,0]
	s_setprio 0
	s_mov_b32 m0, s43
	v_add_u32_e32 v26, s60, v205
	s_barrier
	ds_read_b128 v[18:21], v213 offset:49152
	ds_read_b128 v[22:25], v213 offset:50176
	ds_read_b128 v[146:149], v213 offset:51200
	ds_read_b128 v[150:153], v213 offset:52224
	ds_read_b128 v[154:157], v213 offset:53248
	ds_read_b128 v[158:161], v213 offset:54272
	ds_read_b128 v[170:173], v213 offset:55296
	ds_read_b128 v[174:177], v213 offset:56320
	global_load_lds_dwordx4 v26, s[4:5]
	v_add_u32_e32 v26, s60, v206
	s_mov_b32 m0, s44
	s_nop 0
	global_load_lds_dwordx4 v26, s[4:5]
	s_barrier
	s_waitcnt lgkmcnt(0)
	s_setprio 1

	v_mfma_scale_f32_16x16x128_f8f6f4 v[94:97], v[2:9], v[18:25], v[94:97], v214, v214 op_sel_hi:[0,0,0]
	v_mfma_scale_f32_16x16x128_f8f6f4 v[90:93], v[10:17], v[18:25], v[90:93], v214, v214 op_sel_hi:[0,0,0]
	v_mfma_scale_f32_16x16x128_f8f6f4 v[86:89], v[2:9], v[146:153], v[86:89], v214, v214 op_sel_hi:[0,0,0]
	v_mfma_scale_f32_16x16x128_f8f6f4 v[82:85], v[10:17], v[146:153], v[82:85], v214, v214 op_sel_hi:[0,0,0]
	v_mfma_scale_f32_16x16x128_f8f6f4 v[78:81], v[2:9], v[154:161], v[78:81], v214, v214 op_sel_hi:[0,0,0]
	v_mfma_scale_f32_16x16x128_f8f6f4 v[74:77], v[10:17], v[154:161], v[74:77], v214, v214 op_sel_hi:[0,0,0]
	v_mfma_scale_f32_16x16x128_f8f6f4 v[70:73], v[2:9], v[170:177], v[182:185], v214, v214 op_sel_hi:[0,0,0]
	v_mfma_scale_f32_16x16x128_f8f6f4 v[66:69], v[10:17], v[170:177], v[216:219], v214, v214 op_sel_hi:[0,0,0]
	s_setprio 0
	s_barrier
	s_add_i32 s59, s59, 0x40080
	s_add_i32 s60, s61, s36
	v_add_u32_e32 v2, s59, v1
	s_mov_b32 m0, s60
	s_nop 0
	global_load_lds_dwordx4 v2, s[6:7]
	v_add_u32_e32 v2, s59, v204
	s_add_i32 m0, s60, 0x2000
	s_nop 0
	global_load_lds_dwordx4 v2, s[6:7]
	s_waitcnt vmcnt(6)
	s_barrier
	s_setprio 1
	v_mfma_scale_f32_16x16x128_f8f6f4 v[30:33], v[98:105], v[18:25], v[220:223], v214, v214 op_sel_hi:[0,0,0]
	v_mfma_scale_f32_16x16x128_f8f6f4 v[26:29], v[138:145], v[18:25], v[224:227], v214, v214 op_sel_hi:[0,0,0]
	v_mfma_scale_f32_16x16x128_f8f6f4 v[22:25], v[98:105], v[146:153], v[228:231], v214, v214 op_sel_hi:[0,0,0]
	v_mfma_scale_f32_16x16x128_f8f6f4 v[18:21], v[138:145], v[146:153], v[232:235], v214, v214 op_sel_hi:[0,0,0]
	v_mfma_scale_f32_16x16x128_f8f6f4 v[14:17], v[98:105], v[154:161], v[236:239], v214, v214 op_sel_hi:[0,0,0]
	v_mfma_scale_f32_16x16x128_f8f6f4 v[10:13], v[138:145], v[154:161], v[240:243], v214, v214 op_sel_hi:[0,0,0]
	v_mfma_scale_f32_16x16x128_f8f6f4 v[6:9], v[98:105], v[170:177], v[244:247], v214, v214 op_sel_hi:[0,0,0]
	v_mfma_scale_f32_16x16x128_f8f6f4 v[2:5], v[138:145], v[170:177], v[248:251], v214, v214 op_sel_hi:[0,0,0]
	s_setprio 0
	s_add_i32 s58, s58, 2
	s_addk_i32 s56, 0x100
	s_addk_i32 s57, 0x100
	s_cmp_ge_i32 s58, s45
	s_barrier
	s_cbranch_scc0 .LBB0_2398
	s_branch .LBB0_2393

.LBB0_2505:
	ds_read_b128 v[98:101], v212
	ds_read_b128 v[102:105], v212 offset:1024
	ds_read_b128 v[138:141], v212 offset:2048
	ds_read_b128 v[142:145], v212 offset:3072
	s_add_i32 s58, s55, 0x80
	s_cmp_eq_u32 s48, s57
	s_cselect_b32 s60, s2, s58
	s_cselect_b32 s58, s3, s56
	s_or_b32 s59, s60, 0x80
	v_add_u32_e32 v162, s55, v207
	s_add_i32 m0, s39, 0xc000
	ds_read_b128 v[146:149], v213
	ds_read_b128 v[150:153], v213 offset:1024
	ds_read_b128 v[154:157], v213 offset:2048
	ds_read_b128 v[158:161], v213 offset:3072
	ds_read_b128 v[170:173], v213 offset:4096
	ds_read_b128 v[174:177], v213 offset:5120
	ds_read_b128 v[178:181], v213 offset:6144
	ds_read_b128 v[182:185], v213 offset:7168
	global_load_lds_dwordx4 v162, s[4:5]
	v_add_u32_e32 v162, s55, v208
	s_add_i32 m0, s39, 0xe000
	s_nop 0
	global_load_lds_dwordx4 v162, s[4:5]
	s_waitcnt lgkmcnt(8)
	s_barrier
	s_waitcnt lgkmcnt(0)
	s_setprio 1

	v_mfma_scale_f32_16x16x128_f8f6f4 v[134:137], v[98:105], v[146:153], v[134:137], v214, v214 op_sel_hi:[0,0,0]
	v_mfma_scale_f32_16x16x128_f8f6f4 v[130:133], v[138:145], v[146:153], v[130:133], v214, v214 op_sel_hi:[0,0,0]
	v_mfma_scale_f32_16x16x128_f8f6f4 v[126:129], v[98:105], v[154:161], v[126:129], v214, v214 op_sel_hi:[0,0,0]
	v_mfma_scale_f32_16x16x128_f8f6f4 v[122:125], v[138:145], v[154:161], v[122:125], v214, v214 op_sel_hi:[0,0,0]
	v_mfma_scale_f32_16x16x128_f8f6f4 v[162:165], v[98:105], v[170:177], v[118:121], v214, v214 op_sel_hi:[0,0,0]
	v_mfma_scale_f32_16x16x128_f8f6f4 v[186:189], v[138:145], v[170:177], v[114:117], v214, v214 op_sel_hi:[0,0,0]
	v_mfma_scale_f32_16x16x128_f8f6f4 v[190:193], v[98:105], v[178:185], v[110:113], v214, v214 op_sel_hi:[0,0,0]
	v_mfma_scale_f32_16x16x128_f8f6f4 v[194:197], v[138:145], v[178:185], v[106:109], v214, v214 op_sel_hi:[0,0,0]
	s_setprio 0
	s_barrier
	s_add_i32 s61, s49, s38
	v_add_u32_e32 v198, s58, v1
	s_mov_b32 m0, s61
	s_nop 1
	ds_read_b128 v[106:109], v215
	ds_read_b128 v[110:113], v215 offset:1024
	ds_read_b128 v[114:117], v215 offset:2048
	ds_read_b128 v[118:121], v215 offset:3072
	global_load_lds_dwordx4 v198, s[6:7]
	v_add_u32_e32 v198, s58, v204
	s_add_i32 m0, s61, 0x2000
	s_nop 0
	global_load_lds_dwordx4 v198, s[6:7]
	s_barrier
	s_waitcnt lgkmcnt(0)
	s_setprio 1

	v_mfma_scale_f32_16x16x128_f8f6f4 v[198:201], v[106:113], v[146:153], v[62:65], v214, v214 op_sel_hi:[0,0,0]
	v_mfma_scale_f32_16x16x128_f8f6f4 v[146:149], v[114:121], v[146:153], v[58:61], v214, v214 op_sel_hi:[0,0,0]
	v_mfma_scale_f32_16x16x128_f8f6f4 v[150:153], v[106:113], v[154:161], v[54:57], v214, v214 op_sel_hi:[0,0,0]
	v_mfma_scale_f32_16x16x128_f8f6f4 v[154:157], v[114:121], v[154:161], v[50:53], v214, v214 op_sel_hi:[0,0,0]
	v_mfma_scale_f32_16x16x128_f8f6f4 v[158:161], v[106:113], v[170:177], v[46:49], v214, v214 op_sel_hi:[0,0,0]
	v_mfma_scale_f32_16x16x128_f8f6f4 v[170:173], v[114:121], v[170:177], v[42:45], v214, v214 op_sel_hi:[0,0,0]
	v_mfma_scale_f32_16x16x128_f8f6f4 v[174:177], v[106:113], v[178:185], v[38:41], v214, v214 op_sel_hi:[0,0,0]
	v_mfma_scale_f32_16x16x128_f8f6f4 v[178:181], v[114:121], v[178:185], v[34:37], v214, v214 op_sel_hi:[0,0,0]
	s_setprio 0
	s_mov_b32 m0, s39
	v_add_u32_e32 v182, s60, v205
	s_barrier
	s_nop 2
	ds_read_b128 v[34:37], v213 offset:16384
	ds_read_b128 v[38:41], v213 offset:17408
	ds_read_b128 v[42:45], v213 offset:18432
	ds_read_b128 v[46:49], v213 offset:19456
	ds_read_b128 v[50:53], v213 offset:20480
	ds_read_b128 v[54:57], v213 offset:21504
	ds_read_b128 v[58:61], v213 offset:22528
	ds_read_b128 v[62:65], v213 offset:23552
	global_load_lds_dwordx4 v182, s[4:5]
	v_add_u32_e32 v182, s60, v206
	s_mov_b32 m0, s40
	s_nop 0
	global_load_lds_dwordx4 v182, s[4:5]
	s_barrier
	s_waitcnt lgkmcnt(0)
	s_setprio 1

	v_mfma_scale_f32_16x16x128_f8f6f4 v[94:97], v[98:105], v[34:41], v[94:97], v214, v214 op_sel_hi:[0,0,0]
	v_mfma_scale_f32_16x16x128_f8f6f4 v[90:93], v[138:145], v[34:41], v[90:93], v214, v214 op_sel_hi:[0,0,0]
	v_mfma_scale_f32_16x16x128_f8f6f4 v[86:89], v[98:105], v[42:49], v[86:89], v214, v214 op_sel_hi:[0,0,0]
	v_mfma_scale_f32_16x16x128_f8f6f4 v[82:85], v[138:145], v[42:49], v[82:85], v214, v214 op_sel_hi:[0,0,0]
	v_mfma_scale_f32_16x16x128_f8f6f4 v[78:81], v[98:105], v[50:57], v[78:81], v214, v214 op_sel_hi:[0,0,0]
	v_mfma_scale_f32_16x16x128_f8f6f4 v[74:77], v[138:145], v[50:57], v[74:77], v214, v214 op_sel_hi:[0,0,0]
	v_mfma_scale_f32_16x16x128_f8f6f4 v[182:185], v[98:105], v[58:65], v[70:73], v214, v214 op_sel_hi:[0,0,0]
	v_mfma_scale_f32_16x16x128_f8f6f4 v[216:219], v[138:145], v[58:65], v[66:69], v214, v214 op_sel_hi:[0,0,0]
	s_setprio 0
	s_barrier
	s_add_i32 s61, s58, 0x40000
	s_add_i32 s62, s50, s38
	s_nop 2
	v_add_u32_e32 v66, s61, v1
	s_mov_b32 m0, s62
	s_nop 0
	global_load_lds_dwordx4 v66, s[6:7]
	v_add_u32_e32 v66, s61, v204
	s_add_i32 m0, s62, 0x2000
	s_nop 0
	global_load_lds_dwordx4 v66, s[6:7]
	s_waitcnt vmcnt(6)
	s_barrier
	s_setprio 1
	v_mfma_scale_f32_16x16x128_f8f6f4 v[220:223], v[106:113], v[34:41], v[30:33], v214, v214 op_sel_hi:[0,0,0]
	v_mfma_scale_f32_16x16x128_f8f6f4 v[224:227], v[114:121], v[34:41], v[26:29], v214, v214 op_sel_hi:[0,0,0]
	v_mfma_scale_f32_16x16x128_f8f6f4 v[228:231], v[106:113], v[42:49], v[22:25], v214, v214 op_sel_hi:[0,0,0]
	v_mfma_scale_f32_16x16x128_f8f6f4 v[232:235], v[114:121], v[42:49], v[18:21], v214, v214 op_sel_hi:[0,0,0]
	v_mfma_scale_f32_16x16x128_f8f6f4 v[236:239], v[106:113], v[50:57], v[14:17], v214, v214 op_sel_hi:[0,0,0]
	v_mfma_scale_f32_16x16x128_f8f6f4 v[240:243], v[114:121], v[50:57], v[10:13], v214, v214 op_sel_hi:[0,0,0]
	v_mfma_scale_f32_16x16x128_f8f6f4 v[244:247], v[106:113], v[58:65], v[6:9], v214, v214 op_sel_hi:[0,0,0]
	v_mfma_scale_f32_16x16x128_f8f6f4 v[248:251], v[114:121], v[58:65], v[2:5], v214, v214 op_sel_hi:[0,0,0]
	s_setprio 0
	s_add_i32 s61, 0, 0x18000
	s_nop 1
	v_add_u32_e32 v14, s61, v211
	s_barrier
	s_nop 0
	ds_read_b128 v[2:5], v14
	ds_read_b128 v[6:9], v14 offset:1024
	ds_read_b128 v[10:13], v14 offset:2048
	ds_read_b128 v[14:17], v14 offset:3072
	s_mov_b32 m0, s42
	v_add_u32_e32 v42, s60, v207
	ds_read_b128 v[18:21], v213 offset:32768
	ds_read_b128 v[22:25], v213 offset:33792
	ds_read_b128 v[26:29], v213 offset:34816
	ds_read_b128 v[30:33], v213 offset:35840
	ds_read_b128 v[34:37], v213 offset:36864
	ds_read_b128 v[38:41], v213 offset:37888
	ds_read_b128 v[66:69], v213 offset:38912
	ds_read_b128 v[70:73], v213 offset:39936
	global_load_lds_dwordx4 v42, s[4:5]
	v_add_u32_e32 v42, s60, v208
	s_mov_b32 m0, s43
	s_nop 0
	global_load_lds_dwordx4 v42, s[4:5]
	s_waitcnt lgkmcnt(8)
	s_barrier
	s_waitcnt lgkmcnt(0)
	s_setprio 1

	v_mfma_scale_f32_16x16x128_f8f6f4 v[134:137], v[2:9], v[18:25], v[134:137], v214, v214 op_sel_hi:[0,0,0]
	v_mfma_scale_f32_16x16x128_f8f6f4 v[130:133], v[10:17], v[18:25], v[130:133], v214, v214 op_sel_hi:[0,0,0]
	v_mfma_scale_f32_16x16x128_f8f6f4 v[126:129], v[2:9], v[26:33], v[126:129], v214, v214 op_sel_hi:[0,0,0]
	v_mfma_scale_f32_16x16x128_f8f6f4 v[122:125], v[10:17], v[26:33], v[122:125], v214, v214 op_sel_hi:[0,0,0]
	v_mfma_scale_f32_16x16x128_f8f6f4 v[118:121], v[2:9], v[34:41], v[162:165], v214, v214 op_sel_hi:[0,0,0]
	v_mfma_scale_f32_16x16x128_f8f6f4 v[114:117], v[10:17], v[34:41], v[186:189], v214, v214 op_sel_hi:[0,0,0]
	v_mfma_scale_f32_16x16x128_f8f6f4 v[110:113], v[2:9], v[66:73], v[190:193], v214, v214 op_sel_hi:[0,0,0]
	v_mfma_scale_f32_16x16x128_f8f6f4 v[106:109], v[10:17], v[66:73], v[194:197], v214, v214 op_sel_hi:[0,0,0]
	s_setprio 0
	s_barrier
	s_add_i32 s60, 0, 0x1c000
	v_add_u32_e32 v42, s60, v211
	s_or_b32 s62, s58, 0x80
	s_add_i32 s61, s61, s38
	ds_read_b128 v[98:101], v42
	ds_read_b128 v[102:105], v42 offset:1024
	ds_read_b128 v[138:141], v42 offset:2048
	ds_read_b128 v[142:145], v42 offset:3072
	v_add_u32_e32 v42, s62, v1
	s_mov_b32 m0, s61
	s_nop 0
	global_load_lds_dwordx4 v42, s[6:7]
	v_add_u32_e32 v42, s62, v204
	s_add_i32 m0, s61, 0x2000
	s_nop 0
	global_load_lds_dwordx4 v42, s[6:7]
	s_barrier
	s_waitcnt lgkmcnt(0)
	s_setprio 1

	v_mfma_scale_f32_16x16x128_f8f6f4 v[62:65], v[98:105], v[18:25], v[198:201], v214, v214 op_sel_hi:[0,0,0]
	v_mfma_scale_f32_16x16x128_f8f6f4 v[58:61], v[138:145], v[18:25], v[146:149], v214, v214 op_sel_hi:[0,0,0]
	v_mfma_scale_f32_16x16x128_f8f6f4 v[54:57], v[98:105], v[26:33], v[150:153], v214, v214 op_sel_hi:[0,0,0]
	v_mfma_scale_f32_16x16x128_f8f6f4 v[50:53], v[138:145], v[26:33], v[154:157], v214, v214 op_sel_hi:[0,0,0]
	v_mfma_scale_f32_16x16x128_f8f6f4 v[46:49], v[98:105], v[34:41], v[158:161], v214, v214 op_sel_hi:[0,0,0]
	v_mfma_scale_f32_16x16x128_f8f6f4 v[42:45], v[138:145], v[34:41], v[170:173], v214, v214 op_sel_hi:[0,0,0]
	v_mfma_scale_f32_16x16x128_f8f6f4 v[38:41], v[98:105], v[66:73], v[174:177], v214, v214 op_sel_hi:[0,0,0]
	v_mfma_scale_f32_16x16x128_f8f6f4 v[34:37], v[138:145], v[66:73], v[178:181], v214, v214 op_sel_hi:[0,0,0]
	s_setprio 0
	s_mov_b32 m0, s44
	v_add_u32_e32 v26, s59, v205
	s_barrier
	ds_read_b128 v[18:21], v213 offset:49152
	ds_read_b128 v[22:25], v213 offset:50176
	ds_read_b128 v[146:149], v213 offset:51200
	ds_read_b128 v[150:153], v213 offset:52224
	ds_read_b128 v[154:157], v213 offset:53248
	ds_read_b128 v[158:161], v213 offset:54272
	ds_read_b128 v[170:173], v213 offset:55296
	ds_read_b128 v[174:177], v213 offset:56320
	global_load_lds_dwordx4 v26, s[4:5]
	v_add_u32_e32 v26, s59, v206
	s_mov_b32 m0, s45
	s_nop 0
	global_load_lds_dwordx4 v26, s[4:5]
	s_barrier
	s_waitcnt lgkmcnt(0)
	s_setprio 1

	v_mfma_scale_f32_16x16x128_f8f6f4 v[94:97], v[2:9], v[18:25], v[94:97], v214, v214 op_sel_hi:[0,0,0]
	v_mfma_scale_f32_16x16x128_f8f6f4 v[90:93], v[10:17], v[18:25], v[90:93], v214, v214 op_sel_hi:[0,0,0]
	v_mfma_scale_f32_16x16x128_f8f6f4 v[86:89], v[2:9], v[146:153], v[86:89], v214, v214 op_sel_hi:[0,0,0]
	v_mfma_scale_f32_16x16x128_f8f6f4 v[82:85], v[10:17], v[146:153], v[82:85], v214, v214 op_sel_hi:[0,0,0]
	v_mfma_scale_f32_16x16x128_f8f6f4 v[78:81], v[2:9], v[154:161], v[78:81], v214, v214 op_sel_hi:[0,0,0]
	v_mfma_scale_f32_16x16x128_f8f6f4 v[74:77], v[10:17], v[154:161], v[74:77], v214, v214 op_sel_hi:[0,0,0]
	v_mfma_scale_f32_16x16x128_f8f6f4 v[70:73], v[2:9], v[170:177], v[182:185], v214, v214 op_sel_hi:[0,0,0]
	v_mfma_scale_f32_16x16x128_f8f6f4 v[66:69], v[10:17], v[170:177], v[216:219], v214, v214 op_sel_hi:[0,0,0]
	s_setprio 0
	s_barrier
	s_add_i32 s58, s58, 0x40080
	s_add_i32 s59, s60, s38
	v_add_u32_e32 v2, s58, v1
	s_mov_b32 m0, s59
	s_nop 0
	global_load_lds_dwordx4 v2, s[6:7]
	v_add_u32_e32 v2, s58, v204
	s_add_i32 m0, s59, 0x2000
	s_nop 0
	global_load_lds_dwordx4 v2, s[6:7]
	s_waitcnt vmcnt(6)
	s_barrier
	s_setprio 1
	v_mfma_scale_f32_16x16x128_f8f6f4 v[30:33], v[98:105], v[18:25], v[220:223], v214, v214 op_sel_hi:[0,0,0]
	v_mfma_scale_f32_16x16x128_f8f6f4 v[26:29], v[138:145], v[18:25], v[224:227], v214, v214 op_sel_hi:[0,0,0]
	v_mfma_scale_f32_16x16x128_f8f6f4 v[22:25], v[98:105], v[146:153], v[228:231], v214, v214 op_sel_hi:[0,0,0]
	v_mfma_scale_f32_16x16x128_f8f6f4 v[18:21], v[138:145], v[146:153], v[232:235], v214, v214 op_sel_hi:[0,0,0]
	v_mfma_scale_f32_16x16x128_f8f6f4 v[14:17], v[98:105], v[154:161], v[236:239], v214, v214 op_sel_hi:[0,0,0]
	v_mfma_scale_f32_16x16x128_f8f6f4 v[10:13], v[138:145], v[154:161], v[240:243], v214, v214 op_sel_hi:[0,0,0]
	v_mfma_scale_f32_16x16x128_f8f6f4 v[6:9], v[98:105], v[170:177], v[244:247], v214, v214 op_sel_hi:[0,0,0]
	v_mfma_scale_f32_16x16x128_f8f6f4 v[2:5], v[138:145], v[170:177], v[248:251], v214, v214 op_sel_hi:[0,0,0]
	s_setprio 0
	s_add_i32 s57, s57, 2
	s_addk_i32 s55, 0x100
	s_addk_i32 s56, 0x100
	s_cmp_ge_i32 s57, s46
	s_barrier
	s_cbranch_scc0 .LBB0_2505
	v_readlane_b32 s57, v254, 22
	s_branch .LBB0_2496
